# v73 + GEMM main loops without the per-segment s_setprio toggling (176 removed)
# baseline (speedup 1.0000x reference)
; #define PG8_STAGE(bufoff, gbase, voff) do { _Pragma("unroll") for (int _i = 0; _i < 2; ++_i) \
;         __builtin_amdgcn_global_load_lds((const unsigned*)(wsb + (size_t)(gbase) + (voff)[_i]), (LAS unsigned*)(lds + (bufoff) + ldsw + _i * 8192), 16, 0, 0); } while (0)
; #define PG8_LDA(dst, b, h) do { _Pragma("unroll") for (int m = 0; m < 4; ++m) { if constexpr (FP8) dst##8[m] = PG8_LD8(pa, PG8_SA(b, h) + m * 2048); \
;         else { _Pragma("unroll") for (int k = 0; k < 2; ++k) dst[m][k] = *(const LAS bf16x8*)(pa + PG8_SA(b, h) + m * 2048 + k * 1024); } } } while (0)
; #define PG8_LDB(dst, b, h) do { _Pragma("unroll") for (int n = 0; n < 2; ++n) { if constexpr (FP8) dst##8[n] = PG8_LD8(pb, PG8_SA(b, h) + n * 2048); \
;         else { _Pragma("unroll") for (int k = 0; k < 2; ++k) dst[n][k] = *(const LAS bf16x8*)(pb + PG8_SA(b, h) + n * 2048 + k * 1024); } } } while (0)
; #define PG8_WAIT_V(n) asm volatile("s_waitcnt vmcnt(" #n ")" ::: "memory")
; #define PG8_WAIT_L(n) asm volatile("s_waitcnt lgkmcnt(" #n ")" ::: "memory")
; #define PG8_BAR __builtin_amdgcn_s_barrier()
; #define PG8_SCHED __builtin_amdgcn_sched_barrier(0)
; template <class Epi, class Sched, bool PERM, bool FP8 = false, bool GATHER = false>
; DI void gemm_phase(LAS unsigned char* lds, const unsigned char* wsb, const unsigned lda, const unsigned ldb, const int nt, const Sched& S, const Epi& E) {
;     ...
;             PG8_LDB(B0, 0, 0); PG8_LDB(B1, 0, 1); PG8_SCHED; PG8_LDA(At, 0, 0); PG8_STAGEA(PG8_SA(1, 1), t + 1, 1, false);
;             if constexpr (GATHER) { if (last) {
;                 int tz = tid; asm volatile("" : "+v"(tz));
; #pragma unroll
;                 for (int i = 0; i < 2; ++i) { int R, C; stage_rc(tz * 16 + i * 8192, R, C);
; #pragma unroll
;                     for (int h = 0; h < 2; ++h) { const unsigned tk = (unsigned)tokt[h * HALF + R]; offC[h][i] = (tk < (unsigned)NTOK ? tk : (unsigned)(NTOK - 1)) * lda + (unsigned)C * 2u; } } } }
;             PG8_WAIT_V(8); PG8_WAIT_L(0); PG8_BAR; PG8_MMA(0, 0, At, B0); PG8_MMA(0, 1, At, B1); PG8_BAR; PG8_SCHED;
;             PG8_LDA(At, 0, 1); PG8_STAGE(PG8_SB(0, 0), b2, voffB); PG8_STAGE(PG8_SB(0, 1), b2 + hstepB, voffB); PG8_STAGEA(PG8_SA(0, 0), k2, 0, last);
;             PG8_WAIT_V(8); PG8_WAIT_L(0); PG8_BAR; PG8_MMA(1, 0, At, B0); PG8_MMA(1, 1, At, B1); PG8_BAR; PG8_SCHED;
.LBB0_405:
	ds_read_b128 v[130:133], v186
	ds_read_b128 v[134:137], v186 offset:1024
	ds_read_b128 v[138:141], v186 offset:2048
	ds_read_b128 v[142:145], v186 offset:3072
	ds_read_b128 v[146:149], v186 offset:16384
	ds_read_b128 v[150:153], v186 offset:17408
	ds_read_b128 v[160:163], v186 offset:18432
	ds_read_b128 v[164:167], v186 offset:19456
	s_add_i32 s41, s5, 0xfffe0080
	s_cmp_eq_u32 s7, 4
	s_cselect_b32 s40, s38, s4
	s_cselect_b32 s41, s37, s41
	s_add_i32 s52, s40, 0x80
	s_add_u32 s54, s10, s5
	s_addc_u32 s55, s11, 0
	s_mov_b32 m0, s29
	v_lshl_add_u64 v[206:207], s[54:55], 0, v[154:155]
	ds_read_b128 v[168:171], v185
	ds_read_b128 v[172:175], v185 offset:1024
	ds_read_b128 v[176:179], v185 offset:2048
	ds_read_b128 v[180:183], v185 offset:3072
	ds_read_b128 v[190:193], v185 offset:4096
	ds_read_b128 v[194:197], v185 offset:5120
	ds_read_b128 v[198:201], v185 offset:6144
	ds_read_b128 v[202:205], v185 offset:7168
	global_load_lds_dwordx4 v[206:207], off
	v_lshl_add_u64 v[206:207], s[54:55], 0, v[156:157]
	s_mov_b32 m0, s82
	s_nop 0
	global_load_lds_dwordx4 v[206:207], off
	s_waitcnt vmcnt(8)
	s_waitcnt lgkmcnt(0)
	s_barrier
	s_waitcnt lgkmcnt(0)
	v_mfma_f32_16x16x128_f8f6f4 v[126:129], v[130:137], v[168:175], v[126:129]
	v_mfma_f32_16x16x128_f8f6f4 v[122:125], v[138:145], v[168:175], v[122:125]
	v_mfma_f32_16x16x128_f8f6f4 v[110:113], v[130:137], v[176:183], v[110:113]
	v_mfma_f32_16x16x128_f8f6f4 v[106:109], v[138:145], v[176:183], v[106:109]
	v_mfma_f32_16x16x128_f8f6f4 v[206:209], v[130:137], v[190:197], v[94:97]
	v_mfma_f32_16x16x128_f8f6f4 v[210:213], v[138:145], v[190:197], v[90:93]
	v_mfma_f32_16x16x128_f8f6f4 v[214:217], v[130:137], v[198:205], v[78:81]
	v_mfma_f32_16x16x128_f8f6f4 v[218:221], v[138:145], v[198:205], v[74:77]
	v_mfma_f32_16x16x128_f8f6f4 v[118:121], v[146:153], v[168:175], v[118:121]
	v_mfma_f32_16x16x128_f8f6f4 v[114:117], v[160:167], v[168:175], v[114:117]
	v_mfma_f32_16x16x128_f8f6f4 v[102:105], v[146:153], v[176:183], v[102:105]
	v_mfma_f32_16x16x128_f8f6f4 v[98:101], v[160:167], v[176:183], v[98:101]
	v_mfma_f32_16x16x128_f8f6f4 v[168:171], v[146:153], v[190:197], v[86:89]
	v_mfma_f32_16x16x128_f8f6f4 v[172:175], v[160:167], v[190:197], v[82:85]
	v_mfma_f32_16x16x128_f8f6f4 v[176:179], v[146:153], v[198:205], v[70:73]
	v_mfma_f32_16x16x128_f8f6f4 v[180:183], v[160:167], v[198:205], v[66:69]
	s_barrier
	s_add_u32 s54, s10, s40
	s_addc_u32 s55, s11, 0
	s_mov_b32 m0, s58
	v_lshl_add_u64 v[190:191], s[54:55], 0, v[154:155]
	s_add_i32 s53, s40, 0x20000
	ds_read_b128 v[66:69], v185 offset:16384
	ds_read_b128 v[70:73], v185 offset:17408
	ds_read_b128 v[74:77], v185 offset:18432
	ds_read_b128 v[78:81], v185 offset:19456
	ds_read_b128 v[82:85], v185 offset:20480
	ds_read_b128 v[86:89], v185 offset:21504
	ds_read_b128 v[90:93], v185 offset:22528
	ds_read_b128 v[94:97], v185 offset:23552
	global_load_lds_dwordx4 v[190:191], off
	v_lshl_add_u64 v[190:191], s[54:55], 0, v[156:157]
	s_add_u32 s54, s10, s53
	s_mov_b32 m0, s59
	s_addc_u32 s55, s11, 0
	global_load_lds_dwordx4 v[190:191], off
	v_lshl_add_u64 v[190:191], s[54:55], 0, v[154:155]
	s_mov_b32 m0, s60
	s_nop 0
	global_load_lds_dwordx4 v[190:191], off
	v_lshl_add_u64 v[190:191], s[54:55], 0, v[156:157]
	s_add_u32 s54, s10, s41
	s_mov_b32 m0, s61
	s_addc_u32 s55, s11, 0
	global_load_lds_dwordx4 v[190:191], off
	v_lshl_add_u64 v[190:191], s[54:55], 0, v[154:155]
	s_mov_b32 m0, s57
	s_nop 0
	global_load_lds_dwordx4 v[190:191], off
	v_lshl_add_u64 v[190:191], s[54:55], 0, v[156:157]
	s_mov_b32 m0, s62
	s_nop 0
	global_load_lds_dwordx4 v[190:191], off
	s_waitcnt vmcnt(8)
	s_waitcnt lgkmcnt(0)
	s_barrier
	s_waitcnt lgkmcnt(0)
	v_mfma_f32_16x16x128_f8f6f4 v[62:65], v[130:137], v[66:73], v[62:65]
	v_mfma_f32_16x16x128_f8f6f4 v[58:61], v[138:145], v[66:73], v[58:61]
	v_mfma_f32_16x16x128_f8f6f4 v[190:193], v[130:137], v[74:81], v[46:49]
	v_mfma_f32_16x16x128_f8f6f4 v[194:197], v[138:145], v[74:81], v[42:45]
	v_mfma_f32_16x16x128_f8f6f4 v[198:201], v[130:137], v[82:89], v[30:33]
	v_mfma_f32_16x16x128_f8f6f4 v[202:205], v[138:145], v[82:89], v[26:29]
	v_mfma_f32_16x16x128_f8f6f4 v[222:225], v[130:137], v[90:97], v[14:17]
	v_mfma_f32_16x16x128_f8f6f4 v[226:229], v[138:145], v[90:97], v[10:13]
	v_mfma_f32_16x16x128_f8f6f4 v[54:57], v[146:153], v[66:73], v[54:57]
	v_mfma_f32_16x16x128_f8f6f4 v[50:53], v[160:167], v[66:73], v[50:53]
	v_mfma_f32_16x16x128_f8f6f4 v[230:233], v[146:153], v[74:81], v[38:41]
	v_mfma_f32_16x16x128_f8f6f4 v[234:237], v[160:167], v[74:81], v[34:37]
	v_mfma_f32_16x16x128_f8f6f4 v[238:241], v[146:153], v[82:89], v[22:25]
	v_mfma_f32_16x16x128_f8f6f4 v[242:245], v[160:167], v[82:89], v[18:21]
	v_mfma_f32_16x16x128_f8f6f4 v[246:249], v[146:153], v[90:97], v[6:9]
	v_mfma_f32_16x16x128_f8f6f4 v[250:253], v[160:167], v[90:97], v[2:5]
	s_barrier
; #define PG8_STAGE(bufoff, gbase, voff) do { _Pragma("unroll") for (int _i = 0; _i < 2; ++_i) \
;         __builtin_amdgcn_global_load_lds((const unsigned*)(wsb + (size_t)(gbase) + (voff)[_i]), (LAS unsigned*)(lds + (bufoff) + ldsw + _i * 8192), 16, 0, 0); } while (0)
; #define PG8_LDA(dst, b, h) do { _Pragma("unroll") for (int m = 0; m < 4; ++m) { if constexpr (FP8) dst##8[m] = PG8_LD8(pa, PG8_SA(b, h) + m * 2048); \
;         else { _Pragma("unroll") for (int k = 0; k < 2; ++k) dst[m][k] = *(const LAS bf16x8*)(pa + PG8_SA(b, h) + m * 2048 + k * 1024); } } } while (0)
; #define PG8_LDB(dst, b, h) do { _Pragma("unroll") for (int n = 0; n < 2; ++n) { if constexpr (FP8) dst##8[n] = PG8_LD8(pb, PG8_SA(b, h) + n * 2048); \
;         else { _Pragma("unroll") for (int k = 0; k < 2; ++k) dst[n][k] = *(const LAS bf16x8*)(pb + PG8_SA(b, h) + n * 2048 + k * 1024); } } } while (0)
; #define PG8_WAIT_V(n) asm volatile("s_waitcnt vmcnt(" #n ")" ::: "memory")
; #define PG8_WAIT_L(n) asm volatile("s_waitcnt lgkmcnt(" #n ")" ::: "memory")
; #define PG8_BAR __builtin_amdgcn_s_barrier()
; #define PG8_SCHED __builtin_amdgcn_sched_barrier(0)
; template <class Epi, class Sched, bool PERM, bool FP8 = false, bool GATHER = false>
; DI void gemm_phase(LAS unsigned char* lds, const unsigned char* wsb, const unsigned lda, const unsigned ldb, const int nt, const Sched& S, const Epi& E) {
;     ...
;             PG8_LDB(B0, 1, 0); PG8_LDB(B1, 1, 1); PG8_SCHED; PG8_LDA(At, 1, 0); PG8_STAGEA(PG8_SA(0, 1), k2, 1, last);
;             PG8_WAIT_V(8); PG8_WAIT_L(0); PG8_BAR; PG8_MMA(0, 0, At, B0); PG8_MMA(0, 1, At, B1); PG8_BAR; PG8_SCHED;
;             PG8_LDA(At, 1, 1); PG8_STAGE(PG8_SB(1, 0), b3, voffB); PG8_STAGE(PG8_SB(1, 1), b3 + hstepB, voffB); PG8_STAGEA(PG8_SA(1, 0), k3, 0, last);
;             PG8_WAIT_V(8); PG8_WAIT_L(0); PG8_BAR; PG8_MMA(1, 0, At, B0); PG8_MMA(1, 1, At, B1); PG8_BAR; PG8_SCHED;
;         }
;         if (wr == 0) PG8_BAR;
	s_nop 4
	ds_read_b128 v[2:5], v186 offset:32768
	ds_read_b128 v[6:9], v186 offset:33792
	ds_read_b128 v[18:21], v186 offset:34816
	ds_read_b128 v[22:25], v186 offset:35840
	ds_read_b128 v[130:133], v186 offset:49152
	ds_read_b128 v[134:137], v186 offset:50176
	ds_read_b128 v[138:141], v186 offset:51200
	ds_read_b128 v[142:145], v186 offset:52224
	s_add_i32 s53, s41, 0x20000
	s_add_u32 s54, s10, s53
	s_addc_u32 s55, s11, 0
	s_mov_b32 m0, s63
	v_lshl_add_u64 v[66:67], s[54:55], 0, v[154:155]
	ds_read_b128 v[10:13], v185 offset:32768
	ds_read_b128 v[14:17], v185 offset:33792
	ds_read_b128 v[26:29], v185 offset:34816
	ds_read_b128 v[30:33], v185 offset:35840
	ds_read_b128 v[34:37], v185 offset:36864
	ds_read_b128 v[38:41], v185 offset:37888
	ds_read_b128 v[42:45], v185 offset:38912
	ds_read_b128 v[46:49], v185 offset:39936
	global_load_lds_dwordx4 v[66:67], off
	v_lshl_add_u64 v[66:67], s[54:55], 0, v[156:157]
	s_mov_b32 m0, s64
	s_nop 0
	global_load_lds_dwordx4 v[66:67], off
	s_waitcnt vmcnt(8)
	s_waitcnt lgkmcnt(0)
	s_barrier
	s_waitcnt lgkmcnt(0)
	v_mfma_f32_16x16x128_f8f6f4 v[126:129], v[2:9], v[10:17], v[126:129]
	v_mfma_f32_16x16x128_f8f6f4 v[122:125], v[18:25], v[10:17], v[122:125]
	v_mfma_f32_16x16x128_f8f6f4 v[110:113], v[2:9], v[26:33], v[110:113]
	v_mfma_f32_16x16x128_f8f6f4 v[106:109], v[18:25], v[26:33], v[106:109]
	v_mfma_f32_16x16x128_f8f6f4 v[94:97], v[2:9], v[34:41], v[206:209]
	v_mfma_f32_16x16x128_f8f6f4 v[90:93], v[18:25], v[34:41], v[210:213]
	v_mfma_f32_16x16x128_f8f6f4 v[78:81], v[2:9], v[42:49], v[214:217]
	v_mfma_f32_16x16x128_f8f6f4 v[74:77], v[18:25], v[42:49], v[218:221]
	v_mfma_f32_16x16x128_f8f6f4 v[118:121], v[130:137], v[10:17], v[118:121]
	v_mfma_f32_16x16x128_f8f6f4 v[114:117], v[138:145], v[10:17], v[114:117]
	v_mfma_f32_16x16x128_f8f6f4 v[102:105], v[130:137], v[26:33], v[102:105]
	v_mfma_f32_16x16x128_f8f6f4 v[98:101], v[138:145], v[26:33], v[98:101]
	v_mfma_f32_16x16x128_f8f6f4 v[86:89], v[130:137], v[34:41], v[168:171]
	v_mfma_f32_16x16x128_f8f6f4 v[82:85], v[138:145], v[34:41], v[172:175]
	v_mfma_f32_16x16x128_f8f6f4 v[70:73], v[130:137], v[42:49], v[176:179]
	v_mfma_f32_16x16x128_f8f6f4 v[66:69], v[138:145], v[42:49], v[180:183]
	s_barrier
	s_add_u32 s52, s10, s52
	s_addc_u32 s53, s11, 0
	s_mov_b32 m0, s74
	v_lshl_add_u64 v[10:11], s[52:53], 0, v[154:155]
	s_add_i32 s40, s40, 0x20080
	ds_read_b128 v[34:37], v185 offset:49152
	ds_read_b128 v[38:41], v185 offset:50176
	ds_read_b128 v[146:149], v185 offset:51200
	ds_read_b128 v[150:153], v185 offset:52224
	ds_read_b128 v[160:163], v185 offset:53248
	ds_read_b128 v[164:167], v185 offset:54272
	ds_read_b128 v[168:171], v185 offset:55296
	ds_read_b128 v[172:175], v185 offset:56320
	global_load_lds_dwordx4 v[10:11], off
	v_lshl_add_u64 v[10:11], s[52:53], 0, v[156:157]
	s_add_u32 s52, s10, s40
	s_mov_b32 m0, s75
	s_addc_u32 s53, s11, 0
	s_addk_i32 s41, 0x80
	global_load_lds_dwordx4 v[10:11], off
	v_lshl_add_u64 v[10:11], s[52:53], 0, v[154:155]
	s_mov_b32 m0, s78
	s_add_u32 s40, s10, s41
	global_load_lds_dwordx4 v[10:11], off
	v_lshl_add_u64 v[10:11], s[52:53], 0, v[156:157]
	s_mov_b32 m0, s79
	s_addc_u32 s41, s11, 0
	global_load_lds_dwordx4 v[10:11], off
	v_lshl_add_u64 v[10:11], s[40:41], 0, v[154:155]
	s_mov_b32 m0, s76
	s_nop 0
	global_load_lds_dwordx4 v[10:11], off
	v_lshl_add_u64 v[10:11], s[40:41], 0, v[156:157]
	s_mov_b32 m0, s77
	s_nop 0
	global_load_lds_dwordx4 v[10:11], off
	s_waitcnt vmcnt(8)
	s_waitcnt lgkmcnt(0)
	s_barrier
	s_waitcnt lgkmcnt(0)
	v_mfma_f32_16x16x128_f8f6f4 v[62:65], v[2:9], v[34:41], v[62:65]
	v_mfma_f32_16x16x128_f8f6f4 v[58:61], v[18:25], v[34:41], v[58:61]
	v_mfma_f32_16x16x128_f8f6f4 v[46:49], v[2:9], v[146:153], v[190:193]
	v_mfma_f32_16x16x128_f8f6f4 v[42:45], v[18:25], v[146:153], v[194:197]
	v_mfma_f32_16x16x128_f8f6f4 v[30:33], v[2:9], v[160:167], v[198:201]
	v_mfma_f32_16x16x128_f8f6f4 v[26:29], v[18:25], v[160:167], v[202:205]
	v_mfma_f32_16x16x128_f8f6f4 v[14:17], v[2:9], v[168:175], v[222:225]
	v_mfma_f32_16x16x128_f8f6f4 v[10:13], v[18:25], v[168:175], v[226:229]
	v_mfma_f32_16x16x128_f8f6f4 v[54:57], v[130:137], v[34:41], v[54:57]
	v_mfma_f32_16x16x128_f8f6f4 v[50:53], v[138:145], v[34:41], v[50:53]
	v_mfma_f32_16x16x128_f8f6f4 v[38:41], v[130:137], v[146:153], v[230:233]
	v_mfma_f32_16x16x128_f8f6f4 v[34:37], v[138:145], v[146:153], v[234:237]
	v_mfma_f32_16x16x128_f8f6f4 v[22:25], v[130:137], v[160:167], v[238:241]
	v_mfma_f32_16x16x128_f8f6f4 v[18:21], v[138:145], v[160:167], v[242:245]
	v_mfma_f32_16x16x128_f8f6f4 v[6:9], v[130:137], v[168:175], v[246:249]
	v_mfma_f32_16x16x128_f8f6f4 v[2:5], v[138:145], v[168:175], v[250:253]
	s_barrier
	s_add_i32 s7, s7, 2
	s_addk_i32 s5, 0x100
	s_addk_i32 s4, 0x100
	s_cmp_gt_u32 s7, 5
	s_cbranch_scc0 .LBB0_405
	s_and_b64 vcc, exec, s[14:15]
	s_cbranch_vccz .LBB0_408
	s_barrier

; #define PG8_STAGE(bufoff, gbase, voff) do { _Pragma("unroll") for (int _i = 0; _i < 2; ++_i) \
;         __builtin_amdgcn_global_load_lds((const unsigned*)(wsb + (size_t)(gbase) + (voff)[_i]), (LAS unsigned*)(lds + (bufoff) + ldsw + _i * 8192), 16, 0, 0); } while (0)
; #define PG8_LDA(dst, b, h) do { _Pragma("unroll") for (int m = 0; m < 4; ++m) { if constexpr (FP8) dst##8[m] = PG8_LD8(pa, PG8_SA(b, h) + m * 2048); \
;         else { _Pragma("unroll") for (int k = 0; k < 2; ++k) dst[m][k] = *(const LAS bf16x8*)(pa + PG8_SA(b, h) + m * 2048 + k * 1024); } } } while (0)
; #define PG8_LDB(dst, b, h) do { _Pragma("unroll") for (int n = 0; n < 2; ++n) { if constexpr (FP8) dst##8[n] = PG8_LD8(pb, PG8_SA(b, h) + n * 2048); \
;         else { _Pragma("unroll") for (int k = 0; k < 2; ++k) dst[n][k] = *(const LAS bf16x8*)(pb + PG8_SA(b, h) + n * 2048 + k * 1024); } } } while (0)
; #define PG8_WAIT_V(n) asm volatile("s_waitcnt vmcnt(" #n ")" ::: "memory")
; #define PG8_WAIT_L(n) asm volatile("s_waitcnt lgkmcnt(" #n ")" ::: "memory")
; #define PG8_BAR __builtin_amdgcn_s_barrier()
; #define PG8_SCHED __builtin_amdgcn_sched_barrier(0)
; template <class Epi, class Sched, bool PERM, bool FP8 = false, bool GATHER = false>
; DI void gemm_phase(LAS unsigned char* lds, const unsigned char* wsb, const unsigned lda, const unsigned ldb, const int nt, const Sched& S, const Epi& E) {
;     ...
;             PG8_LDB(B0, 0, 0); PG8_LDB(B1, 0, 1); PG8_SCHED; PG8_LDA(At, 0, 0); PG8_STAGEA(PG8_SA(1, 1), t + 1, 1, false);
;             if constexpr (GATHER) { if (last) {
;                 int tz = tid; asm volatile("" : "+v"(tz));
; #pragma unroll
;                 for (int i = 0; i < 2; ++i) { int R, C; stage_rc(tz * 16 + i * 8192, R, C);
; #pragma unroll
;                     for (int h = 0; h < 2; ++h) { const unsigned tk = (unsigned)tokt[h * HALF + R]; offC[h][i] = (tk < (unsigned)NTOK ? tk : (unsigned)(NTOK - 1)) * lda + (unsigned)C * 2u; } } } }
;             PG8_WAIT_V(8); PG8_WAIT_L(0); PG8_BAR; PG8_MMA(0, 0, At, B0); PG8_MMA(0, 1, At, B1); PG8_BAR; PG8_SCHED;
;             PG8_LDA(At, 0, 1); PG8_STAGE(PG8_SB(0, 0), b2, voffB); PG8_STAGE(PG8_SB(0, 1), b2 + hstepB, voffB); PG8_STAGEA(PG8_SA(0, 0), k2, 0, last);
;             PG8_WAIT_V(8); PG8_WAIT_L(0); PG8_BAR; PG8_MMA(1, 0, At, B0); PG8_MMA(1, 1, At, B1); PG8_BAR; PG8_SCHED;
.LBB0_573:
	ds_read_b128 v[144:147], v142
	ds_read_b128 v[148:151], v142 offset:1024
	ds_read_b128 v[152:155], v142 offset:2048
	ds_read_b128 v[156:159], v142 offset:3072
	ds_read_b128 v[160:163], v142 offset:16384
	ds_read_b128 v[164:167], v142 offset:17408
	ds_read_b128 v[168:171], v142 offset:18432
	ds_read_b128 v[172:175], v142 offset:19456
	s_add_i32 s23, s19, 0xfffe0080
	s_cmp_eq_u32 s20, 4
	s_cselect_b32 s22, s66, s18
	s_cselect_b32 s23, s65, s23
	s_add_i32 s24, s22, 0x80
	s_add_u32 s26, s4, s19
	s_addc_u32 s27, s5, 0
	s_mov_b32 m0, s59
	v_lshl_add_u64 v[130:131], s[26:27], 0, v[136:137]
	ds_read_b128 v[176:179], v141
	ds_read_b128 v[180:183], v141 offset:1024
	ds_read_b128 v[184:187], v141 offset:2048
	ds_read_b128 v[188:191], v141 offset:3072
	ds_read_b128 v[192:195], v141 offset:4096
	ds_read_b128 v[196:199], v141 offset:5120
	ds_read_b128 v[200:203], v141 offset:6144
	ds_read_b128 v[204:207], v141 offset:7168
	global_load_lds_dwordx4 v[130:131], off
	v_lshl_add_u64 v[130:131], s[26:27], 0, v[138:139]
	s_mov_b32 m0, s60
	s_nop 0
	global_load_lds_dwordx4 v[130:131], off
	s_waitcnt vmcnt(8)
	s_waitcnt lgkmcnt(0)
	s_barrier
	s_waitcnt lgkmcnt(0)
	v_mfma_f32_16x16x128_f8f6f4 v[126:129], v[144:151], v[176:183], v[126:129]
	v_mfma_f32_16x16x128_f8f6f4 v[122:125], v[152:159], v[176:183], v[122:125]
	v_mfma_f32_16x16x128_f8f6f4 v[114:117], v[144:151], v[184:191], v[114:117]
	v_mfma_f32_16x16x128_f8f6f4 v[106:109], v[152:159], v[184:191], v[106:109]
	v_mfma_f32_16x16x128_f8f6f4 v[98:101], v[144:151], v[192:199], v[98:101]
	v_mfma_f32_16x16x128_f8f6f4 v[208:211], v[152:159], v[192:199], v[90:93]
	v_mfma_f32_16x16x128_f8f6f4 v[212:215], v[144:151], v[200:207], v[82:85]
	v_mfma_f32_16x16x128_f8f6f4 v[216:219], v[152:159], v[200:207], v[74:77]
	v_mfma_f32_16x16x128_f8f6f4 v[118:121], v[160:167], v[176:183], v[118:121]
	v_mfma_f32_16x16x128_f8f6f4 v[110:113], v[168:175], v[176:183], v[110:113]
	v_mfma_f32_16x16x128_f8f6f4 v[102:105], v[160:167], v[184:191], v[102:105]
	v_mfma_f32_16x16x128_f8f6f4 v[176:179], v[168:175], v[184:191], v[94:97]
	v_mfma_f32_16x16x128_f8f6f4 v[180:183], v[160:167], v[192:199], v[86:89]
	v_mfma_f32_16x16x128_f8f6f4 v[184:187], v[168:175], v[192:199], v[78:81]
	v_mfma_f32_16x16x128_f8f6f4 v[188:191], v[160:167], v[200:207], v[70:73]
	v_mfma_f32_16x16x128_f8f6f4 v[192:195], v[168:175], v[200:207], v[66:69]
	s_barrier
	s_add_u32 s26, s4, s22
	s_addc_u32 s27, s5, 0
	s_mov_b32 m0, s38
	v_lshl_add_u64 v[130:131], s[26:27], 0, v[134:135]
	s_add_i32 s25, s22, 0x20000
	ds_read_b128 v[66:69], v141 offset:16384
	ds_read_b128 v[70:73], v141 offset:17408
	ds_read_b128 v[74:77], v141 offset:18432
	ds_read_b128 v[78:81], v141 offset:19456
	ds_read_b128 v[82:85], v141 offset:20480
	ds_read_b128 v[86:89], v141 offset:21504
	ds_read_b128 v[90:93], v141 offset:22528
	ds_read_b128 v[94:97], v141 offset:23552
	global_load_lds_dwordx4 v[130:131], off
	v_lshl_add_u64 v[130:131], s[26:27], 0, v[252:253]
	s_add_u32 s26, s4, s25
	s_mov_b32 m0, s39
	s_addc_u32 s27, s5, 0
	global_load_lds_dwordx4 v[130:131], off
	v_lshl_add_u64 v[130:131], s[26:27], 0, v[134:135]
	s_mov_b32 m0, s40
	s_nop 0
	global_load_lds_dwordx4 v[130:131], off
	v_lshl_add_u64 v[130:131], s[26:27], 0, v[252:253]
	s_add_u32 s26, s4, s23
	s_mov_b32 m0, s41
	s_addc_u32 s27, s5, 0
	global_load_lds_dwordx4 v[130:131], off
	v_lshl_add_u64 v[130:131], s[26:27], 0, v[136:137]
	s_mov_b32 m0, s29
	s_nop 0
	global_load_lds_dwordx4 v[130:131], off
	v_lshl_add_u64 v[130:131], s[26:27], 0, v[138:139]
	s_mov_b32 m0, s42
	s_nop 0
	global_load_lds_dwordx4 v[130:131], off
	s_waitcnt vmcnt(8)
	s_waitcnt lgkmcnt(0)
	s_barrier
	s_waitcnt lgkmcnt(0)
	v_mfma_f32_16x16x128_f8f6f4 v[62:65], v[144:151], v[66:73], v[62:65]
	v_mfma_f32_16x16x128_f8f6f4 v[58:61], v[152:159], v[66:73], v[58:61]
	v_mfma_f32_16x16x128_f8f6f4 v[50:53], v[144:151], v[74:81], v[50:53]
	v_mfma_f32_16x16x128_f8f6f4 v[196:199], v[152:159], v[74:81], v[42:45]
	v_mfma_f32_16x16x128_f8f6f4 v[200:203], v[144:151], v[82:89], v[34:37]
	v_mfma_f32_16x16x128_f8f6f4 v[204:207], v[152:159], v[82:89], v[26:29]
	v_mfma_f32_16x16x128_f8f6f4 v[220:223], v[144:151], v[90:97], v[18:21]
	v_mfma_f32_16x16x128_f8f6f4 v[224:227], v[152:159], v[90:97], v[10:13]
	v_mfma_f32_16x16x128_f8f6f4 v[54:57], v[160:167], v[66:73], v[54:57]
	v_mfma_f32_16x16x128_f8f6f4 v[228:231], v[168:175], v[66:73], v[46:49]
	v_mfma_f32_16x16x128_f8f6f4 v[232:235], v[160:167], v[74:81], v[38:41]
	v_mfma_f32_16x16x128_f8f6f4 v[236:239], v[168:175], v[74:81], v[30:33]
	v_mfma_f32_16x16x128_f8f6f4 v[240:243], v[160:167], v[82:89], v[22:25]
	v_mfma_f32_16x16x128_f8f6f4 v[244:247], v[168:175], v[82:89], v[14:17]
	v_mfma_f32_16x16x128_f8f6f4 v[248:251], v[160:167], v[90:97], v[6:9]
	v_mfma_f32_16x16x128_f8f6f4 v[130:133], v[168:175], v[90:97], v[2:5]
	s_barrier
; #define PG8_STAGE(bufoff, gbase, voff) do { _Pragma("unroll") for (int _i = 0; _i < 2; ++_i) \
;         __builtin_amdgcn_global_load_lds((const unsigned*)(wsb + (size_t)(gbase) + (voff)[_i]), (LAS unsigned*)(lds + (bufoff) + ldsw + _i * 8192), 16, 0, 0); } while (0)
; #define PG8_LDA(dst, b, h) do { _Pragma("unroll") for (int m = 0; m < 4; ++m) { if constexpr (FP8) dst##8[m] = PG8_LD8(pa, PG8_SA(b, h) + m * 2048); \
;         else { _Pragma("unroll") for (int k = 0; k < 2; ++k) dst[m][k] = *(const LAS bf16x8*)(pa + PG8_SA(b, h) + m * 2048 + k * 1024); } } } while (0)
; #define PG8_LDB(dst, b, h) do { _Pragma("unroll") for (int n = 0; n < 2; ++n) { if constexpr (FP8) dst##8[n] = PG8_LD8(pb, PG8_SA(b, h) + n * 2048); \
;         else { _Pragma("unroll") for (int k = 0; k < 2; ++k) dst[n][k] = *(const LAS bf16x8*)(pb + PG8_SA(b, h) + n * 2048 + k * 1024); } } } while (0)
; #define PG8_WAIT_V(n) asm volatile("s_waitcnt vmcnt(" #n ")" ::: "memory")
; #define PG8_WAIT_L(n) asm volatile("s_waitcnt lgkmcnt(" #n ")" ::: "memory")
; #define PG8_BAR __builtin_amdgcn_s_barrier()
; #define PG8_SCHED __builtin_amdgcn_sched_barrier(0)
; template <class Epi, class Sched, bool PERM, bool FP8 = false, bool GATHER = false>
; DI void gemm_phase(LAS unsigned char* lds, const unsigned char* wsb, const unsigned lda, const unsigned ldb, const int nt, const Sched& S, const Epi& E) {
;     ...
;             PG8_LDB(B0, 1, 0); PG8_LDB(B1, 1, 1); PG8_SCHED; PG8_LDA(At, 1, 0); PG8_STAGEA(PG8_SA(0, 1), k2, 1, last);
;             PG8_WAIT_V(8); PG8_WAIT_L(0); PG8_BAR; PG8_MMA(0, 0, At, B0); PG8_MMA(0, 1, At, B1); PG8_BAR; PG8_SCHED;
;             PG8_LDA(At, 1, 1); PG8_STAGE(PG8_SB(1, 0), b3, voffB); PG8_STAGE(PG8_SB(1, 1), b3 + hstepB, voffB); PG8_STAGEA(PG8_SA(1, 0), k3, 0, last);
;             PG8_WAIT_V(8); PG8_WAIT_L(0); PG8_BAR; PG8_MMA(1, 0, At, B0); PG8_MMA(1, 1, At, B1); PG8_BAR; PG8_SCHED;
;         }
;         if (wr == 0) PG8_BAR;
	s_nop 4
	ds_read_b128 v[2:5], v142 offset:32768
	ds_read_b128 v[6:9], v142 offset:33792
	ds_read_b128 v[10:13], v142 offset:34816
	ds_read_b128 v[14:17], v142 offset:35840
	ds_read_b128 v[144:147], v142 offset:49152
	ds_read_b128 v[148:151], v142 offset:50176
	ds_read_b128 v[152:155], v142 offset:51200
	ds_read_b128 v[156:159], v142 offset:52224
	s_add_i32 s25, s23, 0x20000
	s_add_u32 s26, s4, s25
	s_addc_u32 s27, s5, 0
	s_mov_b32 m0, s43
	v_lshl_add_u64 v[66:67], s[26:27], 0, v[136:137]
	ds_read_b128 v[18:21], v141 offset:32768
	ds_read_b128 v[22:25], v141 offset:33792
	ds_read_b128 v[26:29], v141 offset:34816
	ds_read_b128 v[30:33], v141 offset:35840
	ds_read_b128 v[34:37], v141 offset:36864
	ds_read_b128 v[38:41], v141 offset:37888
	ds_read_b128 v[42:45], v141 offset:38912
	ds_read_b128 v[46:49], v141 offset:39936
	global_load_lds_dwordx4 v[66:67], off
	v_lshl_add_u64 v[66:67], s[26:27], 0, v[138:139]
	s_mov_b32 m0, s44
	s_nop 0
	global_load_lds_dwordx4 v[66:67], off
	s_waitcnt vmcnt(8)
	s_waitcnt lgkmcnt(0)
	s_barrier
	s_waitcnt lgkmcnt(0)
	v_mfma_f32_16x16x128_f8f6f4 v[126:129], v[2:9], v[18:25], v[126:129]
	v_mfma_f32_16x16x128_f8f6f4 v[122:125], v[10:17], v[18:25], v[122:125]
	v_mfma_f32_16x16x128_f8f6f4 v[114:117], v[2:9], v[26:33], v[114:117]
	v_mfma_f32_16x16x128_f8f6f4 v[106:109], v[10:17], v[26:33], v[106:109]
	v_mfma_f32_16x16x128_f8f6f4 v[98:101], v[2:9], v[34:41], v[98:101]
	v_mfma_f32_16x16x128_f8f6f4 v[90:93], v[10:17], v[34:41], v[208:211]
	v_mfma_f32_16x16x128_f8f6f4 v[82:85], v[2:9], v[42:49], v[212:215]
	v_mfma_f32_16x16x128_f8f6f4 v[74:77], v[10:17], v[42:49], v[216:219]
	v_mfma_f32_16x16x128_f8f6f4 v[118:121], v[144:151], v[18:25], v[118:121]
	v_mfma_f32_16x16x128_f8f6f4 v[110:113], v[152:159], v[18:25], v[110:113]
	v_mfma_f32_16x16x128_f8f6f4 v[102:105], v[144:151], v[26:33], v[102:105]
	v_mfma_f32_16x16x128_f8f6f4 v[94:97], v[152:159], v[26:33], v[176:179]
	v_mfma_f32_16x16x128_f8f6f4 v[86:89], v[144:151], v[34:41], v[180:183]
	v_mfma_f32_16x16x128_f8f6f4 v[78:81], v[152:159], v[34:41], v[184:187]
	v_mfma_f32_16x16x128_f8f6f4 v[70:73], v[144:151], v[42:49], v[188:191]
	v_mfma_f32_16x16x128_f8f6f4 v[66:69], v[152:159], v[42:49], v[192:195]
	s_barrier
	s_add_u32 s24, s4, s24
	s_addc_u32 s25, s5, 0
	s_mov_b32 m0, s46
	v_lshl_add_u64 v[18:19], s[24:25], 0, v[134:135]
	s_add_i32 s22, s22, 0x20080
	ds_read_b128 v[160:163], v141 offset:49152
	ds_read_b128 v[164:167], v141 offset:50176
	ds_read_b128 v[168:171], v141 offset:51200
	ds_read_b128 v[172:175], v141 offset:52224
	ds_read_b128 v[176:179], v141 offset:53248
	ds_read_b128 v[180:183], v141 offset:54272
	ds_read_b128 v[184:187], v141 offset:55296
	ds_read_b128 v[188:191], v141 offset:56320
	global_load_lds_dwordx4 v[18:19], off
	v_lshl_add_u64 v[18:19], s[24:25], 0, v[252:253]
	s_add_u32 s24, s4, s22
	s_mov_b32 m0, s47
	s_addc_u32 s25, s5, 0
	s_addk_i32 s23, 0x80
	global_load_lds_dwordx4 v[18:19], off
	v_lshl_add_u64 v[18:19], s[24:25], 0, v[134:135]
	s_mov_b32 m0, s50
	s_add_u32 s22, s4, s23
	global_load_lds_dwordx4 v[18:19], off
	v_lshl_add_u64 v[18:19], s[24:25], 0, v[252:253]
	s_mov_b32 m0, s51
	s_addc_u32 s23, s5, 0
	global_load_lds_dwordx4 v[18:19], off
	v_lshl_add_u64 v[18:19], s[22:23], 0, v[136:137]
	s_mov_b32 m0, s48
	s_nop 0
	global_load_lds_dwordx4 v[18:19], off
	v_lshl_add_u64 v[18:19], s[22:23], 0, v[138:139]
	s_mov_b32 m0, s49
	s_nop 0
	global_load_lds_dwordx4 v[18:19], off
	s_waitcnt vmcnt(8)
	s_waitcnt lgkmcnt(0)
	s_barrier
	s_waitcnt lgkmcnt(0)
	v_mfma_f32_16x16x128_f8f6f4 v[62:65], v[2:9], v[160:167], v[62:65]
	v_mfma_f32_16x16x128_f8f6f4 v[58:61], v[10:17], v[160:167], v[58:61]
	v_mfma_f32_16x16x128_f8f6f4 v[50:53], v[2:9], v[168:175], v[50:53]
	v_mfma_f32_16x16x128_f8f6f4 v[42:45], v[10:17], v[168:175], v[196:199]
	v_mfma_f32_16x16x128_f8f6f4 v[34:37], v[2:9], v[176:183], v[200:203]
	v_mfma_f32_16x16x128_f8f6f4 v[26:29], v[10:17], v[176:183], v[204:207]
	v_mfma_f32_16x16x128_f8f6f4 v[18:21], v[2:9], v[184:191], v[220:223]
	v_mfma_f32_16x16x128_f8f6f4 v[10:13], v[10:17], v[184:191], v[224:227]
	v_mfma_f32_16x16x128_f8f6f4 v[54:57], v[144:151], v[160:167], v[54:57]
	v_mfma_f32_16x16x128_f8f6f4 v[46:49], v[152:159], v[160:167], v[228:231]
	v_mfma_f32_16x16x128_f8f6f4 v[38:41], v[144:151], v[168:175], v[232:235]
	v_mfma_f32_16x16x128_f8f6f4 v[30:33], v[152:159], v[168:175], v[236:239]
	v_mfma_f32_16x16x128_f8f6f4 v[22:25], v[144:151], v[176:183], v[240:243]
	v_mfma_f32_16x16x128_f8f6f4 v[14:17], v[152:159], v[176:183], v[244:247]
	v_mfma_f32_16x16x128_f8f6f4 v[6:9], v[144:151], v[184:191], v[248:251]
	v_mfma_f32_16x16x128_f8f6f4 v[2:5], v[152:159], v[184:191], v[130:133]
	s_barrier
	s_add_i32 s20, s20, 2
	s_addk_i32 s19, 0x100
	s_addk_i32 s18, 0x100
	s_cmp_gt_u32 s20, 5
	s_cbranch_scc0 .LBB0_573
	s_and_b64 vcc, exec, s[12:13]
	s_cbranch_vccz .LBB0_576
	s_barrier

; #define PG8_STAGE(bufoff, gbase, voff) do { _Pragma("unroll") for (int _i = 0; _i < 2; ++_i) \
;         __builtin_amdgcn_global_load_lds((const unsigned*)(wsb + (size_t)(gbase) + (voff)[_i]), (LAS unsigned*)(lds + (bufoff) + ldsw + _i * 8192), 16, 0, 0); } while (0)
; #define PG8_LDA(dst, b, h) do { _Pragma("unroll") for (int m = 0; m < 4; ++m) { if constexpr (FP8) dst##8[m] = PG8_LD8(pa, PG8_SA(b, h) + m * 2048); \
;         else { _Pragma("unroll") for (int k = 0; k < 2; ++k) dst[m][k] = *(const LAS bf16x8*)(pa + PG8_SA(b, h) + m * 2048 + k * 1024); } } } while (0)
; #define PG8_LDB(dst, b, h) do { _Pragma("unroll") for (int n = 0; n < 2; ++n) { if constexpr (FP8) dst##8[n] = PG8_LD8(pb, PG8_SA(b, h) + n * 2048); \
;         else { _Pragma("unroll") for (int k = 0; k < 2; ++k) dst[n][k] = *(const LAS bf16x8*)(pb + PG8_SA(b, h) + n * 2048 + k * 1024); } } } while (0)
; #define PG8_WAIT_V(n) asm volatile("s_waitcnt vmcnt(" #n ")" ::: "memory")
; #define PG8_WAIT_L(n) asm volatile("s_waitcnt lgkmcnt(" #n ")" ::: "memory")
; #define PG8_BAR __builtin_amdgcn_s_barrier()
; #define PG8_SCHED __builtin_amdgcn_sched_barrier(0)
; template <class Epi, class Sched, bool PERM, bool FP8 = false, bool GATHER = false>
; DI void gemm_phase(LAS unsigned char* lds, const unsigned char* wsb, const unsigned lda, const unsigned ldb, const int nt, const Sched& S, const Epi& E) {
;     ...
;             PG8_LDB(B0, 0, 0); PG8_LDB(B1, 0, 1); PG8_SCHED; PG8_LDA(At, 0, 0); PG8_STAGEA(PG8_SA(1, 1), t + 1, 1, false);
;             if constexpr (GATHER) { if (last) {
;                 int tz = tid; asm volatile("" : "+v"(tz));
; #pragma unroll
;                 for (int i = 0; i < 2; ++i) { int R, C; stage_rc(tz * 16 + i * 8192, R, C);
; #pragma unroll
;                     for (int h = 0; h < 2; ++h) { const unsigned tk = (unsigned)tokt[h * HALF + R]; offC[h][i] = (tk < (unsigned)NTOK ? tk : (unsigned)(NTOK - 1)) * lda + (unsigned)C * 2u; } } } }
;             PG8_WAIT_V(8); PG8_WAIT_L(0); PG8_BAR; PG8_MMA(0, 0, At, B0); PG8_MMA(0, 1, At, B1); PG8_BAR; PG8_SCHED;
;             PG8_LDA(At, 0, 1); PG8_STAGE(PG8_SB(0, 0), b2, voffB); PG8_STAGE(PG8_SB(0, 1), b2 + hstepB, voffB); PG8_STAGEA(PG8_SA(0, 0), k2, 0, last);
;             PG8_WAIT_V(8); PG8_WAIT_L(0); PG8_BAR; PG8_MMA(1, 0, At, B0); PG8_MMA(1, 1, At, B1); PG8_BAR; PG8_SCHED;
.LBB0_725:
	ds_read_b128 v[150:153], v147
	ds_read_b128 v[154:157], v147 offset:1024
	ds_read_b128 v[158:161], v147 offset:2048
	ds_read_b128 v[162:165], v147 offset:3072
	ds_read_b128 v[166:169], v147 offset:16384
	ds_read_b128 v[170:173], v147 offset:17408
	ds_read_b128 v[174:177], v147 offset:18432
	ds_read_b128 v[178:181], v147 offset:19456
	s_add_i32 s85, s83, s42
	s_add_u32 s54, s42, 0x100
	s_addc_u32 s55, s43, 0
	s_cmp_eq_u32 s84, 4
	s_cselect_b32 s85, s82, s85
	s_mov_b32 m0, s68
	v_lshl_add_u64 v[142:143], v[140:141], 0, s[42:43]
	ds_read_b128 v[182:185], v146
	ds_read_b128 v[186:189], v146 offset:1024
	ds_read_b128 v[190:193], v146 offset:2048
	ds_read_b128 v[194:197], v146 offset:3072
	ds_read_b128 v[198:201], v146 offset:4096
	ds_read_b128 v[202:205], v146 offset:5120
	ds_read_b128 v[212:215], v146 offset:6144
	ds_read_b128 v[216:219], v146 offset:7168
	global_load_lds_dwordx4 v[142:143], off
	v_lshl_add_u64 v[142:143], v[138:139], 0, s[42:43]
	s_mov_b32 m0, s69
	s_cselect_b32 s43, 0, s54
	global_load_lds_dwordx4 v[142:143], off
	s_waitcnt vmcnt(8)
	s_waitcnt lgkmcnt(0)
	s_add_i32 s42, s85, 0x80
	s_barrier
	s_waitcnt lgkmcnt(0)
	v_mfma_f32_16x16x32_bf16 v[126:129], v[150:153], v[182:185], v[126:129]
	v_mfma_f32_16x16x32_bf16 v[122:125], v[158:161], v[182:185], v[122:125]
	v_mfma_f32_16x16x32_bf16 v[110:113], v[150:153], v[190:193], v[110:113]
	v_mfma_f32_16x16x32_bf16 v[106:109], v[158:161], v[190:193], v[106:109]
	v_mfma_f32_16x16x32_bf16 v[94:97], v[150:153], v[198:201], v[94:97]
	v_mfma_f32_16x16x32_bf16 v[90:93], v[158:161], v[198:201], v[90:93]
	v_mfma_f32_16x16x32_bf16 v[78:81], v[150:153], v[212:215], v[78:81]
	v_mfma_f32_16x16x32_bf16 v[74:77], v[158:161], v[212:215], v[74:77]
	v_mfma_f32_16x16x32_bf16 v[126:129], v[154:157], v[186:189], v[126:129]
	v_mfma_f32_16x16x32_bf16 v[122:125], v[162:165], v[186:189], v[122:125]
	v_mfma_f32_16x16x32_bf16 v[110:113], v[154:157], v[194:197], v[110:113]
	v_mfma_f32_16x16x32_bf16 v[106:109], v[162:165], v[194:197], v[106:109]
	v_mfma_f32_16x16x32_bf16 v[94:97], v[154:157], v[202:205], v[94:97]
	v_mfma_f32_16x16x32_bf16 v[90:93], v[162:165], v[202:205], v[90:93]
	v_mfma_f32_16x16x32_bf16 v[78:81], v[154:157], v[216:219], v[78:81]
	v_mfma_f32_16x16x32_bf16 v[74:77], v[162:165], v[216:219], v[74:77]
	v_mfma_f32_16x16x32_bf16 v[118:121], v[166:169], v[182:185], v[118:121]
	v_mfma_f32_16x16x32_bf16 v[114:117], v[174:177], v[182:185], v[114:117]
	v_mfma_f32_16x16x32_bf16 v[102:105], v[166:169], v[190:193], v[102:105]
	v_mfma_f32_16x16x32_bf16 v[98:101], v[174:177], v[190:193], v[98:101]
	v_mfma_f32_16x16x32_bf16 v[86:89], v[166:169], v[198:201], v[86:89]
	v_mfma_f32_16x16x32_bf16 v[82:85], v[174:177], v[198:201], v[82:85]
	v_mfma_f32_16x16x32_bf16 v[70:73], v[166:169], v[212:215], v[70:73]
	v_mfma_f32_16x16x32_bf16 v[66:69], v[174:177], v[212:215], v[66:69]
	v_mfma_f32_16x16x32_bf16 v[118:121], v[170:173], v[186:189], v[118:121]
	v_mfma_f32_16x16x32_bf16 v[114:117], v[178:181], v[186:189], v[114:117]
	v_mfma_f32_16x16x32_bf16 v[102:105], v[170:173], v[194:197], v[102:105]
	v_mfma_f32_16x16x32_bf16 v[98:101], v[178:181], v[194:197], v[98:101]
	v_mfma_f32_16x16x32_bf16 v[86:89], v[170:173], v[202:205], v[86:89]
	v_mfma_f32_16x16x32_bf16 v[82:85], v[178:181], v[202:205], v[82:85]
	v_mfma_f32_16x16x32_bf16 v[70:73], v[170:173], v[216:219], v[70:73]
	v_mfma_f32_16x16x32_bf16 v[66:69], v[178:181], v[216:219], v[66:69]
	s_barrier
	s_add_u32 s86, s6, s85
	s_addc_u32 s87, s7, 0
	s_mov_b32 m0, s47
	v_lshl_add_u64 v[142:143], s[86:87], 0, v[134:135]
	ds_read_b128 v[182:185], v146 offset:16384
	ds_read_b128 v[186:189], v146 offset:17408
	ds_read_b128 v[190:193], v146 offset:18432
	ds_read_b128 v[194:197], v146 offset:19456
	ds_read_b128 v[198:201], v146 offset:20480
	ds_read_b128 v[202:205], v146 offset:21504
	ds_read_b128 v[212:215], v146 offset:22528
	ds_read_b128 v[216:219], v146 offset:23552
	global_load_lds_dwordx4 v[142:143], off
	v_lshl_add_u64 v[142:143], s[86:87], 0, v[130:131]
	s_add_i32 s86, s85, 0x20000
	s_add_u32 s86, s6, s86
	s_addc_u32 s87, s7, 0
	s_mov_b32 m0, s48
	s_add_u32 s88, s6, s43
	global_load_lds_dwordx4 v[142:143], off
	v_lshl_add_u64 v[142:143], s[86:87], 0, v[134:135]
	s_mov_b32 m0, s49
	s_addc_u32 s89, s7, 0
	global_load_lds_dwordx4 v[142:143], off
	v_lshl_add_u64 v[142:143], s[86:87], 0, v[130:131]
	s_add_u32 s86, s88, 0x1d094000
	s_mov_b32 m0, s56
	s_addc_u32 s87, s89, 0
	global_load_lds_dwordx4 v[142:143], off
	v_lshl_add_u64 v[142:143], s[86:87], 0, v[136:137]
	s_mov_b32 m0, s46
	s_nop 0
	global_load_lds_dwordx4 v[142:143], off
	v_lshl_add_u64 v[142:143], s[86:87], 0, v[132:133]
	s_mov_b32 m0, s57
	s_nop 0
	global_load_lds_dwordx4 v[142:143], off
	s_waitcnt vmcnt(8)
	s_waitcnt lgkmcnt(0)
	s_barrier
; #define PG8_STAGE(bufoff, gbase, voff) do { _Pragma("unroll") for (int _i = 0; _i < 2; ++_i) \
;         __builtin_amdgcn_global_load_lds((const unsigned*)(wsb + (size_t)(gbase) + (voff)[_i]), (LAS unsigned*)(lds + (bufoff) + ldsw + _i * 8192), 16, 0, 0); } while (0)
; #define PG8_LDA(dst, b, h) do { _Pragma("unroll") for (int m = 0; m < 4; ++m) { if constexpr (FP8) dst##8[m] = PG8_LD8(pa, PG8_SA(b, h) + m * 2048); \
;         else { _Pragma("unroll") for (int k = 0; k < 2; ++k) dst[m][k] = *(const LAS bf16x8*)(pa + PG8_SA(b, h) + m * 2048 + k * 1024); } } } while (0)
; #define PG8_WAIT_V(n) asm volatile("s_waitcnt vmcnt(" #n ")" ::: "memory")
; template <class Epi, class Sched, bool PERM, bool FP8 = false, bool GATHER = false>
; DI void gemm_phase(LAS unsigned char* lds, const unsigned char* wsb, const unsigned lda, const unsigned ldb, const int nt, const Sched& S, const Epi& E) {
;     ...
;             PG8_LDB(B0, 0, 0); PG8_LDB(B1, 0, 1); PG8_SCHED; PG8_LDA(At, 0, 0); PG8_STAGEA(PG8_SA(1, 1), t + 1, 1, false);
;             if constexpr (GATHER) { if (last) {
;                 int tz = tid; asm volatile("" : "+v"(tz));
; #pragma unroll
;                 for (int i = 0; i < 2; ++i) { int R, C; stage_rc(tz * 16 + i * 8192, R, C);
; #pragma unroll
;                     for (int h = 0; h < 2; ++h) { const unsigned tk = (unsigned)tokt[h * HALF + R]; offC[h][i] = (tk < (unsigned)NTOK ? tk : (unsigned)(NTOK - 1)) * lda + (unsigned)C * 2u; } } } }
;             PG8_WAIT_V(8); PG8_WAIT_L(0); PG8_BAR; PG8_MMA(0, 0, At, B0); PG8_MMA(0, 1, At, B1); PG8_BAR; PG8_SCHED;
;             PG8_LDA(At, 0, 1); PG8_STAGE(PG8_SB(0, 0), b2, voffB); PG8_STAGE(PG8_SB(0, 1), b2 + hstepB, voffB); PG8_STAGEA(PG8_SA(0, 0), k2, 0, last);
;             PG8_WAIT_V(8); PG8_WAIT_L(0); PG8_BAR; PG8_MMA(1, 0, At, B0); PG8_MMA(1, 1, At, B1); PG8_BAR; PG8_SCHED;
;             PG8_LDB(B0, 1, 0); PG8_LDB(B1, 1, 1); PG8_SCHED; PG8_LDA(At, 1, 0); PG8_STAGEA(PG8_SA(0, 1), k2, 1, last);
;             PG8_WAIT_V(8); PG8_WAIT_L(0); PG8_BAR; PG8_MMA(0, 0, At, B0); PG8_MMA(0, 1, At, B1); PG8_BAR; PG8_SCHED;
;             PG8_LDA(At, 1, 1); PG8_STAGE(PG8_SB(1, 0), b3, voffB); PG8_STAGE(PG8_SB(1, 1), b3 + hstepB, voffB); PG8_STAGEA(PG8_SA(1, 0), k3, 0, last);
;             PG8_WAIT_V(8); PG8_WAIT_L(0); PG8_BAR; PG8_MMA(1, 0, At, B0); PG8_MMA(1, 1, At, B1); PG8_BAR; PG8_SCHED;
	s_waitcnt lgkmcnt(0)
	v_mfma_f32_16x16x32_bf16 v[62:65], v[150:153], v[182:185], v[62:65]
	v_mfma_f32_16x16x32_bf16 v[58:61], v[158:161], v[182:185], v[58:61]
	v_mfma_f32_16x16x32_bf16 v[46:49], v[150:153], v[190:193], v[46:49]
	v_mfma_f32_16x16x32_bf16 v[42:45], v[158:161], v[190:193], v[42:45]
	v_mfma_f32_16x16x32_bf16 v[30:33], v[150:153], v[198:201], v[30:33]
	v_mfma_f32_16x16x32_bf16 v[26:29], v[158:161], v[198:201], v[26:29]
	v_mfma_f32_16x16x32_bf16 v[14:17], v[150:153], v[212:215], v[14:17]
	v_mfma_f32_16x16x32_bf16 v[10:13], v[158:161], v[212:215], v[10:13]
	v_mfma_f32_16x16x32_bf16 v[62:65], v[154:157], v[186:189], v[62:65]
	v_mfma_f32_16x16x32_bf16 v[58:61], v[162:165], v[186:189], v[58:61]
	v_mfma_f32_16x16x32_bf16 v[46:49], v[154:157], v[194:197], v[46:49]
	v_mfma_f32_16x16x32_bf16 v[42:45], v[162:165], v[194:197], v[42:45]
	v_mfma_f32_16x16x32_bf16 v[30:33], v[154:157], v[202:205], v[30:33]
	v_mfma_f32_16x16x32_bf16 v[26:29], v[162:165], v[202:205], v[26:29]
	v_mfma_f32_16x16x32_bf16 v[14:17], v[154:157], v[216:219], v[14:17]
	v_mfma_f32_16x16x32_bf16 v[10:13], v[162:165], v[216:219], v[10:13]
	v_mfma_f32_16x16x32_bf16 v[54:57], v[166:169], v[182:185], v[54:57]
	v_mfma_f32_16x16x32_bf16 v[50:53], v[174:177], v[182:185], v[50:53]
	v_mfma_f32_16x16x32_bf16 v[38:41], v[166:169], v[190:193], v[38:41]
	v_mfma_f32_16x16x32_bf16 v[34:37], v[174:177], v[190:193], v[34:37]
	v_mfma_f32_16x16x32_bf16 v[22:25], v[166:169], v[198:201], v[22:25]
	v_mfma_f32_16x16x32_bf16 v[18:21], v[174:177], v[198:201], v[18:21]
	v_mfma_f32_16x16x32_bf16 v[6:9], v[166:169], v[212:215], v[6:9]
	v_mfma_f32_16x16x32_bf16 v[2:5], v[174:177], v[212:215], v[2:5]
	v_mfma_f32_16x16x32_bf16 v[54:57], v[170:173], v[186:189], v[54:57]
	v_mfma_f32_16x16x32_bf16 v[50:53], v[178:181], v[186:189], v[50:53]
	v_mfma_f32_16x16x32_bf16 v[38:41], v[170:173], v[194:197], v[38:41]
	v_mfma_f32_16x16x32_bf16 v[34:37], v[178:181], v[194:197], v[34:37]
	v_mfma_f32_16x16x32_bf16 v[22:25], v[170:173], v[202:205], v[22:25]
	v_mfma_f32_16x16x32_bf16 v[18:21], v[178:181], v[202:205], v[18:21]
	v_mfma_f32_16x16x32_bf16 v[6:9], v[170:173], v[216:219], v[6:9]
	v_mfma_f32_16x16x32_bf16 v[2:5], v[178:181], v[216:219], v[2:5]
	s_barrier
	ds_read_b128 v[150:153], v147 offset:32768
	ds_read_b128 v[154:157], v147 offset:33792
	ds_read_b128 v[158:161], v147 offset:34816
	ds_read_b128 v[162:165], v147 offset:35840
	ds_read_b128 v[166:169], v147 offset:49152
	ds_read_b128 v[170:173], v147 offset:50176
	ds_read_b128 v[174:177], v147 offset:51200
	ds_read_b128 v[178:181], v147 offset:52224
	s_add_u32 s86, s88, 0x1d0b4000
	s_addc_u32 s87, s89, 0
	s_mov_b32 m0, s58
	v_lshl_add_u64 v[142:143], s[86:87], 0, v[136:137]
	ds_read_b128 v[182:185], v146 offset:32768
	ds_read_b128 v[186:189], v146 offset:33792
	ds_read_b128 v[190:193], v146 offset:34816
	ds_read_b128 v[194:197], v146 offset:35840
	ds_read_b128 v[198:201], v146 offset:36864
	ds_read_b128 v[202:205], v146 offset:37888
	ds_read_b128 v[212:215], v146 offset:38912
	ds_read_b128 v[216:219], v146 offset:39936
	global_load_lds_dwordx4 v[142:143], off
	v_lshl_add_u64 v[142:143], s[86:87], 0, v[132:133]
	s_mov_b32 m0, s59
	s_nop 0
	global_load_lds_dwordx4 v[142:143], off
	s_waitcnt vmcnt(8)
	s_waitcnt lgkmcnt(0)
	s_barrier
	s_waitcnt lgkmcnt(0)
	v_mfma_f32_16x16x32_bf16 v[126:129], v[150:153], v[182:185], v[126:129]
	v_mfma_f32_16x16x32_bf16 v[122:125], v[158:161], v[182:185], v[122:125]
	v_mfma_f32_16x16x32_bf16 v[110:113], v[150:153], v[190:193], v[110:113]
	v_mfma_f32_16x16x32_bf16 v[106:109], v[158:161], v[190:193], v[106:109]
	v_mfma_f32_16x16x32_bf16 v[94:97], v[150:153], v[198:201], v[94:97]
	v_mfma_f32_16x16x32_bf16 v[90:93], v[158:161], v[198:201], v[90:93]
	v_mfma_f32_16x16x32_bf16 v[78:81], v[150:153], v[212:215], v[78:81]
	v_mfma_f32_16x16x32_bf16 v[74:77], v[158:161], v[212:215], v[74:77]
	v_mfma_f32_16x16x32_bf16 v[126:129], v[154:157], v[186:189], v[126:129]
	v_mfma_f32_16x16x32_bf16 v[122:125], v[162:165], v[186:189], v[122:125]
	v_mfma_f32_16x16x32_bf16 v[110:113], v[154:157], v[194:197], v[110:113]
	v_mfma_f32_16x16x32_bf16 v[106:109], v[162:165], v[194:197], v[106:109]
	v_mfma_f32_16x16x32_bf16 v[94:97], v[154:157], v[202:205], v[94:97]
	v_mfma_f32_16x16x32_bf16 v[90:93], v[162:165], v[202:205], v[90:93]
	v_mfma_f32_16x16x32_bf16 v[78:81], v[154:157], v[216:219], v[78:81]
	v_mfma_f32_16x16x32_bf16 v[74:77], v[162:165], v[216:219], v[74:77]
	v_mfma_f32_16x16x32_bf16 v[118:121], v[166:169], v[182:185], v[118:121]
	v_mfma_f32_16x16x32_bf16 v[114:117], v[174:177], v[182:185], v[114:117]
	v_mfma_f32_16x16x32_bf16 v[102:105], v[166:169], v[190:193], v[102:105]
	v_mfma_f32_16x16x32_bf16 v[98:101], v[174:177], v[190:193], v[98:101]
	v_mfma_f32_16x16x32_bf16 v[86:89], v[166:169], v[198:201], v[86:89]
	v_mfma_f32_16x16x32_bf16 v[82:85], v[174:177], v[198:201], v[82:85]
	v_mfma_f32_16x16x32_bf16 v[70:73], v[166:169], v[212:215], v[70:73]
	v_mfma_f32_16x16x32_bf16 v[66:69], v[174:177], v[212:215], v[66:69]
	v_mfma_f32_16x16x32_bf16 v[118:121], v[170:173], v[186:189], v[118:121]
	v_mfma_f32_16x16x32_bf16 v[114:117], v[178:181], v[186:189], v[114:117]
	v_mfma_f32_16x16x32_bf16 v[102:105], v[170:173], v[194:197], v[102:105]
	v_mfma_f32_16x16x32_bf16 v[98:101], v[178:181], v[194:197], v[98:101]
	v_mfma_f32_16x16x32_bf16 v[86:89], v[170:173], v[202:205], v[86:89]
	v_mfma_f32_16x16x32_bf16 v[82:85], v[178:181], v[202:205], v[82:85]
	v_mfma_f32_16x16x32_bf16 v[70:73], v[170:173], v[216:219], v[70:73]
	v_mfma_f32_16x16x32_bf16 v[66:69], v[178:181], v[216:219], v[66:69]
	s_barrier
; #define PG8_STAGE(bufoff, gbase, voff) do { _Pragma("unroll") for (int _i = 0; _i < 2; ++_i) \
;         __builtin_amdgcn_global_load_lds((const unsigned*)(wsb + (size_t)(gbase) + (voff)[_i]), (LAS unsigned*)(lds + (bufoff) + ldsw + _i * 8192), 16, 0, 0); } while (0)
; #define PG8_LDA(dst, b, h) do { _Pragma("unroll") for (int m = 0; m < 4; ++m) { if constexpr (FP8) dst##8[m] = PG8_LD8(pa, PG8_SA(b, h) + m * 2048); \
;         else { _Pragma("unroll") for (int k = 0; k < 2; ++k) dst[m][k] = *(const LAS bf16x8*)(pa + PG8_SA(b, h) + m * 2048 + k * 1024); } } } while (0)
; #define PG8_LDB(dst, b, h) do { _Pragma("unroll") for (int n = 0; n < 2; ++n) { if constexpr (FP8) dst##8[n] = PG8_LD8(pb, PG8_SA(b, h) + n * 2048); \
;         else { _Pragma("unroll") for (int k = 0; k < 2; ++k) dst[n][k] = *(const LAS bf16x8*)(pb + PG8_SA(b, h) + n * 2048 + k * 1024); } } } while (0)
; #define PG8_WAIT_V(n) asm volatile("s_waitcnt vmcnt(" #n ")" ::: "memory")
; #define PG8_WAIT_L(n) asm volatile("s_waitcnt lgkmcnt(" #n ")" ::: "memory")
; #define PG8_BAR __builtin_amdgcn_s_barrier()
; #define PG8_SCHED __builtin_amdgcn_sched_barrier(0)
; template <class Epi, class Sched, bool PERM, bool FP8 = false, bool GATHER = false>
; DI void gemm_phase(LAS unsigned char* lds, const unsigned char* wsb, const unsigned lda, const unsigned ldb, const int nt, const Sched& S, const Epi& E) {
;     ...
;             PG8_LDB(B0, 1, 0); PG8_LDB(B1, 1, 1); PG8_SCHED; PG8_LDA(At, 1, 0); PG8_STAGEA(PG8_SA(0, 1), k2, 1, last);
;             PG8_WAIT_V(8); PG8_WAIT_L(0); PG8_BAR; PG8_MMA(0, 0, At, B0); PG8_MMA(0, 1, At, B1); PG8_BAR; PG8_SCHED;
;             PG8_LDA(At, 1, 1); PG8_STAGE(PG8_SB(1, 0), b3, voffB); PG8_STAGE(PG8_SB(1, 1), b3 + hstepB, voffB); PG8_STAGEA(PG8_SA(1, 0), k3, 0, last);
;             PG8_WAIT_V(8); PG8_WAIT_L(0); PG8_BAR; PG8_MMA(1, 0, At, B0); PG8_MMA(1, 1, At, B1); PG8_BAR; PG8_SCHED;
;         }
;         if (wr == 0) PG8_BAR;
	s_add_u32 s42, s6, s42
	s_addc_u32 s43, s7, 0
	s_mov_b32 m0, s60
	v_lshl_add_u64 v[142:143], s[42:43], 0, v[134:135]
	s_add_i32 s85, s85, 0x20080
	ds_read_b128 v[182:185], v146 offset:49152
	ds_read_b128 v[186:189], v146 offset:50176
	ds_read_b128 v[190:193], v146 offset:51200
	ds_read_b128 v[194:197], v146 offset:52224
	ds_read_b128 v[198:201], v146 offset:53248
	ds_read_b128 v[202:205], v146 offset:54272
	ds_read_b128 v[212:215], v146 offset:55296
	ds_read_b128 v[216:219], v146 offset:56320
	global_load_lds_dwordx4 v[142:143], off
	v_lshl_add_u64 v[142:143], s[42:43], 0, v[130:131]
	s_add_u32 s42, s6, s85
	s_mov_b32 m0, s61
	s_addc_u32 s43, s7, 0
	global_load_lds_dwordx4 v[142:143], off
	v_lshl_add_u64 v[142:143], s[42:43], 0, v[134:135]
	s_mov_b32 m0, s65
	s_nop 0
	global_load_lds_dwordx4 v[142:143], off
	v_lshl_add_u64 v[142:143], s[42:43], 0, v[130:131]
	s_add_u32 s42, s88, 0x1d094080
	s_mov_b32 m0, s66
	s_addc_u32 s43, s89, 0
	global_load_lds_dwordx4 v[142:143], off
	v_lshl_add_u64 v[142:143], s[42:43], 0, v[136:137]
	s_mov_b32 m0, s62
	s_nop 0
	global_load_lds_dwordx4 v[142:143], off
	v_lshl_add_u64 v[142:143], s[42:43], 0, v[132:133]
	s_mov_b32 m0, s63
	s_nop 0
	global_load_lds_dwordx4 v[142:143], off
	s_waitcnt vmcnt(8)
	s_waitcnt lgkmcnt(0)
	s_barrier
	s_waitcnt lgkmcnt(0)
	v_mfma_f32_16x16x32_bf16 v[62:65], v[150:153], v[182:185], v[62:65]
	v_mfma_f32_16x16x32_bf16 v[58:61], v[158:161], v[182:185], v[58:61]
	v_mfma_f32_16x16x32_bf16 v[46:49], v[150:153], v[190:193], v[46:49]
	v_mfma_f32_16x16x32_bf16 v[42:45], v[158:161], v[190:193], v[42:45]
	v_mfma_f32_16x16x32_bf16 v[30:33], v[150:153], v[198:201], v[30:33]
	v_mfma_f32_16x16x32_bf16 v[26:29], v[158:161], v[198:201], v[26:29]
	v_mfma_f32_16x16x32_bf16 v[14:17], v[150:153], v[212:215], v[14:17]
	v_mfma_f32_16x16x32_bf16 v[10:13], v[158:161], v[212:215], v[10:13]
	v_mfma_f32_16x16x32_bf16 v[62:65], v[154:157], v[186:189], v[62:65]
	v_mfma_f32_16x16x32_bf16 v[58:61], v[162:165], v[186:189], v[58:61]
	v_mfma_f32_16x16x32_bf16 v[46:49], v[154:157], v[194:197], v[46:49]
	v_mfma_f32_16x16x32_bf16 v[42:45], v[162:165], v[194:197], v[42:45]
	v_mfma_f32_16x16x32_bf16 v[30:33], v[154:157], v[202:205], v[30:33]
	v_mfma_f32_16x16x32_bf16 v[26:29], v[162:165], v[202:205], v[26:29]
	v_mfma_f32_16x16x32_bf16 v[14:17], v[154:157], v[216:219], v[14:17]
	v_mfma_f32_16x16x32_bf16 v[10:13], v[162:165], v[216:219], v[10:13]
	v_mfma_f32_16x16x32_bf16 v[54:57], v[166:169], v[182:185], v[54:57]
	v_mfma_f32_16x16x32_bf16 v[50:53], v[174:177], v[182:185], v[50:53]
	v_mfma_f32_16x16x32_bf16 v[38:41], v[166:169], v[190:193], v[38:41]
	v_mfma_f32_16x16x32_bf16 v[34:37], v[174:177], v[190:193], v[34:37]
	v_mfma_f32_16x16x32_bf16 v[22:25], v[166:169], v[198:201], v[22:25]
	v_mfma_f32_16x16x32_bf16 v[18:21], v[174:177], v[198:201], v[18:21]
	v_mfma_f32_16x16x32_bf16 v[6:9], v[166:169], v[212:215], v[6:9]
	v_mfma_f32_16x16x32_bf16 v[2:5], v[174:177], v[212:215], v[2:5]
	v_mfma_f32_16x16x32_bf16 v[54:57], v[170:173], v[186:189], v[54:57]
	v_mfma_f32_16x16x32_bf16 v[50:53], v[178:181], v[186:189], v[50:53]
	v_mfma_f32_16x16x32_bf16 v[38:41], v[170:173], v[194:197], v[38:41]
	v_mfma_f32_16x16x32_bf16 v[34:37], v[178:181], v[194:197], v[34:37]
	v_mfma_f32_16x16x32_bf16 v[22:25], v[170:173], v[202:205], v[22:25]
	v_mfma_f32_16x16x32_bf16 v[18:21], v[178:181], v[202:205], v[18:21]
	v_mfma_f32_16x16x32_bf16 v[6:9], v[170:173], v[216:219], v[6:9]
	v_mfma_f32_16x16x32_bf16 v[2:5], v[178:181], v[216:219], v[2:5]
	s_barrier
	s_add_i32 s84, s84, 2
	s_cmp_gt_u32 s84, 5
	s_mov_b64 s[42:43], s[54:55]
	s_cbranch_scc0 .LBB0_725
	s_and_b64 vcc, exec, s[10:11]
	s_cbranch_vccz .LBB0_728
	s_barrier

; #define PG8_STAGE(bufoff, gbase, voff) do { _Pragma("unroll") for (int _i = 0; _i < 2; ++_i) \
;         __builtin_amdgcn_global_load_lds((const unsigned*)(wsb + (size_t)(gbase) + (voff)[_i]), (LAS unsigned*)(lds + (bufoff) + ldsw + _i * 8192), 16, 0, 0); } while (0)
; #define PG8_LDA(dst, b, h) do { _Pragma("unroll") for (int m = 0; m < 4; ++m) { if constexpr (FP8) dst##8[m] = PG8_LD8(pa, PG8_SA(b, h) + m * 2048); \
;         else { _Pragma("unroll") for (int k = 0; k < 2; ++k) dst[m][k] = *(const LAS bf16x8*)(pa + PG8_SA(b, h) + m * 2048 + k * 1024); } } } while (0)
; #define PG8_LDB(dst, b, h) do { _Pragma("unroll") for (int n = 0; n < 2; ++n) { if constexpr (FP8) dst##8[n] = PG8_LD8(pb, PG8_SA(b, h) + n * 2048); \
;         else { _Pragma("unroll") for (int k = 0; k < 2; ++k) dst[n][k] = *(const LAS bf16x8*)(pb + PG8_SA(b, h) + n * 2048 + k * 1024); } } } while (0)
; #define PG8_WAIT_V(n) asm volatile("s_waitcnt vmcnt(" #n ")" ::: "memory")
; #define PG8_WAIT_L(n) asm volatile("s_waitcnt lgkmcnt(" #n ")" ::: "memory")
; #define PG8_BAR __builtin_amdgcn_s_barrier()
; #define PG8_SCHED __builtin_amdgcn_sched_barrier(0)
; template <class Epi, class Sched, bool PERM, bool FP8 = false, bool GATHER = false>
; DI void gemm_phase(LAS unsigned char* lds, const unsigned char* wsb, const unsigned lda, const unsigned ldb, const int nt, const Sched& S, const Epi& E) {
;     ...
;             PG8_LDB(B0, 0, 0); PG8_LDB(B1, 0, 1); PG8_SCHED; PG8_LDA(At, 0, 0); PG8_STAGEA(PG8_SA(1, 1), t + 1, 1, false);
;             if constexpr (GATHER) { if (last) {
;                 int tz = tid; asm volatile("" : "+v"(tz));
; #pragma unroll
;                 for (int i = 0; i < 2; ++i) { int R, C; stage_rc(tz * 16 + i * 8192, R, C);
; #pragma unroll
;                     for (int h = 0; h < 2; ++h) { const unsigned tk = (unsigned)tokt[h * HALF + R]; offC[h][i] = (tk < (unsigned)NTOK ? tk : (unsigned)(NTOK - 1)) * lda + (unsigned)C * 2u; } } } }
;             PG8_WAIT_V(8); PG8_WAIT_L(0); PG8_BAR; PG8_MMA(0, 0, At, B0); PG8_MMA(0, 1, At, B1); PG8_BAR; PG8_SCHED;
;             PG8_LDA(At, 0, 1); PG8_STAGE(PG8_SB(0, 0), b2, voffB); PG8_STAGE(PG8_SB(0, 1), b2 + hstepB, voffB); PG8_STAGEA(PG8_SA(0, 0), k2, 0, last);
;             PG8_WAIT_V(8); PG8_WAIT_L(0); PG8_BAR; PG8_MMA(1, 0, At, B0); PG8_MMA(1, 1, At, B1); PG8_BAR; PG8_SCHED;
.LBB0_910:
	ds_read_b128 v[130:133], v162
	ds_read_b128 v[134:137], v162 offset:1024
	ds_read_b128 v[138:141], v162 offset:2048
	ds_read_b128 v[142:145], v162 offset:3072
	ds_read_b128 v[150:153], v162 offset:16384
	ds_read_b128 v[154:157], v162 offset:17408
	ds_read_b128 v[164:167], v162 offset:18432
	ds_read_b128 v[168:171], v162 offset:19456
	s_add_i32 s25, s21, 0xfffe0080
	s_cmp_eq_u32 s23, 4
	s_cselect_b32 s24, s59, s22
	s_cselect_b32 s25, s58, s25
	s_add_i32 s61, s24, 0x80
	s_add_u32 s62, s6, s21
	s_addc_u32 s63, s7, 0
	s_mov_b32 m0, s54
	v_lshl_add_u64 v[158:159], s[62:63], 0, v[148:149]
	ds_read_b128 v[172:175], v161
	ds_read_b128 v[176:179], v161 offset:1024
	ds_read_b128 v[180:183], v161 offset:2048
	ds_read_b128 v[184:187], v161 offset:3072
	ds_read_b128 v[188:191], v161 offset:4096
	ds_read_b128 v[192:195], v161 offset:5120
	ds_read_b128 v[196:199], v161 offset:6144
	ds_read_b128 v[200:203], v161 offset:7168
	global_load_lds_dwordx4 v[158:159], off
	v_lshl_add_u64 v[158:159], s[62:63], 0, v[146:147]
	s_mov_b32 m0, s55
	s_nop 0
	global_load_lds_dwordx4 v[158:159], off
	s_waitcnt vmcnt(8)
	s_waitcnt lgkmcnt(0)
	s_barrier
	s_waitcnt lgkmcnt(0)
	v_mfma_f32_16x16x128_f8f6f4 v[126:129], v[130:137], v[172:179], v[126:129]
	v_mfma_f32_16x16x128_f8f6f4 v[122:125], v[138:145], v[172:179], v[122:125]
	v_mfma_f32_16x16x128_f8f6f4 v[118:121], v[130:137], v[180:187], v[118:121]
	v_mfma_f32_16x16x128_f8f6f4 v[114:117], v[138:145], v[180:187], v[114:117]
	v_mfma_f32_16x16x128_f8f6f4 v[102:105], v[130:137], v[188:195], v[102:105]
	v_mfma_f32_16x16x128_f8f6f4 v[98:101], v[138:145], v[188:195], v[98:101]
	v_mfma_f32_16x16x128_f8f6f4 v[204:207], v[130:137], v[196:203], v[86:89]
	v_mfma_f32_16x16x128_f8f6f4 v[208:211], v[138:145], v[196:203], v[78:81]
	v_mfma_f32_16x16x128_f8f6f4 v[110:113], v[150:157], v[172:179], v[110:113]
	v_mfma_f32_16x16x128_f8f6f4 v[106:109], v[164:171], v[172:179], v[106:109]
	v_mfma_f32_16x16x128_f8f6f4 v[172:175], v[150:157], v[180:187], v[94:97]
	v_mfma_f32_16x16x128_f8f6f4 v[176:179], v[164:171], v[180:187], v[90:93]
	v_mfma_f32_16x16x128_f8f6f4 v[180:183], v[150:157], v[188:195], v[82:85]
	v_mfma_f32_16x16x128_f8f6f4 v[184:187], v[164:171], v[188:195], v[74:77]
	v_mfma_f32_16x16x128_f8f6f4 v[188:191], v[150:157], v[196:203], v[70:73]
	v_mfma_f32_16x16x128_f8f6f4 v[192:195], v[164:171], v[196:203], v[66:69]
	s_barrier
	s_add_u32 s62, s6, s24
	s_addc_u32 s63, s7, 0
	s_mov_b32 m0, s36
	v_lshl_add_u64 v[158:159], s[62:63], 0, v[148:149]
	s_nop 0
	ds_read_b128 v[66:69], v161 offset:16384
	ds_read_b128 v[70:73], v161 offset:17408
	ds_read_b128 v[74:77], v161 offset:18432
	ds_read_b128 v[78:81], v161 offset:19456
	ds_read_b128 v[82:85], v161 offset:20480
	ds_read_b128 v[86:89], v161 offset:21504
	ds_read_b128 v[90:93], v161 offset:22528
	ds_read_b128 v[94:97], v161 offset:23552
	global_load_lds_dwordx4 v[158:159], off
	v_lshl_add_u64 v[158:159], s[62:63], 0, v[146:147]
	s_add_i32 s62, s24, 0x20000
	s_add_u32 s62, s6, s62
	s_mov_b32 m0, s37
	s_addc_u32 s63, s7, 0
	global_load_lds_dwordx4 v[158:159], off
	v_lshl_add_u64 v[158:159], s[62:63], 0, v[148:149]
	s_mov_b32 m0, s38
	s_nop 0
	global_load_lds_dwordx4 v[158:159], off
	v_lshl_add_u64 v[158:159], s[62:63], 0, v[146:147]
	s_add_u32 s62, s6, s25
	s_mov_b32 m0, s39
	s_addc_u32 s63, s7, 0
	global_load_lds_dwordx4 v[158:159], off
	v_lshl_add_u64 v[158:159], s[62:63], 0, v[148:149]
	s_mov_b32 m0, s29
	s_nop 0
	global_load_lds_dwordx4 v[158:159], off
	v_lshl_add_u64 v[158:159], s[62:63], 0, v[146:147]
	s_mov_b32 m0, s40
	s_nop 0
	global_load_lds_dwordx4 v[158:159], off
	s_waitcnt vmcnt(8)
	s_waitcnt lgkmcnt(0)
	s_barrier
	s_waitcnt lgkmcnt(0)
	v_mfma_f32_16x16x128_f8f6f4 v[62:65], v[130:137], v[66:73], v[62:65]
	v_mfma_f32_16x16x128_f8f6f4 v[58:61], v[138:145], v[66:73], v[58:61]
	v_mfma_f32_16x16x128_f8f6f4 v[50:53], v[130:137], v[74:81], v[50:53]
	v_mfma_f32_16x16x128_f8f6f4 v[196:199], v[138:145], v[74:81], v[42:45]
	v_mfma_f32_16x16x128_f8f6f4 v[200:203], v[130:137], v[82:89], v[38:41]
	v_mfma_f32_16x16x128_f8f6f4 v[212:215], v[138:145], v[82:89], v[30:33]
	v_mfma_f32_16x16x128_f8f6f4 v[216:219], v[130:137], v[90:97], v[22:25]
	v_mfma_f32_16x16x128_f8f6f4 v[220:223], v[138:145], v[90:97], v[14:17]
	v_mfma_f32_16x16x128_f8f6f4 v[54:57], v[150:157], v[66:73], v[54:57]
	v_mfma_f32_16x16x128_f8f6f4 v[224:227], v[164:171], v[66:73], v[46:49]
	v_mfma_f32_16x16x128_f8f6f4 v[228:231], v[150:157], v[74:81], v[34:37]
	v_mfma_f32_16x16x128_f8f6f4 v[232:235], v[164:171], v[74:81], v[26:29]
	v_mfma_f32_16x16x128_f8f6f4 v[236:239], v[150:157], v[82:89], v[18:21]
	v_mfma_f32_16x16x128_f8f6f4 v[240:243], v[164:171], v[82:89], v[10:13]
	v_mfma_f32_16x16x128_f8f6f4 v[244:247], v[150:157], v[90:97], v[6:9]
	v_mfma_f32_16x16x128_f8f6f4 v[248:251], v[164:171], v[90:97], v[2:5]
	s_barrier
; #define PG8_STAGE(bufoff, gbase, voff) do { _Pragma("unroll") for (int _i = 0; _i < 2; ++_i) \
;         __builtin_amdgcn_global_load_lds((const unsigned*)(wsb + (size_t)(gbase) + (voff)[_i]), (LAS unsigned*)(lds + (bufoff) + ldsw + _i * 8192), 16, 0, 0); } while (0)
; #define PG8_LDA(dst, b, h) do { _Pragma("unroll") for (int m = 0; m < 4; ++m) { if constexpr (FP8) dst##8[m] = PG8_LD8(pa, PG8_SA(b, h) + m * 2048); \
;         else { _Pragma("unroll") for (int k = 0; k < 2; ++k) dst[m][k] = *(const LAS bf16x8*)(pa + PG8_SA(b, h) + m * 2048 + k * 1024); } } } while (0)
; #define PG8_LDB(dst, b, h) do { _Pragma("unroll") for (int n = 0; n < 2; ++n) { if constexpr (FP8) dst##8[n] = PG8_LD8(pb, PG8_SA(b, h) + n * 2048); \
;         else { _Pragma("unroll") for (int k = 0; k < 2; ++k) dst[n][k] = *(const LAS bf16x8*)(pb + PG8_SA(b, h) + n * 2048 + k * 1024); } } } while (0)
; #define PG8_WAIT_V(n) asm volatile("s_waitcnt vmcnt(" #n ")" ::: "memory")
; #define PG8_WAIT_L(n) asm volatile("s_waitcnt lgkmcnt(" #n ")" ::: "memory")
; #define PG8_BAR __builtin_amdgcn_s_barrier()
; #define PG8_SCHED __builtin_amdgcn_sched_barrier(0)
; template <class Epi, class Sched, bool PERM, bool FP8 = false, bool GATHER = false>
; DI void gemm_phase(LAS unsigned char* lds, const unsigned char* wsb, const unsigned lda, const unsigned ldb, const int nt, const Sched& S, const Epi& E) {
;     ...
;             PG8_LDB(B0, 1, 0); PG8_LDB(B1, 1, 1); PG8_SCHED; PG8_LDA(At, 1, 0); PG8_STAGEA(PG8_SA(0, 1), k2, 1, last);
;             PG8_WAIT_V(8); PG8_WAIT_L(0); PG8_BAR; PG8_MMA(0, 0, At, B0); PG8_MMA(0, 1, At, B1); PG8_BAR; PG8_SCHED;
;             PG8_LDA(At, 1, 1); PG8_STAGE(PG8_SB(1, 0), b3, voffB); PG8_STAGE(PG8_SB(1, 1), b3 + hstepB, voffB); PG8_STAGEA(PG8_SA(1, 0), k3, 0, last);
;             PG8_WAIT_V(8); PG8_WAIT_L(0); PG8_BAR; PG8_MMA(1, 0, At, B0); PG8_MMA(1, 1, At, B1); PG8_BAR; PG8_SCHED;
;         }
;         if (wr == 0) PG8_BAR;
	s_nop 4
	ds_read_b128 v[2:5], v162 offset:32768
	ds_read_b128 v[6:9], v162 offset:33792
	ds_read_b128 v[10:13], v162 offset:34816
	ds_read_b128 v[14:17], v162 offset:35840
	ds_read_b128 v[130:133], v162 offset:49152
	ds_read_b128 v[134:137], v162 offset:50176
	ds_read_b128 v[138:141], v162 offset:51200
	ds_read_b128 v[142:145], v162 offset:52224
	s_add_i32 s62, s25, 0x20000
	s_add_u32 s62, s6, s62
	s_addc_u32 s63, s7, 0
	s_mov_b32 m0, s41
	v_lshl_add_u64 v[66:67], s[62:63], 0, v[148:149]
	ds_read_b128 v[18:21], v161 offset:32768
	ds_read_b128 v[22:25], v161 offset:33792
	ds_read_b128 v[26:29], v161 offset:34816
	ds_read_b128 v[30:33], v161 offset:35840
	ds_read_b128 v[34:37], v161 offset:36864
	ds_read_b128 v[38:41], v161 offset:37888
	ds_read_b128 v[42:45], v161 offset:38912
	ds_read_b128 v[46:49], v161 offset:39936
	global_load_lds_dwordx4 v[66:67], off
	v_lshl_add_u64 v[66:67], s[62:63], 0, v[146:147]
	s_mov_b32 m0, s42
	s_nop 0
	global_load_lds_dwordx4 v[66:67], off
	s_waitcnt vmcnt(8)
	s_waitcnt lgkmcnt(0)
	s_barrier
	s_waitcnt lgkmcnt(0)
	v_mfma_f32_16x16x128_f8f6f4 v[126:129], v[2:9], v[18:25], v[126:129]
	v_mfma_f32_16x16x128_f8f6f4 v[122:125], v[10:17], v[18:25], v[122:125]
	v_mfma_f32_16x16x128_f8f6f4 v[118:121], v[2:9], v[26:33], v[118:121]
	v_mfma_f32_16x16x128_f8f6f4 v[114:117], v[10:17], v[26:33], v[114:117]
	v_mfma_f32_16x16x128_f8f6f4 v[102:105], v[2:9], v[34:41], v[102:105]
	v_mfma_f32_16x16x128_f8f6f4 v[98:101], v[10:17], v[34:41], v[98:101]
	v_mfma_f32_16x16x128_f8f6f4 v[86:89], v[2:9], v[42:49], v[204:207]
	v_mfma_f32_16x16x128_f8f6f4 v[78:81], v[10:17], v[42:49], v[208:211]
	v_mfma_f32_16x16x128_f8f6f4 v[110:113], v[130:137], v[18:25], v[110:113]
	v_mfma_f32_16x16x128_f8f6f4 v[106:109], v[138:145], v[18:25], v[106:109]
	v_mfma_f32_16x16x128_f8f6f4 v[94:97], v[130:137], v[26:33], v[172:175]
	v_mfma_f32_16x16x128_f8f6f4 v[90:93], v[138:145], v[26:33], v[176:179]
	v_mfma_f32_16x16x128_f8f6f4 v[82:85], v[130:137], v[34:41], v[180:183]
	v_mfma_f32_16x16x128_f8f6f4 v[74:77], v[138:145], v[34:41], v[184:187]
	v_mfma_f32_16x16x128_f8f6f4 v[70:73], v[130:137], v[42:49], v[188:191]
	v_mfma_f32_16x16x128_f8f6f4 v[66:69], v[138:145], v[42:49], v[192:195]
	s_barrier
	s_add_u32 s62, s6, s61
	s_addc_u32 s63, s7, 0
	s_mov_b32 m0, s46
	v_lshl_add_u64 v[18:19], s[62:63], 0, v[148:149]
	s_add_i32 s24, s24, 0x20080
	ds_read_b128 v[150:153], v161 offset:49152
	ds_read_b128 v[154:157], v161 offset:50176
	ds_read_b128 v[164:167], v161 offset:51200
	ds_read_b128 v[168:171], v161 offset:52224
	ds_read_b128 v[172:175], v161 offset:53248
	ds_read_b128 v[176:179], v161 offset:54272
	ds_read_b128 v[180:183], v161 offset:55296
	ds_read_b128 v[184:187], v161 offset:56320
	global_load_lds_dwordx4 v[18:19], off
	v_lshl_add_u64 v[18:19], s[62:63], 0, v[146:147]
	s_add_u32 s62, s6, s24
	s_mov_b32 m0, s47
	s_addc_u32 s63, s7, 0
	s_addk_i32 s25, 0x80
	global_load_lds_dwordx4 v[18:19], off
	v_lshl_add_u64 v[18:19], s[62:63], 0, v[148:149]
	s_mov_b32 m0, s50
	s_add_u32 s24, s6, s25
	global_load_lds_dwordx4 v[18:19], off
	v_lshl_add_u64 v[18:19], s[62:63], 0, v[146:147]
	s_mov_b32 m0, s51
	s_addc_u32 s25, s7, 0
	global_load_lds_dwordx4 v[18:19], off
	v_lshl_add_u64 v[18:19], s[24:25], 0, v[148:149]
	s_mov_b32 m0, s48
	s_nop 0
	global_load_lds_dwordx4 v[18:19], off
	v_lshl_add_u64 v[18:19], s[24:25], 0, v[146:147]
	s_mov_b32 m0, s49
	s_nop 0
	global_load_lds_dwordx4 v[18:19], off
	s_waitcnt vmcnt(8)
	s_waitcnt lgkmcnt(0)
	s_barrier
	s_waitcnt lgkmcnt(0)
	v_mfma_f32_16x16x128_f8f6f4 v[62:65], v[2:9], v[150:157], v[62:65]
	v_mfma_f32_16x16x128_f8f6f4 v[58:61], v[10:17], v[150:157], v[58:61]
	v_mfma_f32_16x16x128_f8f6f4 v[50:53], v[2:9], v[164:171], v[50:53]
	v_mfma_f32_16x16x128_f8f6f4 v[42:45], v[10:17], v[164:171], v[196:199]
	v_mfma_f32_16x16x128_f8f6f4 v[38:41], v[2:9], v[172:179], v[200:203]
	v_mfma_f32_16x16x128_f8f6f4 v[30:33], v[10:17], v[172:179], v[212:215]
	v_mfma_f32_16x16x128_f8f6f4 v[22:25], v[2:9], v[180:187], v[216:219]
	v_mfma_f32_16x16x128_f8f6f4 v[14:17], v[10:17], v[180:187], v[220:223]
	v_mfma_f32_16x16x128_f8f6f4 v[54:57], v[130:137], v[150:157], v[54:57]
	v_mfma_f32_16x16x128_f8f6f4 v[46:49], v[138:145], v[150:157], v[224:227]
	v_mfma_f32_16x16x128_f8f6f4 v[34:37], v[130:137], v[164:171], v[228:231]
	v_mfma_f32_16x16x128_f8f6f4 v[26:29], v[138:145], v[164:171], v[232:235]
	v_mfma_f32_16x16x128_f8f6f4 v[18:21], v[130:137], v[172:179], v[236:239]
	v_mfma_f32_16x16x128_f8f6f4 v[10:13], v[138:145], v[172:179], v[240:243]
	v_mfma_f32_16x16x128_f8f6f4 v[6:9], v[130:137], v[180:187], v[244:247]
	v_mfma_f32_16x16x128_f8f6f4 v[2:5], v[138:145], v[180:187], v[248:251]
	s_barrier
	s_add_i32 s23, s23, 2
	s_addk_i32 s21, 0x100
	s_addk_i32 s22, 0x100
	s_cmp_gt_u32 s23, 5
	s_cbranch_scc0 .LBB0_910
	s_and_b64 vcc, exec, s[10:11]
	s_cbranch_vccz .LBB0_913
	s_barrier

; #define PG8_STAGE(bufoff, gbase, voff) do { _Pragma("unroll") for (int _i = 0; _i < 2; ++_i) \
;         __builtin_amdgcn_global_load_lds((const unsigned*)(wsb + (size_t)(gbase) + (voff)[_i]), (LAS unsigned*)(lds + (bufoff) + ldsw + _i * 8192), 16, 0, 0); } while (0)
; #define PG8_LDA(dst, b, h) do { _Pragma("unroll") for (int m = 0; m < 4; ++m) { if constexpr (FP8) dst##8[m] = PG8_LD8(pa, PG8_SA(b, h) + m * 2048); \
;         else { _Pragma("unroll") for (int k = 0; k < 2; ++k) dst[m][k] = *(const LAS bf16x8*)(pa + PG8_SA(b, h) + m * 2048 + k * 1024); } } } while (0)
; #define PG8_LDB(dst, b, h) do { _Pragma("unroll") for (int n = 0; n < 2; ++n) { if constexpr (FP8) dst##8[n] = PG8_LD8(pb, PG8_SA(b, h) + n * 2048); \
;         else { _Pragma("unroll") for (int k = 0; k < 2; ++k) dst[n][k] = *(const LAS bf16x8*)(pb + PG8_SA(b, h) + n * 2048 + k * 1024); } } } while (0)
; #define PG8_WAIT_V(n) asm volatile("s_waitcnt vmcnt(" #n ")" ::: "memory")
; #define PG8_WAIT_L(n) asm volatile("s_waitcnt lgkmcnt(" #n ")" ::: "memory")
; #define PG8_BAR __builtin_amdgcn_s_barrier()
; #define PG8_SCHED __builtin_amdgcn_sched_barrier(0)
; template <class Epi, class Sched, bool PERM, bool FP8 = false, bool GATHER = false>
; DI void gemm_phase(LAS unsigned char* lds, const unsigned char* wsb, const unsigned lda, const unsigned ldb, const int nt, const Sched& S, const Epi& E) {
;     ...
;             PG8_LDB(B0, 0, 0); PG8_LDB(B1, 0, 1); PG8_SCHED; PG8_LDA(At, 0, 0); PG8_STAGEA(PG8_SA(1, 1), t + 1, 1, false);
;             if constexpr (GATHER) { if (last) {
;                 int tz = tid; asm volatile("" : "+v"(tz));
; #pragma unroll
;                 for (int i = 0; i < 2; ++i) { int R, C; stage_rc(tz * 16 + i * 8192, R, C);
; #pragma unroll
;                     for (int h = 0; h < 2; ++h) { const unsigned tk = (unsigned)tokt[h * HALF + R]; offC[h][i] = (tk < (unsigned)NTOK ? tk : (unsigned)(NTOK - 1)) * lda + (unsigned)C * 2u; } } } }
;             PG8_WAIT_V(8); PG8_WAIT_L(0); PG8_BAR; PG8_MMA(0, 0, At, B0); PG8_MMA(0, 1, At, B1); PG8_BAR; PG8_SCHED;
;             PG8_LDA(At, 0, 1); PG8_STAGE(PG8_SB(0, 0), b2, voffB); PG8_STAGE(PG8_SB(0, 1), b2 + hstepB, voffB); PG8_STAGEA(PG8_SA(0, 0), k2, 0, last);
;             PG8_WAIT_V(8); PG8_WAIT_L(0); PG8_BAR; PG8_MMA(1, 0, At, B0); PG8_MMA(1, 1, At, B1); PG8_BAR; PG8_SCHED;
.LBB0_1342:
	s_waitcnt vmcnt(8)
	s_add_i32 s85, s83, s50
	s_waitcnt lgkmcnt(0)
	s_and_b64 s[86:87], s[52:53], exec
	s_cselect_b32 s85, s14, s85
	v_mov_b32_e32 v205, v197
	s_add_i32 s86, s85, 0x80
	s_barrier
	s_waitcnt lgkmcnt(0)
	v_mfma_f32_16x16x128_f8f6f4 v[190:193], v[18:25], v[58:65], v[190:193]
	v_mfma_f32_16x16x128_f8f6f4 v[186:189], v[26:33], v[58:65], v[186:189]
	v_mfma_f32_16x16x128_f8f6f4 v[174:177], v[18:25], v[50:57], v[174:177]
	v_mfma_f32_16x16x128_f8f6f4 v[166:169], v[26:33], v[50:57], v[166:169]
	v_mfma_f32_16x16x128_f8f6f4 v[158:161], v[18:25], v[42:49], v[158:161]
	v_mfma_f32_16x16x128_f8f6f4 v[150:153], v[26:33], v[42:49], v[150:153]
	v_mfma_f32_16x16x128_f8f6f4 v[142:145], v[18:25], v[34:41], v[142:145]
	v_mfma_f32_16x16x128_f8f6f4 v[134:137], v[26:33], v[34:41], v[134:137]
	v_mfma_f32_16x16x128_f8f6f4 v[182:185], v[2:9], v[58:65], v[182:185]
	v_mfma_f32_16x16x128_f8f6f4 v[178:181], v[10:17], v[58:65], v[178:181]
	v_mfma_f32_16x16x128_f8f6f4 v[170:173], v[2:9], v[50:57], v[170:173]
	v_mfma_f32_16x16x128_f8f6f4 v[162:165], v[10:17], v[50:57], v[162:165]
	v_mfma_f32_16x16x128_f8f6f4 v[154:157], v[2:9], v[42:49], v[154:157]
	v_mfma_f32_16x16x128_f8f6f4 v[146:149], v[10:17], v[42:49], v[146:149]
	v_mfma_f32_16x16x128_f8f6f4 v[138:141], v[2:9], v[34:41], v[138:141]
	v_mfma_f32_16x16x128_f8f6f4 v[130:133], v[10:17], v[34:41], v[130:133]
	s_barrier
	s_add_u32 s88, s10, s85
	s_addc_u32 s89, s11, 0
	s_mov_b32 m0, s41
	v_lshl_add_u64 v[214:215], s[88:89], 0, v[198:199]
	s_add_i32 s87, s85, 0x20000
	ds_read_b128 v[34:37], v209 offset:16384
	ds_read_b128 v[38:41], v209 offset:17408
	ds_read_b128 v[42:45], v209 offset:18432
	ds_read_b128 v[46:49], v209 offset:19456
	ds_read_b128 v[50:53], v209 offset:20480
	ds_read_b128 v[54:57], v209 offset:21504
	ds_read_b128 v[58:61], v209 offset:22528
	ds_read_b128 v[62:65], v209 offset:23552
	global_load_lds_dwordx4 v[214:215], off
	v_lshl_add_u64 v[214:215], s[88:89], 0, v[200:201]
	s_add_u32 s88, s10, s87
	s_addc_u32 s89, s11, 0
	s_add_u32 s50, s50, 0x100
	s_addc_u32 s51, s51, 0
	s_mov_b32 m0, s46
	s_and_b64 s[52:53], s[52:53], exec
	global_load_lds_dwordx4 v[214:215], off
	v_lshl_add_u64 v[214:215], s[88:89], 0, v[198:199]
	s_mov_b32 m0, s47
	s_cselect_b32 s87, 0, s50
	global_load_lds_dwordx4 v[214:215], off
	v_lshl_add_u64 v[214:215], s[88:89], 0, v[200:201]
	s_mov_b32 m0, s54
	s_add_u32 s52, s12, s87
	global_load_lds_dwordx4 v[214:215], off
	s_addc_u32 s53, s13, 0
	s_mov_b32 m0, s39
	s_nop 0
	global_load_lds_dwordx4 v212, s[52:53]
	s_mov_b32 m0, s55
	s_nop 0
	global_load_lds_dwordx4 v202, s[52:53]
	s_waitcnt vmcnt(8)
	s_waitcnt lgkmcnt(0)
	s_barrier
	s_waitcnt lgkmcnt(0)
	v_mfma_f32_16x16x128_f8f6f4 v[126:129], v[18:25], v[34:41], v[126:129]
	v_mfma_f32_16x16x128_f8f6f4 v[118:121], v[26:33], v[34:41], v[118:121]
	v_mfma_f32_16x16x128_f8f6f4 v[110:113], v[18:25], v[42:49], v[110:113]
	v_mfma_f32_16x16x128_f8f6f4 v[102:105], v[26:33], v[42:49], v[102:105]
	v_mfma_f32_16x16x128_f8f6f4 v[94:97], v[18:25], v[50:57], v[94:97]
	v_mfma_f32_16x16x128_f8f6f4 v[86:89], v[26:33], v[50:57], v[86:89]
	v_mfma_f32_16x16x128_f8f6f4 v[78:81], v[18:25], v[58:65], v[78:81]
	v_mfma_f32_16x16x128_f8f6f4 v[70:73], v[26:33], v[58:65], v[70:73]
	v_mfma_f32_16x16x128_f8f6f4 v[122:125], v[2:9], v[34:41], v[122:125]
	v_mfma_f32_16x16x128_f8f6f4 v[114:117], v[10:17], v[34:41], v[114:117]
	v_mfma_f32_16x16x128_f8f6f4 v[106:109], v[2:9], v[42:49], v[106:109]
	v_mfma_f32_16x16x128_f8f6f4 v[98:101], v[10:17], v[42:49], v[98:101]
	v_mfma_f32_16x16x128_f8f6f4 v[90:93], v[2:9], v[50:57], v[90:93]
	v_mfma_f32_16x16x128_f8f6f4 v[82:85], v[10:17], v[50:57], v[82:85]
	v_mfma_f32_16x16x128_f8f6f4 v[74:77], v[2:9], v[58:65], v[74:77]
	v_mfma_f32_16x16x128_f8f6f4 v[66:69], v[10:17], v[58:65], v[66:69]
	s_barrier
; #define PG8_STAGE(bufoff, gbase, voff) do { _Pragma("unroll") for (int _i = 0; _i < 2; ++_i) \
;         __builtin_amdgcn_global_load_lds((const unsigned*)(wsb + (size_t)(gbase) + (voff)[_i]), (LAS unsigned*)(lds + (bufoff) + ldsw + _i * 8192), 16, 0, 0); } while (0)
; #define PG8_LDA(dst, b, h) do { _Pragma("unroll") for (int m = 0; m < 4; ++m) { if constexpr (FP8) dst##8[m] = PG8_LD8(pa, PG8_SA(b, h) + m * 2048); \
;         else { _Pragma("unroll") for (int k = 0; k < 2; ++k) dst[m][k] = *(const LAS bf16x8*)(pa + PG8_SA(b, h) + m * 2048 + k * 1024); } } } while (0)
; #define PG8_LDB(dst, b, h) do { _Pragma("unroll") for (int n = 0; n < 2; ++n) { if constexpr (FP8) dst##8[n] = PG8_LD8(pb, PG8_SA(b, h) + n * 2048); \
;         else { _Pragma("unroll") for (int k = 0; k < 2; ++k) dst[n][k] = *(const LAS bf16x8*)(pb + PG8_SA(b, h) + n * 2048 + k * 1024); } } } while (0)
; #define PG8_WAIT_V(n) asm volatile("s_waitcnt vmcnt(" #n ")" ::: "memory")
; #define PG8_WAIT_L(n) asm volatile("s_waitcnt lgkmcnt(" #n ")" ::: "memory")
; #define PG8_BAR __builtin_amdgcn_s_barrier()
; #define PG8_SCHED __builtin_amdgcn_sched_barrier(0)
; template <class Epi, class Sched, bool PERM, bool FP8 = false, bool GATHER = false>
; DI void gemm_phase(LAS unsigned char* lds, const unsigned char* wsb, const unsigned lda, const unsigned ldb, const int nt, const Sched& S, const Epi& E) {
;     ...
;             PG8_LDB(B0, 1, 0); PG8_LDB(B1, 1, 1); PG8_SCHED; PG8_LDA(At, 1, 0); PG8_STAGEA(PG8_SA(0, 1), k2, 1, last);
;             PG8_WAIT_V(8); PG8_WAIT_L(0); PG8_BAR; PG8_MMA(0, 0, At, B0); PG8_MMA(0, 1, At, B1); PG8_BAR; PG8_SCHED;
;             PG8_LDA(At, 1, 1); PG8_STAGE(PG8_SB(1, 0), b3, voffB); PG8_STAGE(PG8_SB(1, 1), b3 + hstepB, voffB); PG8_STAGEA(PG8_SA(1, 0), k3, 0, last);
;             PG8_WAIT_V(8); PG8_WAIT_L(0); PG8_BAR; PG8_MMA(1, 0, At, B0); PG8_MMA(1, 1, At, B1); PG8_BAR; PG8_SCHED;
;         }
	ds_read_b128 v[2:5], v210 offset:32768
	ds_read_b128 v[6:9], v210 offset:33792
	ds_read_b128 v[10:13], v210 offset:34816
	ds_read_b128 v[14:17], v210 offset:35840
	ds_read_b128 v[18:21], v210 offset:49152
	ds_read_b128 v[22:25], v210 offset:50176
	ds_read_b128 v[26:29], v210 offset:51200
	ds_read_b128 v[30:33], v210 offset:52224
	s_mov_b32 m0, s56
	v_lshl_add_u64 v[214:215], s[52:53], 0, v[196:197]
	ds_read_b128 v[34:37], v209 offset:32768
	ds_read_b128 v[38:41], v209 offset:33792
	ds_read_b128 v[42:45], v209 offset:34816
	ds_read_b128 v[46:49], v209 offset:35840
	ds_read_b128 v[50:53], v209 offset:36864
	ds_read_b128 v[54:57], v209 offset:37888
	ds_read_b128 v[58:61], v209 offset:38912
	ds_read_b128 v[62:65], v209 offset:39936
	global_load_lds_dwordx4 v[214:215], off
	v_lshl_add_u64 v[214:215], s[52:53], 0, v[204:205]
	s_mov_b32 m0, s57
	s_nop 0
	global_load_lds_dwordx4 v[214:215], off
	s_waitcnt vmcnt(8)
	s_waitcnt lgkmcnt(0)
	s_barrier
	s_waitcnt lgkmcnt(0)
	v_mfma_f32_16x16x128_f8f6f4 v[190:193], v[2:9], v[34:41], v[190:193]
	v_mfma_f32_16x16x128_f8f6f4 v[186:189], v[10:17], v[34:41], v[186:189]
	v_mfma_f32_16x16x128_f8f6f4 v[174:177], v[2:9], v[42:49], v[174:177]
	v_mfma_f32_16x16x128_f8f6f4 v[166:169], v[10:17], v[42:49], v[166:169]
	v_mfma_f32_16x16x128_f8f6f4 v[158:161], v[2:9], v[50:57], v[158:161]
	v_mfma_f32_16x16x128_f8f6f4 v[150:153], v[10:17], v[50:57], v[150:153]
	v_mfma_f32_16x16x128_f8f6f4 v[142:145], v[2:9], v[58:65], v[142:145]
	v_mfma_f32_16x16x128_f8f6f4 v[134:137], v[10:17], v[58:65], v[134:137]
	v_mfma_f32_16x16x128_f8f6f4 v[182:185], v[18:25], v[34:41], v[182:185]
	v_mfma_f32_16x16x128_f8f6f4 v[178:181], v[26:33], v[34:41], v[178:181]
	v_mfma_f32_16x16x128_f8f6f4 v[170:173], v[18:25], v[42:49], v[170:173]
	v_mfma_f32_16x16x128_f8f6f4 v[162:165], v[26:33], v[42:49], v[162:165]
	v_mfma_f32_16x16x128_f8f6f4 v[154:157], v[18:25], v[50:57], v[154:157]
	v_mfma_f32_16x16x128_f8f6f4 v[146:149], v[26:33], v[50:57], v[146:149]
	v_mfma_f32_16x16x128_f8f6f4 v[138:141], v[18:25], v[58:65], v[138:141]
	v_mfma_f32_16x16x128_f8f6f4 v[130:133], v[26:33], v[58:65], v[130:133]
	s_barrier
	s_add_u32 s52, s10, s86
	s_addc_u32 s53, s11, 0
	s_mov_b32 m0, s61
	v_lshl_add_u64 v[214:215], s[52:53], 0, v[198:199]
	s_add_i32 s85, s85, 0x20080
	ds_read_b128 v[34:37], v209 offset:49152
	ds_read_b128 v[38:41], v209 offset:50176
	ds_read_b128 v[42:45], v209 offset:51200
	ds_read_b128 v[46:49], v209 offset:52224
	ds_read_b128 v[50:53], v209 offset:53248
	ds_read_b128 v[54:57], v209 offset:54272
	ds_read_b128 v[58:61], v209 offset:55296
	ds_read_b128 v[62:65], v209 offset:56320
	global_load_lds_dwordx4 v[214:215], off
	v_lshl_add_u64 v[214:215], s[52:53], 0, v[200:201]
	s_add_u32 s52, s10, s85
	s_mov_b32 m0, s63
	s_addc_u32 s53, s11, 0
	global_load_lds_dwordx4 v[214:215], off
	v_lshl_add_u64 v[214:215], s[52:53], 0, v[198:199]
	s_mov_b32 m0, s66
	s_nop 0
	global_load_lds_dwordx4 v[214:215], off
	v_lshl_add_u64 v[214:215], s[52:53], 0, v[200:201]
	s_add_u32 s52, s10, s87
	s_addc_u32 s53, s11, 0
	s_mov_b32 m0, s67
	s_add_u32 s52, s52, 0x5b9d4080
	global_load_lds_dwordx4 v[214:215], off
	s_addc_u32 s53, s53, 0
	s_mov_b32 m0, s64
	s_nop 0
	global_load_lds_dwordx4 v212, s[52:53]
	s_mov_b32 m0, s65
	s_nop 0
	global_load_lds_dwordx4 v202, s[52:53]
	s_waitcnt vmcnt(8)
	s_waitcnt lgkmcnt(0)
	s_barrier
	s_waitcnt lgkmcnt(0)
	v_mfma_f32_16x16x128_f8f6f4 v[126:129], v[2:9], v[34:41], v[126:129]
	v_mfma_f32_16x16x128_f8f6f4 v[118:121], v[10:17], v[34:41], v[118:121]
	v_mfma_f32_16x16x128_f8f6f4 v[110:113], v[2:9], v[42:49], v[110:113]
	v_mfma_f32_16x16x128_f8f6f4 v[102:105], v[10:17], v[42:49], v[102:105]
	v_mfma_f32_16x16x128_f8f6f4 v[94:97], v[2:9], v[50:57], v[94:97]
	v_mfma_f32_16x16x128_f8f6f4 v[86:89], v[10:17], v[50:57], v[86:89]
	v_mfma_f32_16x16x128_f8f6f4 v[78:81], v[2:9], v[58:65], v[78:81]
	v_mfma_f32_16x16x128_f8f6f4 v[70:73], v[10:17], v[58:65], v[70:73]
	v_mfma_f32_16x16x128_f8f6f4 v[122:125], v[18:25], v[34:41], v[122:125]
	v_mfma_f32_16x16x128_f8f6f4 v[114:117], v[26:33], v[34:41], v[114:117]
	v_mfma_f32_16x16x128_f8f6f4 v[106:109], v[18:25], v[42:49], v[106:109]
	v_mfma_f32_16x16x128_f8f6f4 v[98:101], v[26:33], v[42:49], v[98:101]
	v_mfma_f32_16x16x128_f8f6f4 v[90:93], v[18:25], v[50:57], v[90:93]
	v_mfma_f32_16x16x128_f8f6f4 v[82:85], v[26:33], v[50:57], v[82:85]
	v_mfma_f32_16x16x128_f8f6f4 v[74:77], v[18:25], v[58:65], v[74:77]
	v_mfma_f32_16x16x128_f8f6f4 v[66:69], v[26:33], v[58:65], v[66:69]
	s_barrier
	s_add_i32 s84, s84, 2
	s_cmp_gt_u32 s84, 5
	s_cbranch_scc1 .LBB0_1345

; #define PG8_STAGE(bufoff, gbase, voff) do { _Pragma("unroll") for (int _i = 0; _i < 2; ++_i) \
;         __builtin_amdgcn_global_load_lds((const unsigned*)(wsb + (size_t)(gbase) + (voff)[_i]), (LAS unsigned*)(lds + (bufoff) + ldsw + _i * 8192), 16, 0, 0); } while (0)
; #define PG8_LDA(dst, b, h) do { _Pragma("unroll") for (int m = 0; m < 4; ++m) { if constexpr (FP8) dst##8[m] = PG8_LD8(pa, PG8_SA(b, h) + m * 2048); \
;         else { _Pragma("unroll") for (int k = 0; k < 2; ++k) dst[m][k] = *(const LAS bf16x8*)(pa + PG8_SA(b, h) + m * 2048 + k * 1024); } } } while (0)
; #define PG8_LDB(dst, b, h) do { _Pragma("unroll") for (int n = 0; n < 2; ++n) { if constexpr (FP8) dst##8[n] = PG8_LD8(pb, PG8_SA(b, h) + n * 2048); \
;         else { _Pragma("unroll") for (int k = 0; k < 2; ++k) dst[n][k] = *(const LAS bf16x8*)(pb + PG8_SA(b, h) + n * 2048 + k * 1024); } } } while (0)
; #define PG8_WAIT_V(n) asm volatile("s_waitcnt vmcnt(" #n ")" ::: "memory")
; #define PG8_WAIT_L(n) asm volatile("s_waitcnt lgkmcnt(" #n ")" ::: "memory")
; #define PG8_BAR __builtin_amdgcn_s_barrier()
; #define PG8_SCHED __builtin_amdgcn_sched_barrier(0)
; template <class Epi, class Sched, bool PERM, bool FP8 = false, bool GATHER = false>
; DI void gemm_phase(LAS unsigned char* lds, const unsigned char* wsb, const unsigned lda, const unsigned ldb, const int nt, const Sched& S, const Epi& E) {
;     ...
;             PG8_LDB(B0, 0, 0); PG8_LDB(B1, 0, 1); PG8_SCHED; PG8_LDA(At, 0, 0); PG8_STAGEA(PG8_SA(1, 1), t + 1, 1, false);
;             if constexpr (GATHER) { if (last) {
;                 int tz = tid; asm volatile("" : "+v"(tz));
; #pragma unroll
;                 for (int i = 0; i < 2; ++i) { int R, C; stage_rc(tz * 16 + i * 8192, R, C);
; #pragma unroll
;                     for (int h = 0; h < 2; ++h) { const unsigned tk = (unsigned)tokt[h * HALF + R]; offC[h][i] = (tk < (unsigned)NTOK ? tk : (unsigned)(NTOK - 1)) * lda + (unsigned)C * 2u; } } } }
;             PG8_WAIT_V(8); PG8_WAIT_L(0); PG8_BAR; PG8_MMA(0, 0, At, B0); PG8_MMA(0, 1, At, B1); PG8_BAR; PG8_SCHED;
;             PG8_LDA(At, 0, 1); PG8_STAGE(PG8_SB(0, 0), b2, voffB); PG8_STAGE(PG8_SB(0, 1), b2 + hstepB, voffB); PG8_STAGEA(PG8_SA(0, 0), k2, 0, last);
;             PG8_WAIT_V(8); PG8_WAIT_L(0); PG8_BAR; PG8_MMA(1, 0, At, B0); PG8_MMA(1, 1, At, B1); PG8_BAR; PG8_SCHED;
.LBB0_1450:
	ds_read_b128 v[130:133], v154
	ds_read_b128 v[134:137], v154 offset:1024
	ds_read_b128 v[138:141], v154 offset:2048
	ds_read_b128 v[142:145], v154 offset:3072
	ds_read_b128 v[158:161], v154 offset:16384
	ds_read_b128 v[162:165], v154 offset:17408
	ds_read_b128 v[166:169], v154 offset:18432
	ds_read_b128 v[170:173], v154 offset:19456
	s_add_i32 s74, s71, 0xfffe0080
	s_add_i32 s75, s74, s68
	s_cmp_eq_u32 s70, 4
	s_cselect_b64 s[24:25], -1, 0
	s_and_b64 s[72:73], s[24:25], exec
	s_cselect_b32 s72, s69, s75
	s_cselect_b32 s76, 0, s74
	s_add_i32 s73, s72, 0x80
	s_add_i32 s74, s67, s71
	s_add_u32 s74, s10, s74
	s_addc_u32 s75, s11, 0
	v_lshl_add_u64 v[150:151], s[74:75], 0, v[146:147]
	s_add_i32 m0, s5, 0xc000
	ds_read_b128 v[174:177], v153
	ds_read_b128 v[178:181], v153 offset:1024
	ds_read_b128 v[182:185], v153 offset:2048
	ds_read_b128 v[186:189], v153 offset:3072
	ds_read_b128 v[190:193], v153 offset:4096
	ds_read_b128 v[194:197], v153 offset:5120
	ds_read_b128 v[198:201], v153 offset:6144
	ds_read_b128 v[202:205], v153 offset:7168
	global_load_lds_dwordx4 v[150:151], off
	v_lshl_add_u64 v[150:151], s[74:75], 0, v[148:149]
	s_add_i32 m0, s5, 0xe000
	s_nop 0
	global_load_lds_dwordx4 v[150:151], off
	s_waitcnt vmcnt(8)
	s_waitcnt lgkmcnt(0)
	s_barrier
	s_waitcnt lgkmcnt(0)
	v_mfma_f32_16x16x128_f8f6f4 v[126:129], v[130:137], v[174:181], v[126:129]
	v_mfma_f32_16x16x128_f8f6f4 v[122:125], v[138:145], v[174:181], v[122:125]
	v_mfma_f32_16x16x128_f8f6f4 v[118:121], v[130:137], v[182:189], v[118:121]
	v_mfma_f32_16x16x128_f8f6f4 v[114:117], v[138:145], v[182:189], v[114:117]
	v_mfma_f32_16x16x128_f8f6f4 v[206:209], v[130:137], v[190:197], v[94:97]
	v_mfma_f32_16x16x128_f8f6f4 v[210:213], v[138:145], v[190:197], v[90:93]
	v_mfma_f32_16x16x128_f8f6f4 v[214:217], v[130:137], v[198:205], v[82:85]
	v_mfma_f32_16x16x128_f8f6f4 v[218:221], v[138:145], v[198:205], v[74:77]
	v_mfma_f32_16x16x128_f8f6f4 v[110:113], v[158:165], v[174:181], v[110:113]
	v_mfma_f32_16x16x128_f8f6f4 v[106:109], v[166:173], v[174:181], v[106:109]
	v_mfma_f32_16x16x128_f8f6f4 v[102:105], v[158:165], v[182:189], v[102:105]
	v_mfma_f32_16x16x128_f8f6f4 v[98:101], v[166:173], v[182:189], v[98:101]
	v_mfma_f32_16x16x128_f8f6f4 v[174:177], v[158:165], v[190:197], v[86:89]
	v_mfma_f32_16x16x128_f8f6f4 v[178:181], v[166:173], v[190:197], v[78:81]
	v_mfma_f32_16x16x128_f8f6f4 v[182:185], v[158:165], v[198:205], v[70:73]
	v_mfma_f32_16x16x128_f8f6f4 v[186:189], v[166:173], v[198:205], v[66:69]
	s_barrier
	s_add_u32 s74, s10, s72
	s_addc_u32 s75, s11, 0
	s_mov_b32 m0, s19
	v_lshl_add_u64 v[150:151], s[74:75], 0, v[146:147]
	s_nop 0
	ds_read_b128 v[66:69], v153 offset:16384
	ds_read_b128 v[70:73], v153 offset:17408
	ds_read_b128 v[74:77], v153 offset:18432
	ds_read_b128 v[78:81], v153 offset:19456
	ds_read_b128 v[82:85], v153 offset:20480
	ds_read_b128 v[86:89], v153 offset:21504
	ds_read_b128 v[90:93], v153 offset:22528
	ds_read_b128 v[94:97], v153 offset:23552
	global_load_lds_dwordx4 v[150:151], off
	v_lshl_add_u64 v[150:151], s[74:75], 0, v[148:149]
	s_add_i32 s74, s72, 0x20000
	s_add_u32 s74, s10, s74
	s_addc_u32 s75, s11, 0
	s_and_b64 s[24:25], s[20:21], s[24:25]
	s_and_b64 s[24:25], s[24:25], exec
	s_mov_b32 m0, s28
	s_cselect_b32 s24, s60, s67
	global_load_lds_dwordx4 v[150:151], off
	v_lshl_add_u64 v[150:151], s[74:75], 0, v[146:147]
	s_mov_b32 m0, s29
	s_add_i32 s24, s76, s24
	global_load_lds_dwordx4 v[150:151], off
	v_lshl_add_u64 v[150:151], s[74:75], 0, v[148:149]
	s_add_u32 s74, s10, s24
	s_mov_b32 m0, s36
	s_addc_u32 s75, s11, 0
	global_load_lds_dwordx4 v[150:151], off
	v_lshl_add_u64 v[150:151], s[74:75], 0, v[146:147]
	s_mov_b32 m0, s5
	s_nop 0
	global_load_lds_dwordx4 v[150:151], off
	v_lshl_add_u64 v[150:151], s[74:75], 0, v[148:149]
	s_mov_b32 m0, s37
	s_nop 0
	global_load_lds_dwordx4 v[150:151], off
	s_waitcnt vmcnt(8)
	s_waitcnt lgkmcnt(0)
	s_barrier
	s_waitcnt lgkmcnt(0)
	v_mfma_f32_16x16x128_f8f6f4 v[62:65], v[130:137], v[66:73], v[62:65]
	v_mfma_f32_16x16x128_f8f6f4 v[58:61], v[138:145], v[66:73], v[58:61]
	v_mfma_f32_16x16x128_f8f6f4 v[50:53], v[130:137], v[74:81], v[50:53]
	v_mfma_f32_16x16x128_f8f6f4 v[190:193], v[138:145], v[74:81], v[42:45]
	v_mfma_f32_16x16x128_f8f6f4 v[194:197], v[130:137], v[82:89], v[34:37]
	v_mfma_f32_16x16x128_f8f6f4 v[198:201], v[138:145], v[82:89], v[26:29]
	v_mfma_f32_16x16x128_f8f6f4 v[202:205], v[130:137], v[90:97], v[18:21]
	v_mfma_f32_16x16x128_f8f6f4 v[222:225], v[138:145], v[90:97], v[10:13]
	v_mfma_f32_16x16x128_f8f6f4 v[54:57], v[158:165], v[66:73], v[54:57]
	v_mfma_f32_16x16x128_f8f6f4 v[226:229], v[166:173], v[66:73], v[46:49]
	v_mfma_f32_16x16x128_f8f6f4 v[230:233], v[158:165], v[74:81], v[38:41]
	v_mfma_f32_16x16x128_f8f6f4 v[234:237], v[166:173], v[74:81], v[30:33]
	v_mfma_f32_16x16x128_f8f6f4 v[238:241], v[158:165], v[82:89], v[22:25]
	v_mfma_f32_16x16x128_f8f6f4 v[242:245], v[166:173], v[82:89], v[14:17]
	v_mfma_f32_16x16x128_f8f6f4 v[246:249], v[158:165], v[90:97], v[6:9]
	v_mfma_f32_16x16x128_f8f6f4 v[250:253], v[166:173], v[90:97], v[2:5]
	s_barrier
; #define PG8_STAGE(bufoff, gbase, voff) do { _Pragma("unroll") for (int _i = 0; _i < 2; ++_i) \
;         __builtin_amdgcn_global_load_lds((const unsigned*)(wsb + (size_t)(gbase) + (voff)[_i]), (LAS unsigned*)(lds + (bufoff) + ldsw + _i * 8192), 16, 0, 0); } while (0)
; #define PG8_LDA(dst, b, h) do { _Pragma("unroll") for (int m = 0; m < 4; ++m) { if constexpr (FP8) dst##8[m] = PG8_LD8(pa, PG8_SA(b, h) + m * 2048); \
;         else { _Pragma("unroll") for (int k = 0; k < 2; ++k) dst[m][k] = *(const LAS bf16x8*)(pa + PG8_SA(b, h) + m * 2048 + k * 1024); } } } while (0)
; #define PG8_LDB(dst, b, h) do { _Pragma("unroll") for (int n = 0; n < 2; ++n) { if constexpr (FP8) dst##8[n] = PG8_LD8(pb, PG8_SA(b, h) + n * 2048); \
;         else { _Pragma("unroll") for (int k = 0; k < 2; ++k) dst[n][k] = *(const LAS bf16x8*)(pb + PG8_SA(b, h) + n * 2048 + k * 1024); } } } while (0)
; #define PG8_WAIT_V(n) asm volatile("s_waitcnt vmcnt(" #n ")" ::: "memory")
; #define PG8_WAIT_L(n) asm volatile("s_waitcnt lgkmcnt(" #n ")" ::: "memory")
; #define PG8_BAR __builtin_amdgcn_s_barrier()
; #define PG8_SCHED __builtin_amdgcn_sched_barrier(0)
; template <class Epi, class Sched, bool PERM, bool FP8 = false, bool GATHER = false>
; DI void gemm_phase(LAS unsigned char* lds, const unsigned char* wsb, const unsigned lda, const unsigned ldb, const int nt, const Sched& S, const Epi& E) {
;     ...
;             PG8_LDB(B0, 1, 0); PG8_LDB(B1, 1, 1); PG8_SCHED; PG8_LDA(At, 1, 0); PG8_STAGEA(PG8_SA(0, 1), k2, 1, last);
;             PG8_WAIT_V(8); PG8_WAIT_L(0); PG8_BAR; PG8_MMA(0, 0, At, B0); PG8_MMA(0, 1, At, B1); PG8_BAR; PG8_SCHED;
;             PG8_LDA(At, 1, 1); PG8_STAGE(PG8_SB(1, 0), b3, voffB); PG8_STAGE(PG8_SB(1, 1), b3 + hstepB, voffB); PG8_STAGEA(PG8_SA(1, 0), k3, 0, last);
;             PG8_WAIT_V(8); PG8_WAIT_L(0); PG8_BAR; PG8_MMA(1, 0, At, B0); PG8_MMA(1, 1, At, B1); PG8_BAR; PG8_SCHED;
;         }
;         if (wr == 0) PG8_BAR;
	s_nop 4
	ds_read_b128 v[2:5], v154 offset:32768
	ds_read_b128 v[6:9], v154 offset:33792
	ds_read_b128 v[10:13], v154 offset:34816
	ds_read_b128 v[14:17], v154 offset:35840
	ds_read_b128 v[130:133], v154 offset:49152
	ds_read_b128 v[134:137], v154 offset:50176
	ds_read_b128 v[138:141], v154 offset:51200
	ds_read_b128 v[142:145], v154 offset:52224
	s_add_i32 s25, s24, 0x20000
	s_add_u32 s74, s10, s25
	s_addc_u32 s75, s11, 0
	s_mov_b32 m0, s38
	v_lshl_add_u64 v[66:67], s[74:75], 0, v[146:147]
	ds_read_b128 v[18:21], v153 offset:32768
	ds_read_b128 v[22:25], v153 offset:33792
	ds_read_b128 v[26:29], v153 offset:34816
	ds_read_b128 v[30:33], v153 offset:35840
	ds_read_b128 v[34:37], v153 offset:36864
	ds_read_b128 v[38:41], v153 offset:37888
	ds_read_b128 v[42:45], v153 offset:38912
	ds_read_b128 v[46:49], v153 offset:39936
	global_load_lds_dwordx4 v[66:67], off
	v_lshl_add_u64 v[66:67], s[74:75], 0, v[148:149]
	s_mov_b32 m0, s39
	s_nop 0
	global_load_lds_dwordx4 v[66:67], off
	s_waitcnt vmcnt(8)
	s_waitcnt lgkmcnt(0)
	s_barrier
	s_waitcnt lgkmcnt(0)
	v_mfma_f32_16x16x128_f8f6f4 v[126:129], v[2:9], v[18:25], v[126:129]
	v_mfma_f32_16x16x128_f8f6f4 v[122:125], v[10:17], v[18:25], v[122:125]
	v_mfma_f32_16x16x128_f8f6f4 v[118:121], v[2:9], v[26:33], v[118:121]
	v_mfma_f32_16x16x128_f8f6f4 v[114:117], v[10:17], v[26:33], v[114:117]
	v_mfma_f32_16x16x128_f8f6f4 v[94:97], v[2:9], v[34:41], v[206:209]
	v_mfma_f32_16x16x128_f8f6f4 v[90:93], v[10:17], v[34:41], v[210:213]
	v_mfma_f32_16x16x128_f8f6f4 v[82:85], v[2:9], v[42:49], v[214:217]
	v_mfma_f32_16x16x128_f8f6f4 v[74:77], v[10:17], v[42:49], v[218:221]
	v_mfma_f32_16x16x128_f8f6f4 v[110:113], v[130:137], v[18:25], v[110:113]
	v_mfma_f32_16x16x128_f8f6f4 v[106:109], v[138:145], v[18:25], v[106:109]
	v_mfma_f32_16x16x128_f8f6f4 v[102:105], v[130:137], v[26:33], v[102:105]
	v_mfma_f32_16x16x128_f8f6f4 v[98:101], v[138:145], v[26:33], v[98:101]
	v_mfma_f32_16x16x128_f8f6f4 v[86:89], v[130:137], v[34:41], v[174:177]
	v_mfma_f32_16x16x128_f8f6f4 v[78:81], v[138:145], v[34:41], v[178:181]
	v_mfma_f32_16x16x128_f8f6f4 v[70:73], v[130:137], v[42:49], v[182:185]
	v_mfma_f32_16x16x128_f8f6f4 v[66:69], v[138:145], v[42:49], v[186:189]
	s_barrier
	s_add_u32 s74, s10, s73
	s_addc_u32 s75, s11, 0
	s_add_i32 s72, s72, 0x20080
	s_mov_b32 m0, s43
	v_lshl_add_u64 v[18:19], s[74:75], 0, v[146:147]
	s_add_u32 s72, s10, s72
	ds_read_b128 v[158:161], v153 offset:49152
	ds_read_b128 v[162:165], v153 offset:50176
	ds_read_b128 v[166:169], v153 offset:51200
	ds_read_b128 v[170:173], v153 offset:52224
	ds_read_b128 v[174:177], v153 offset:53248
	ds_read_b128 v[178:181], v153 offset:54272
	ds_read_b128 v[182:185], v153 offset:55296
	ds_read_b128 v[186:189], v153 offset:56320
	global_load_lds_dwordx4 v[18:19], off
	v_lshl_add_u64 v[18:19], s[74:75], 0, v[148:149]
	s_mov_b32 m0, s46
	s_addc_u32 s73, s11, 0
	s_addk_i32 s24, 0x80
	global_load_lds_dwordx4 v[18:19], off
	v_lshl_add_u64 v[18:19], s[72:73], 0, v[146:147]
	s_mov_b32 m0, s49
	s_add_u32 s24, s10, s24
	global_load_lds_dwordx4 v[18:19], off
	v_lshl_add_u64 v[18:19], s[72:73], 0, v[148:149]
	s_mov_b32 m0, s50
	s_addc_u32 s25, s11, 0
	global_load_lds_dwordx4 v[18:19], off
	v_lshl_add_u64 v[18:19], s[24:25], 0, v[146:147]
	s_mov_b32 m0, s47
	s_nop 0
	global_load_lds_dwordx4 v[18:19], off
	v_lshl_add_u64 v[18:19], s[24:25], 0, v[148:149]
	s_mov_b32 m0, s48
	s_nop 0
	global_load_lds_dwordx4 v[18:19], off
	s_waitcnt vmcnt(8)
	s_waitcnt lgkmcnt(0)
	s_barrier
	s_waitcnt lgkmcnt(0)
	v_mfma_f32_16x16x128_f8f6f4 v[62:65], v[2:9], v[158:165], v[62:65]
	v_mfma_f32_16x16x128_f8f6f4 v[58:61], v[10:17], v[158:165], v[58:61]
	v_mfma_f32_16x16x128_f8f6f4 v[50:53], v[2:9], v[166:173], v[50:53]
	v_mfma_f32_16x16x128_f8f6f4 v[42:45], v[10:17], v[166:173], v[190:193]
	v_mfma_f32_16x16x128_f8f6f4 v[34:37], v[2:9], v[174:181], v[194:197]
	v_mfma_f32_16x16x128_f8f6f4 v[26:29], v[10:17], v[174:181], v[198:201]
	v_mfma_f32_16x16x128_f8f6f4 v[18:21], v[2:9], v[182:189], v[202:205]
	v_mfma_f32_16x16x128_f8f6f4 v[10:13], v[10:17], v[182:189], v[222:225]
	v_mfma_f32_16x16x128_f8f6f4 v[54:57], v[130:137], v[158:165], v[54:57]
	v_mfma_f32_16x16x128_f8f6f4 v[46:49], v[138:145], v[158:165], v[226:229]
	v_mfma_f32_16x16x128_f8f6f4 v[38:41], v[130:137], v[166:173], v[230:233]
	v_mfma_f32_16x16x128_f8f6f4 v[30:33], v[138:145], v[166:173], v[234:237]
	v_mfma_f32_16x16x128_f8f6f4 v[22:25], v[130:137], v[174:181], v[238:241]
	v_mfma_f32_16x16x128_f8f6f4 v[14:17], v[138:145], v[174:181], v[242:245]
	v_mfma_f32_16x16x128_f8f6f4 v[6:9], v[130:137], v[182:189], v[246:249]
	v_mfma_f32_16x16x128_f8f6f4 v[2:5], v[138:145], v[182:189], v[250:253]
	s_barrier
	s_add_i32 s70, s70, 2
	s_addk_i32 s71, 0x100
	s_cmp_gt_u32 s70, 5
	s_cbranch_scc0 .LBB0_1450
	s_and_b64 vcc, exec, s[14:15]
	s_cbranch_vccz .LBB0_1453
	s_barrier

; #define PG8_STAGE(bufoff, gbase, voff) do { _Pragma("unroll") for (int _i = 0; _i < 2; ++_i) \
;         __builtin_amdgcn_global_load_lds((const unsigned*)(wsb + (size_t)(gbase) + (voff)[_i]), (LAS unsigned*)(lds + (bufoff) + ldsw + _i * 8192), 16, 0, 0); } while (0)
; #define PG8_LDA(dst, b, h) do { _Pragma("unroll") for (int m = 0; m < 4; ++m) { if constexpr (FP8) dst##8[m] = PG8_LD8(pa, PG8_SA(b, h) + m * 2048); \
;         else { _Pragma("unroll") for (int k = 0; k < 2; ++k) dst[m][k] = *(const LAS bf16x8*)(pa + PG8_SA(b, h) + m * 2048 + k * 1024); } } } while (0)
; #define PG8_LDB(dst, b, h) do { _Pragma("unroll") for (int n = 0; n < 2; ++n) { if constexpr (FP8) dst##8[n] = PG8_LD8(pb, PG8_SA(b, h) + n * 2048); \
;         else { _Pragma("unroll") for (int k = 0; k < 2; ++k) dst[n][k] = *(const LAS bf16x8*)(pb + PG8_SA(b, h) + n * 2048 + k * 1024); } } } while (0)
; #define PG8_WAIT_V(n) asm volatile("s_waitcnt vmcnt(" #n ")" ::: "memory")
; #define PG8_WAIT_L(n) asm volatile("s_waitcnt lgkmcnt(" #n ")" ::: "memory")
; #define PG8_BAR __builtin_amdgcn_s_barrier()
; #define PG8_SCHED __builtin_amdgcn_sched_barrier(0)
; template <class Epi, class Sched, bool PERM, bool FP8 = false, bool GATHER = false>
; DI void gemm_phase(LAS unsigned char* lds, const unsigned char* wsb, const unsigned lda, const unsigned ldb, const int nt, const Sched& S, const Epi& E) {
;     ...
;             PG8_LDB(B0, 0, 0); PG8_LDB(B1, 0, 1); PG8_SCHED; PG8_LDA(At, 0, 0); PG8_STAGEA(PG8_SA(1, 1), t + 1, 1, false);
;             if constexpr (GATHER) { if (last) {
;                 int tz = tid; asm volatile("" : "+v"(tz));
; #pragma unroll
;                 for (int i = 0; i < 2; ++i) { int R, C; stage_rc(tz * 16 + i * 8192, R, C);
; #pragma unroll
;                     for (int h = 0; h < 2; ++h) { const unsigned tk = (unsigned)tokt[h * HALF + R]; offC[h][i] = (tk < (unsigned)NTOK ? tk : (unsigned)(NTOK - 1)) * lda + (unsigned)C * 2u; } } } }
;             PG8_WAIT_V(8); PG8_WAIT_L(0); PG8_BAR; PG8_MMA(0, 0, At, B0); PG8_MMA(0, 1, At, B1); PG8_BAR; PG8_SCHED;
;             PG8_LDA(At, 0, 1); PG8_STAGE(PG8_SB(0, 0), b2, voffB); PG8_STAGE(PG8_SB(0, 1), b2 + hstepB, voffB); PG8_STAGEA(PG8_SA(0, 0), k2, 0, last);
;             PG8_WAIT_V(8); PG8_WAIT_L(0); PG8_BAR; PG8_MMA(1, 0, At, B0); PG8_MMA(1, 1, At, B1); PG8_BAR; PG8_SCHED;
.LBB0_1626:
	ds_read_b128 v[130:133], v186
	ds_read_b128 v[134:137], v186 offset:1024
	ds_read_b128 v[138:141], v186 offset:2048
	ds_read_b128 v[142:145], v186 offset:3072
	ds_read_b128 v[146:149], v186 offset:16384
	ds_read_b128 v[150:153], v186 offset:17408
	ds_read_b128 v[160:163], v186 offset:18432
	ds_read_b128 v[164:167], v186 offset:19456
	s_add_i32 s53, s7, 0xfffe0080
	s_cmp_eq_u32 s8, 4
	s_cselect_b32 s9, s50, s6
	s_cselect_b32 s53, s49, s53
	s_add_i32 s58, s9, 0x80
	s_add_u32 s60, s12, s7
	s_addc_u32 s61, s13, 0
	v_lshl_add_u64 v[206:207], s[60:61], 0, v[154:155]
	s_add_i32 m0, s69, 0xc000
	ds_read_b128 v[168:171], v185
	ds_read_b128 v[172:175], v185 offset:1024
	ds_read_b128 v[176:179], v185 offset:2048
	ds_read_b128 v[180:183], v185 offset:3072
	ds_read_b128 v[190:193], v185 offset:4096
	ds_read_b128 v[194:197], v185 offset:5120
	ds_read_b128 v[198:201], v185 offset:6144
	ds_read_b128 v[202:205], v185 offset:7168
	global_load_lds_dwordx4 v[206:207], off
	v_lshl_add_u64 v[206:207], s[60:61], 0, v[156:157]
	s_add_i32 m0, s69, 0xe000
	s_nop 0
	global_load_lds_dwordx4 v[206:207], off
	s_waitcnt vmcnt(8)
	s_waitcnt lgkmcnt(0)
	s_barrier
	s_waitcnt lgkmcnt(0)
	v_mfma_f32_16x16x128_f8f6f4 v[126:129], v[130:137], v[168:175], v[126:129]
	v_mfma_f32_16x16x128_f8f6f4 v[122:125], v[138:145], v[168:175], v[122:125]
	v_mfma_f32_16x16x128_f8f6f4 v[110:113], v[130:137], v[176:183], v[110:113]
	v_mfma_f32_16x16x128_f8f6f4 v[106:109], v[138:145], v[176:183], v[106:109]
	v_mfma_f32_16x16x128_f8f6f4 v[206:209], v[130:137], v[190:197], v[94:97]
	v_mfma_f32_16x16x128_f8f6f4 v[210:213], v[138:145], v[190:197], v[90:93]
	v_mfma_f32_16x16x128_f8f6f4 v[214:217], v[130:137], v[198:205], v[78:81]
	v_mfma_f32_16x16x128_f8f6f4 v[218:221], v[138:145], v[198:205], v[74:77]
	v_mfma_f32_16x16x128_f8f6f4 v[118:121], v[146:153], v[168:175], v[118:121]
	v_mfma_f32_16x16x128_f8f6f4 v[114:117], v[160:167], v[168:175], v[114:117]
	v_mfma_f32_16x16x128_f8f6f4 v[102:105], v[146:153], v[176:183], v[102:105]
	v_mfma_f32_16x16x128_f8f6f4 v[98:101], v[160:167], v[176:183], v[98:101]
	v_mfma_f32_16x16x128_f8f6f4 v[168:171], v[146:153], v[190:197], v[86:89]
	v_mfma_f32_16x16x128_f8f6f4 v[172:175], v[160:167], v[190:197], v[82:85]
	v_mfma_f32_16x16x128_f8f6f4 v[176:179], v[146:153], v[198:205], v[70:73]
	v_mfma_f32_16x16x128_f8f6f4 v[180:183], v[160:167], v[198:205], v[66:69]
	s_barrier
	s_add_u32 s60, s12, s9
	s_addc_u32 s61, s13, 0
	s_mov_b32 m0, s70
	v_lshl_add_u64 v[190:191], s[60:61], 0, v[154:155]
	s_add_i32 s59, s9, 0x20000
	ds_read_b128 v[66:69], v185 offset:16384
	ds_read_b128 v[70:73], v185 offset:17408
	ds_read_b128 v[74:77], v185 offset:18432
	ds_read_b128 v[78:81], v185 offset:19456
	ds_read_b128 v[82:85], v185 offset:20480
	ds_read_b128 v[86:89], v185 offset:21504
	ds_read_b128 v[90:93], v185 offset:22528
	ds_read_b128 v[94:97], v185 offset:23552
	global_load_lds_dwordx4 v[190:191], off
	v_lshl_add_u64 v[190:191], s[60:61], 0, v[156:157]
	s_add_u32 s60, s12, s59
	s_mov_b32 m0, s71
	s_addc_u32 s61, s13, 0
	global_load_lds_dwordx4 v[190:191], off
	v_lshl_add_u64 v[190:191], s[60:61], 0, v[154:155]
	s_mov_b32 m0, s72
	s_nop 0
	global_load_lds_dwordx4 v[190:191], off
	v_lshl_add_u64 v[190:191], s[60:61], 0, v[156:157]
	s_add_u32 s60, s12, s53
	s_mov_b32 m0, s73
	s_addc_u32 s61, s13, 0
	global_load_lds_dwordx4 v[190:191], off
	v_lshl_add_u64 v[190:191], s[60:61], 0, v[154:155]
	s_mov_b32 m0, s69
	s_nop 0
	global_load_lds_dwordx4 v[190:191], off
	v_lshl_add_u64 v[190:191], s[60:61], 0, v[156:157]
	s_mov_b32 m0, s74
	s_nop 0
	global_load_lds_dwordx4 v[190:191], off
	s_waitcnt vmcnt(8)
	s_waitcnt lgkmcnt(0)
	s_barrier
	s_waitcnt lgkmcnt(0)
	v_mfma_f32_16x16x128_f8f6f4 v[62:65], v[130:137], v[66:73], v[62:65]
	v_mfma_f32_16x16x128_f8f6f4 v[58:61], v[138:145], v[66:73], v[58:61]
	v_mfma_f32_16x16x128_f8f6f4 v[190:193], v[130:137], v[74:81], v[46:49]
	v_mfma_f32_16x16x128_f8f6f4 v[194:197], v[138:145], v[74:81], v[42:45]
	v_mfma_f32_16x16x128_f8f6f4 v[198:201], v[130:137], v[82:89], v[30:33]
	v_mfma_f32_16x16x128_f8f6f4 v[202:205], v[138:145], v[82:89], v[26:29]
	v_mfma_f32_16x16x128_f8f6f4 v[222:225], v[130:137], v[90:97], v[14:17]
	v_mfma_f32_16x16x128_f8f6f4 v[226:229], v[138:145], v[90:97], v[10:13]
	v_mfma_f32_16x16x128_f8f6f4 v[54:57], v[146:153], v[66:73], v[54:57]
	v_mfma_f32_16x16x128_f8f6f4 v[50:53], v[160:167], v[66:73], v[50:53]
	v_mfma_f32_16x16x128_f8f6f4 v[230:233], v[146:153], v[74:81], v[38:41]
	v_mfma_f32_16x16x128_f8f6f4 v[234:237], v[160:167], v[74:81], v[34:37]
	v_mfma_f32_16x16x128_f8f6f4 v[238:241], v[146:153], v[82:89], v[22:25]
	v_mfma_f32_16x16x128_f8f6f4 v[242:245], v[160:167], v[82:89], v[18:21]
	v_mfma_f32_16x16x128_f8f6f4 v[246:249], v[146:153], v[90:97], v[6:9]
	v_mfma_f32_16x16x128_f8f6f4 v[250:253], v[160:167], v[90:97], v[2:5]
	s_barrier
; #define PG8_STAGE(bufoff, gbase, voff) do { _Pragma("unroll") for (int _i = 0; _i < 2; ++_i) \
;         __builtin_amdgcn_global_load_lds((const unsigned*)(wsb + (size_t)(gbase) + (voff)[_i]), (LAS unsigned*)(lds + (bufoff) + ldsw + _i * 8192), 16, 0, 0); } while (0)
; #define PG8_LDA(dst, b, h) do { _Pragma("unroll") for (int m = 0; m < 4; ++m) { if constexpr (FP8) dst##8[m] = PG8_LD8(pa, PG8_SA(b, h) + m * 2048); \
;         else { _Pragma("unroll") for (int k = 0; k < 2; ++k) dst[m][k] = *(const LAS bf16x8*)(pa + PG8_SA(b, h) + m * 2048 + k * 1024); } } } while (0)
; #define PG8_LDB(dst, b, h) do { _Pragma("unroll") for (int n = 0; n < 2; ++n) { if constexpr (FP8) dst##8[n] = PG8_LD8(pb, PG8_SA(b, h) + n * 2048); \
;         else { _Pragma("unroll") for (int k = 0; k < 2; ++k) dst[n][k] = *(const LAS bf16x8*)(pb + PG8_SA(b, h) + n * 2048 + k * 1024); } } } while (0)
; #define PG8_WAIT_V(n) asm volatile("s_waitcnt vmcnt(" #n ")" ::: "memory")
; #define PG8_WAIT_L(n) asm volatile("s_waitcnt lgkmcnt(" #n ")" ::: "memory")
; #define PG8_BAR __builtin_amdgcn_s_barrier()
; #define PG8_SCHED __builtin_amdgcn_sched_barrier(0)
; template <class Epi, class Sched, bool PERM, bool FP8 = false, bool GATHER = false>
; DI void gemm_phase(LAS unsigned char* lds, const unsigned char* wsb, const unsigned lda, const unsigned ldb, const int nt, const Sched& S, const Epi& E) {
;     ...
;             PG8_LDB(B0, 1, 0); PG8_LDB(B1, 1, 1); PG8_SCHED; PG8_LDA(At, 1, 0); PG8_STAGEA(PG8_SA(0, 1), k2, 1, last);
;             PG8_WAIT_V(8); PG8_WAIT_L(0); PG8_BAR; PG8_MMA(0, 0, At, B0); PG8_MMA(0, 1, At, B1); PG8_BAR; PG8_SCHED;
;             PG8_LDA(At, 1, 1); PG8_STAGE(PG8_SB(1, 0), b3, voffB); PG8_STAGE(PG8_SB(1, 1), b3 + hstepB, voffB); PG8_STAGEA(PG8_SA(1, 0), k3, 0, last);
;             PG8_WAIT_V(8); PG8_WAIT_L(0); PG8_BAR; PG8_MMA(1, 0, At, B0); PG8_MMA(1, 1, At, B1); PG8_BAR; PG8_SCHED;
;         }
;         if (wr == 0) PG8_BAR;
	s_nop 4
	ds_read_b128 v[2:5], v186 offset:32768
	ds_read_b128 v[6:9], v186 offset:33792
	ds_read_b128 v[18:21], v186 offset:34816
	ds_read_b128 v[22:25], v186 offset:35840
	ds_read_b128 v[130:133], v186 offset:49152
	ds_read_b128 v[134:137], v186 offset:50176
	ds_read_b128 v[138:141], v186 offset:51200
	ds_read_b128 v[142:145], v186 offset:52224
	s_add_i32 s59, s53, 0x20000
	s_add_u32 s60, s12, s59
	s_addc_u32 s61, s13, 0
	s_mov_b32 m0, s75
	v_lshl_add_u64 v[66:67], s[60:61], 0, v[154:155]
	ds_read_b128 v[10:13], v185 offset:32768
	ds_read_b128 v[14:17], v185 offset:33792
	ds_read_b128 v[26:29], v185 offset:34816
	ds_read_b128 v[30:33], v185 offset:35840
	ds_read_b128 v[34:37], v185 offset:36864
	ds_read_b128 v[38:41], v185 offset:37888
	ds_read_b128 v[42:45], v185 offset:38912
	ds_read_b128 v[46:49], v185 offset:39936
	global_load_lds_dwordx4 v[66:67], off
	v_lshl_add_u64 v[66:67], s[60:61], 0, v[156:157]
	s_mov_b32 m0, s76
	s_nop 0
	global_load_lds_dwordx4 v[66:67], off
	s_waitcnt vmcnt(8)
	s_waitcnt lgkmcnt(0)
	s_barrier
	s_waitcnt lgkmcnt(0)
	v_mfma_f32_16x16x128_f8f6f4 v[126:129], v[2:9], v[10:17], v[126:129]
	v_mfma_f32_16x16x128_f8f6f4 v[122:125], v[18:25], v[10:17], v[122:125]
	v_mfma_f32_16x16x128_f8f6f4 v[110:113], v[2:9], v[26:33], v[110:113]
	v_mfma_f32_16x16x128_f8f6f4 v[106:109], v[18:25], v[26:33], v[106:109]
	v_mfma_f32_16x16x128_f8f6f4 v[94:97], v[2:9], v[34:41], v[206:209]
	v_mfma_f32_16x16x128_f8f6f4 v[90:93], v[18:25], v[34:41], v[210:213]
	v_mfma_f32_16x16x128_f8f6f4 v[78:81], v[2:9], v[42:49], v[214:217]
	v_mfma_f32_16x16x128_f8f6f4 v[74:77], v[18:25], v[42:49], v[218:221]
	v_mfma_f32_16x16x128_f8f6f4 v[118:121], v[130:137], v[10:17], v[118:121]
	v_mfma_f32_16x16x128_f8f6f4 v[114:117], v[138:145], v[10:17], v[114:117]
	v_mfma_f32_16x16x128_f8f6f4 v[102:105], v[130:137], v[26:33], v[102:105]
	v_mfma_f32_16x16x128_f8f6f4 v[98:101], v[138:145], v[26:33], v[98:101]
	v_mfma_f32_16x16x128_f8f6f4 v[86:89], v[130:137], v[34:41], v[168:171]
	v_mfma_f32_16x16x128_f8f6f4 v[82:85], v[138:145], v[34:41], v[172:175]
	v_mfma_f32_16x16x128_f8f6f4 v[70:73], v[130:137], v[42:49], v[176:179]
	v_mfma_f32_16x16x128_f8f6f4 v[66:69], v[138:145], v[42:49], v[180:183]
	s_barrier
	s_add_u32 s58, s12, s58
	s_addc_u32 s59, s13, 0
	s_mov_b32 m0, s85
	v_lshl_add_u64 v[10:11], s[58:59], 0, v[154:155]
	s_add_i32 s9, s9, 0x20080
	ds_read_b128 v[34:37], v185 offset:49152
	ds_read_b128 v[38:41], v185 offset:50176
	ds_read_b128 v[146:149], v185 offset:51200
	ds_read_b128 v[150:153], v185 offset:52224
	ds_read_b128 v[160:163], v185 offset:53248
	ds_read_b128 v[164:167], v185 offset:54272
	ds_read_b128 v[168:171], v185 offset:55296
	ds_read_b128 v[172:175], v185 offset:56320
	global_load_lds_dwordx4 v[10:11], off
	v_lshl_add_u64 v[10:11], s[58:59], 0, v[156:157]
	s_add_u32 s58, s12, s9
	s_mov_b32 m0, s86
	s_addc_u32 s59, s13, 0
	global_load_lds_dwordx4 v[10:11], off
	v_lshl_add_u64 v[10:11], s[58:59], 0, v[154:155]
	s_mov_b32 m0, s89
	s_addk_i32 s53, 0x80
	global_load_lds_dwordx4 v[10:11], off
	v_lshl_add_u64 v[10:11], s[58:59], 0, v[156:157]
	s_add_u32 s58, s12, s53
	s_mov_b32 m0, s90
	s_addc_u32 s59, s13, 0
	global_load_lds_dwordx4 v[10:11], off
	v_lshl_add_u64 v[10:11], s[58:59], 0, v[154:155]
	s_mov_b32 m0, s87
	s_nop 0
	global_load_lds_dwordx4 v[10:11], off
	v_lshl_add_u64 v[10:11], s[58:59], 0, v[156:157]
	s_mov_b32 m0, s88
	s_nop 0
	global_load_lds_dwordx4 v[10:11], off
	s_waitcnt vmcnt(8)
	s_waitcnt lgkmcnt(0)
	s_barrier
	s_waitcnt lgkmcnt(0)
	v_mfma_f32_16x16x128_f8f6f4 v[62:65], v[2:9], v[34:41], v[62:65]
	v_mfma_f32_16x16x128_f8f6f4 v[58:61], v[18:25], v[34:41], v[58:61]
	v_mfma_f32_16x16x128_f8f6f4 v[46:49], v[2:9], v[146:153], v[190:193]
	v_mfma_f32_16x16x128_f8f6f4 v[42:45], v[18:25], v[146:153], v[194:197]
	v_mfma_f32_16x16x128_f8f6f4 v[30:33], v[2:9], v[160:167], v[198:201]
	v_mfma_f32_16x16x128_f8f6f4 v[26:29], v[18:25], v[160:167], v[202:205]
	v_mfma_f32_16x16x128_f8f6f4 v[14:17], v[2:9], v[168:175], v[222:225]
	v_mfma_f32_16x16x128_f8f6f4 v[10:13], v[18:25], v[168:175], v[226:229]
	v_mfma_f32_16x16x128_f8f6f4 v[54:57], v[130:137], v[34:41], v[54:57]
	v_mfma_f32_16x16x128_f8f6f4 v[50:53], v[138:145], v[34:41], v[50:53]
	v_mfma_f32_16x16x128_f8f6f4 v[38:41], v[130:137], v[146:153], v[230:233]
	v_mfma_f32_16x16x128_f8f6f4 v[34:37], v[138:145], v[146:153], v[234:237]
	v_mfma_f32_16x16x128_f8f6f4 v[22:25], v[130:137], v[160:167], v[238:241]
	v_mfma_f32_16x16x128_f8f6f4 v[18:21], v[138:145], v[160:167], v[242:245]
	v_mfma_f32_16x16x128_f8f6f4 v[6:9], v[130:137], v[168:175], v[246:249]
	v_mfma_f32_16x16x128_f8f6f4 v[2:5], v[138:145], v[168:175], v[250:253]
	s_barrier
	s_add_i32 s8, s8, 2
	s_addk_i32 s7, 0x100
	s_addk_i32 s6, 0x100
	s_cmp_gt_u32 s8, 5
	s_cbranch_scc0 .LBB0_1626
	s_and_b64 vcc, exec, s[16:17]
	s_cbranch_vccz .LBB0_1629
	s_barrier

; #define PG8_STAGE(bufoff, gbase, voff) do { _Pragma("unroll") for (int _i = 0; _i < 2; ++_i) \
;         __builtin_amdgcn_global_load_lds((const unsigned*)(wsb + (size_t)(gbase) + (voff)[_i]), (LAS unsigned*)(lds + (bufoff) + ldsw + _i * 8192), 16, 0, 0); } while (0)
; #define PG8_LDA(dst, b, h) do { _Pragma("unroll") for (int m = 0; m < 4; ++m) { if constexpr (FP8) dst##8[m] = PG8_LD8(pa, PG8_SA(b, h) + m * 2048); \
;         else { _Pragma("unroll") for (int k = 0; k < 2; ++k) dst[m][k] = *(const LAS bf16x8*)(pa + PG8_SA(b, h) + m * 2048 + k * 1024); } } } while (0)
; #define PG8_LDB(dst, b, h) do { _Pragma("unroll") for (int n = 0; n < 2; ++n) { if constexpr (FP8) dst##8[n] = PG8_LD8(pb, PG8_SA(b, h) + n * 2048); \
;         else { _Pragma("unroll") for (int k = 0; k < 2; ++k) dst[n][k] = *(const LAS bf16x8*)(pb + PG8_SA(b, h) + n * 2048 + k * 1024); } } } while (0)
; #define PG8_WAIT_V(n) asm volatile("s_waitcnt vmcnt(" #n ")" ::: "memory")
; #define PG8_WAIT_L(n) asm volatile("s_waitcnt lgkmcnt(" #n ")" ::: "memory")
; #define PG8_BAR __builtin_amdgcn_s_barrier()
; #define PG8_SCHED __builtin_amdgcn_sched_barrier(0)
; template <class Epi, class Sched, bool PERM, bool FP8 = false, bool GATHER = false>
; DI void gemm_phase(LAS unsigned char* lds, const unsigned char* wsb, const unsigned lda, const unsigned ldb, const int nt, const Sched& S, const Epi& E) {
;     ...
;             PG8_LDB(B0, 0, 0); PG8_LDB(B1, 0, 1); PG8_SCHED; PG8_LDA(At, 0, 0); PG8_STAGEA(PG8_SA(1, 1), t + 1, 1, false);
;             if constexpr (GATHER) { if (last) {
;                 int tz = tid; asm volatile("" : "+v"(tz));
; #pragma unroll
;                 for (int i = 0; i < 2; ++i) { int R, C; stage_rc(tz * 16 + i * 8192, R, C);
; #pragma unroll
;                     for (int h = 0; h < 2; ++h) { const unsigned tk = (unsigned)tokt[h * HALF + R]; offC[h][i] = (tk < (unsigned)NTOK ? tk : (unsigned)(NTOK - 1)) * lda + (unsigned)C * 2u; } } } }
;             PG8_WAIT_V(8); PG8_WAIT_L(0); PG8_BAR; PG8_MMA(0, 0, At, B0); PG8_MMA(0, 1, At, B1); PG8_BAR; PG8_SCHED;
;             PG8_LDA(At, 0, 1); PG8_STAGE(PG8_SB(0, 0), b2, voffB); PG8_STAGE(PG8_SB(0, 1), b2 + hstepB, voffB); PG8_STAGEA(PG8_SA(0, 0), k2, 0, last);
;             PG8_WAIT_V(8); PG8_WAIT_L(0); PG8_BAR; PG8_MMA(1, 0, At, B0); PG8_MMA(1, 1, At, B1); PG8_BAR; PG8_SCHED;
.LBB0_1802:
	ds_read_b128 v[144:147], v142
	ds_read_b128 v[148:151], v142 offset:1024
	ds_read_b128 v[152:155], v142 offset:2048
	ds_read_b128 v[156:159], v142 offset:3072
	ds_read_b128 v[160:163], v142 offset:16384
	ds_read_b128 v[164:167], v142 offset:17408
	ds_read_b128 v[168:171], v142 offset:18432
	ds_read_b128 v[172:175], v142 offset:19456
	s_add_i32 s24, s20, 0xfffe0080
	s_cmp_eq_u32 s21, 4
	s_cselect_b32 s22, s72, s8
	s_cselect_b32 s24, s71, s24
	s_add_i32 s36, s22, 0x80
	s_add_u32 s38, s6, s20
	s_addc_u32 s39, s7, 0
	s_mov_b32 m0, s65
	v_lshl_add_u64 v[130:131], s[38:39], 0, v[138:139]
	ds_read_b128 v[176:179], v141
	ds_read_b128 v[180:183], v141 offset:1024
	ds_read_b128 v[184:187], v141 offset:2048
	ds_read_b128 v[188:191], v141 offset:3072
	ds_read_b128 v[192:195], v141 offset:4096
	ds_read_b128 v[196:199], v141 offset:5120
	ds_read_b128 v[200:203], v141 offset:6144
	ds_read_b128 v[204:207], v141 offset:7168
	global_load_lds_dwordx4 v[130:131], off
	v_lshl_add_u64 v[130:131], s[38:39], 0, v[134:135]
	s_mov_b32 m0, s66
	s_nop 0
	global_load_lds_dwordx4 v[130:131], off
	s_waitcnt vmcnt(8)
	s_waitcnt lgkmcnt(0)
	s_barrier
	s_waitcnt lgkmcnt(0)
	v_mfma_f32_16x16x128_f8f6f4 v[126:129], v[144:151], v[176:183], v[126:129]
	v_mfma_f32_16x16x128_f8f6f4 v[122:125], v[152:159], v[176:183], v[122:125]
	v_mfma_f32_16x16x128_f8f6f4 v[114:117], v[144:151], v[184:191], v[114:117]
	v_mfma_f32_16x16x128_f8f6f4 v[106:109], v[152:159], v[184:191], v[106:109]
	v_mfma_f32_16x16x128_f8f6f4 v[98:101], v[144:151], v[192:199], v[98:101]
	v_mfma_f32_16x16x128_f8f6f4 v[208:211], v[152:159], v[192:199], v[90:93]
	v_mfma_f32_16x16x128_f8f6f4 v[212:215], v[144:151], v[200:207], v[82:85]
	v_mfma_f32_16x16x128_f8f6f4 v[216:219], v[152:159], v[200:207], v[74:77]
	v_mfma_f32_16x16x128_f8f6f4 v[118:121], v[160:167], v[176:183], v[118:121]
	v_mfma_f32_16x16x128_f8f6f4 v[110:113], v[168:175], v[176:183], v[110:113]
	v_mfma_f32_16x16x128_f8f6f4 v[102:105], v[160:167], v[184:191], v[102:105]
	v_mfma_f32_16x16x128_f8f6f4 v[176:179], v[168:175], v[184:191], v[94:97]
	v_mfma_f32_16x16x128_f8f6f4 v[180:183], v[160:167], v[192:199], v[86:89]
	v_mfma_f32_16x16x128_f8f6f4 v[184:187], v[168:175], v[192:199], v[78:81]
	v_mfma_f32_16x16x128_f8f6f4 v[188:191], v[160:167], v[200:207], v[70:73]
	v_mfma_f32_16x16x128_f8f6f4 v[192:195], v[168:175], v[200:207], v[66:69]
	s_barrier
	s_add_u32 s38, s6, s22
	s_addc_u32 s39, s7, 0
	s_mov_b32 m0, s28
	v_lshl_add_u64 v[130:131], s[38:39], 0, v[252:253]
	s_add_i32 s37, s22, 0x20000
	ds_read_b128 v[66:69], v141 offset:16384
	ds_read_b128 v[70:73], v141 offset:17408
	ds_read_b128 v[74:77], v141 offset:18432
	ds_read_b128 v[78:81], v141 offset:19456
	ds_read_b128 v[82:85], v141 offset:20480
	ds_read_b128 v[86:89], v141 offset:21504
	ds_read_b128 v[90:93], v141 offset:22528
	ds_read_b128 v[94:97], v141 offset:23552
	global_load_lds_dwordx4 v[130:131], off
	v_lshl_add_u64 v[130:131], s[38:39], 0, v[136:137]
	s_add_u32 s38, s6, s37
	s_mov_b32 m0, s29
	s_addc_u32 s39, s7, 0
	global_load_lds_dwordx4 v[130:131], off
	v_lshl_add_u64 v[130:131], s[38:39], 0, v[252:253]
	s_mov_b32 m0, s42
	s_nop 0
	global_load_lds_dwordx4 v[130:131], off
	v_lshl_add_u64 v[130:131], s[38:39], 0, v[136:137]
	s_add_u32 s38, s6, s24
	s_mov_b32 m0, s43
	s_addc_u32 s39, s7, 0
	global_load_lds_dwordx4 v[130:131], off
	v_lshl_add_u64 v[130:131], s[38:39], 0, v[138:139]
	s_mov_b32 m0, s17
	s_nop 0
	global_load_lds_dwordx4 v[130:131], off
	v_lshl_add_u64 v[130:131], s[38:39], 0, v[134:135]
	s_mov_b32 m0, s46
	s_nop 0
	global_load_lds_dwordx4 v[130:131], off
	s_waitcnt vmcnt(8)
	s_waitcnt lgkmcnt(0)
	s_barrier
	s_waitcnt lgkmcnt(0)
	v_mfma_f32_16x16x128_f8f6f4 v[62:65], v[144:151], v[66:73], v[62:65]
	v_mfma_f32_16x16x128_f8f6f4 v[58:61], v[152:159], v[66:73], v[58:61]
	v_mfma_f32_16x16x128_f8f6f4 v[50:53], v[144:151], v[74:81], v[50:53]
	v_mfma_f32_16x16x128_f8f6f4 v[196:199], v[152:159], v[74:81], v[42:45]
	v_mfma_f32_16x16x128_f8f6f4 v[200:203], v[144:151], v[82:89], v[34:37]
	v_mfma_f32_16x16x128_f8f6f4 v[204:207], v[152:159], v[82:89], v[26:29]
	v_mfma_f32_16x16x128_f8f6f4 v[220:223], v[144:151], v[90:97], v[18:21]
	v_mfma_f32_16x16x128_f8f6f4 v[224:227], v[152:159], v[90:97], v[10:13]
	v_mfma_f32_16x16x128_f8f6f4 v[54:57], v[160:167], v[66:73], v[54:57]
	v_mfma_f32_16x16x128_f8f6f4 v[228:231], v[168:175], v[66:73], v[46:49]
	v_mfma_f32_16x16x128_f8f6f4 v[232:235], v[160:167], v[74:81], v[38:41]
	v_mfma_f32_16x16x128_f8f6f4 v[236:239], v[168:175], v[74:81], v[30:33]
	v_mfma_f32_16x16x128_f8f6f4 v[240:243], v[160:167], v[82:89], v[22:25]
	v_mfma_f32_16x16x128_f8f6f4 v[244:247], v[168:175], v[82:89], v[14:17]
	v_mfma_f32_16x16x128_f8f6f4 v[248:251], v[160:167], v[90:97], v[6:9]
	v_mfma_f32_16x16x128_f8f6f4 v[130:133], v[168:175], v[90:97], v[2:5]
	s_barrier
; #define PG8_STAGE(bufoff, gbase, voff) do { _Pragma("unroll") for (int _i = 0; _i < 2; ++_i) \
;         __builtin_amdgcn_global_load_lds((const unsigned*)(wsb + (size_t)(gbase) + (voff)[_i]), (LAS unsigned*)(lds + (bufoff) + ldsw + _i * 8192), 16, 0, 0); } while (0)
; #define PG8_LDA(dst, b, h) do { _Pragma("unroll") for (int m = 0; m < 4; ++m) { if constexpr (FP8) dst##8[m] = PG8_LD8(pa, PG8_SA(b, h) + m * 2048); \
;         else { _Pragma("unroll") for (int k = 0; k < 2; ++k) dst[m][k] = *(const LAS bf16x8*)(pa + PG8_SA(b, h) + m * 2048 + k * 1024); } } } while (0)
; #define PG8_LDB(dst, b, h) do { _Pragma("unroll") for (int n = 0; n < 2; ++n) { if constexpr (FP8) dst##8[n] = PG8_LD8(pb, PG8_SA(b, h) + n * 2048); \
;         else { _Pragma("unroll") for (int k = 0; k < 2; ++k) dst[n][k] = *(const LAS bf16x8*)(pb + PG8_SA(b, h) + n * 2048 + k * 1024); } } } while (0)
; #define PG8_WAIT_V(n) asm volatile("s_waitcnt vmcnt(" #n ")" ::: "memory")
; #define PG8_WAIT_L(n) asm volatile("s_waitcnt lgkmcnt(" #n ")" ::: "memory")
; #define PG8_BAR __builtin_amdgcn_s_barrier()
; #define PG8_SCHED __builtin_amdgcn_sched_barrier(0)
; template <class Epi, class Sched, bool PERM, bool FP8 = false, bool GATHER = false>
; DI void gemm_phase(LAS unsigned char* lds, const unsigned char* wsb, const unsigned lda, const unsigned ldb, const int nt, const Sched& S, const Epi& E) {
;     ...
;             PG8_LDB(B0, 1, 0); PG8_LDB(B1, 1, 1); PG8_SCHED; PG8_LDA(At, 1, 0); PG8_STAGEA(PG8_SA(0, 1), k2, 1, last);
;             PG8_WAIT_V(8); PG8_WAIT_L(0); PG8_BAR; PG8_MMA(0, 0, At, B0); PG8_MMA(0, 1, At, B1); PG8_BAR; PG8_SCHED;
;             PG8_LDA(At, 1, 1); PG8_STAGE(PG8_SB(1, 0), b3, voffB); PG8_STAGE(PG8_SB(1, 1), b3 + hstepB, voffB); PG8_STAGEA(PG8_SA(1, 0), k3, 0, last);
;             PG8_WAIT_V(8); PG8_WAIT_L(0); PG8_BAR; PG8_MMA(1, 0, At, B0); PG8_MMA(1, 1, At, B1); PG8_BAR; PG8_SCHED;
;         }
;         if (wr == 0) PG8_BAR;
	s_nop 4
	ds_read_b128 v[2:5], v142 offset:32768
	ds_read_b128 v[6:9], v142 offset:33792
	ds_read_b128 v[10:13], v142 offset:34816
	ds_read_b128 v[14:17], v142 offset:35840
	ds_read_b128 v[144:147], v142 offset:49152
	ds_read_b128 v[148:151], v142 offset:50176
	ds_read_b128 v[152:155], v142 offset:51200
	ds_read_b128 v[156:159], v142 offset:52224
	s_add_i32 s37, s24, 0x20000
	s_add_u32 s38, s6, s37
	s_addc_u32 s39, s7, 0
	s_mov_b32 m0, s47
	v_lshl_add_u64 v[66:67], s[38:39], 0, v[138:139]
	ds_read_b128 v[18:21], v141 offset:32768
	ds_read_b128 v[22:25], v141 offset:33792
	ds_read_b128 v[26:29], v141 offset:34816
	ds_read_b128 v[30:33], v141 offset:35840
	ds_read_b128 v[34:37], v141 offset:36864
	ds_read_b128 v[38:41], v141 offset:37888
	ds_read_b128 v[42:45], v141 offset:38912
	ds_read_b128 v[46:49], v141 offset:39936
	global_load_lds_dwordx4 v[66:67], off
	v_lshl_add_u64 v[66:67], s[38:39], 0, v[134:135]
	s_mov_b32 m0, s48
	s_nop 0
	global_load_lds_dwordx4 v[66:67], off
	s_waitcnt vmcnt(8)
	s_waitcnt lgkmcnt(0)
	s_barrier
	s_waitcnt lgkmcnt(0)
	v_mfma_f32_16x16x128_f8f6f4 v[126:129], v[2:9], v[18:25], v[126:129]
	v_mfma_f32_16x16x128_f8f6f4 v[122:125], v[10:17], v[18:25], v[122:125]
	v_mfma_f32_16x16x128_f8f6f4 v[114:117], v[2:9], v[26:33], v[114:117]
	v_mfma_f32_16x16x128_f8f6f4 v[106:109], v[10:17], v[26:33], v[106:109]
	v_mfma_f32_16x16x128_f8f6f4 v[98:101], v[2:9], v[34:41], v[98:101]
	v_mfma_f32_16x16x128_f8f6f4 v[90:93], v[10:17], v[34:41], v[208:211]
	v_mfma_f32_16x16x128_f8f6f4 v[82:85], v[2:9], v[42:49], v[212:215]
	v_mfma_f32_16x16x128_f8f6f4 v[74:77], v[10:17], v[42:49], v[216:219]
	v_mfma_f32_16x16x128_f8f6f4 v[118:121], v[144:151], v[18:25], v[118:121]
	v_mfma_f32_16x16x128_f8f6f4 v[110:113], v[152:159], v[18:25], v[110:113]
	v_mfma_f32_16x16x128_f8f6f4 v[102:105], v[144:151], v[26:33], v[102:105]
	v_mfma_f32_16x16x128_f8f6f4 v[94:97], v[152:159], v[26:33], v[176:179]
	v_mfma_f32_16x16x128_f8f6f4 v[86:89], v[144:151], v[34:41], v[180:183]
	v_mfma_f32_16x16x128_f8f6f4 v[78:81], v[152:159], v[34:41], v[184:187]
	v_mfma_f32_16x16x128_f8f6f4 v[70:73], v[144:151], v[42:49], v[188:191]
	v_mfma_f32_16x16x128_f8f6f4 v[66:69], v[152:159], v[42:49], v[192:195]
	s_barrier
	s_add_u32 s36, s6, s36
	s_addc_u32 s37, s7, 0
	s_mov_b32 m0, s50
	v_lshl_add_u64 v[18:19], s[36:37], 0, v[252:253]
	s_add_i32 s22, s22, 0x20080
	ds_read_b128 v[160:163], v141 offset:49152
	ds_read_b128 v[164:167], v141 offset:50176
	ds_read_b128 v[168:171], v141 offset:51200
	ds_read_b128 v[172:175], v141 offset:52224
	ds_read_b128 v[176:179], v141 offset:53248
	ds_read_b128 v[180:183], v141 offset:54272
	ds_read_b128 v[184:187], v141 offset:55296
	ds_read_b128 v[188:191], v141 offset:56320
	global_load_lds_dwordx4 v[18:19], off
	v_lshl_add_u64 v[18:19], s[36:37], 0, v[136:137]
	s_add_u32 s36, s6, s22
	s_mov_b32 m0, s51
	s_addc_u32 s37, s7, 0
	global_load_lds_dwordx4 v[18:19], off
	v_lshl_add_u64 v[18:19], s[36:37], 0, v[252:253]
	s_mov_b32 m0, s54
	s_addk_i32 s24, 0x80
	global_load_lds_dwordx4 v[18:19], off
	v_lshl_add_u64 v[18:19], s[36:37], 0, v[136:137]
	s_add_u32 s36, s6, s24
	s_mov_b32 m0, s55
	s_addc_u32 s37, s7, 0
	global_load_lds_dwordx4 v[18:19], off
	v_lshl_add_u64 v[18:19], s[36:37], 0, v[138:139]
	s_mov_b32 m0, s52
	s_nop 0
	global_load_lds_dwordx4 v[18:19], off
	v_lshl_add_u64 v[18:19], s[36:37], 0, v[134:135]
	s_mov_b32 m0, s53
	s_nop 0
	global_load_lds_dwordx4 v[18:19], off
	s_waitcnt vmcnt(8)
	s_waitcnt lgkmcnt(0)
	s_barrier
	s_waitcnt lgkmcnt(0)
	v_mfma_f32_16x16x128_f8f6f4 v[62:65], v[2:9], v[160:167], v[62:65]
	v_mfma_f32_16x16x128_f8f6f4 v[58:61], v[10:17], v[160:167], v[58:61]
	v_mfma_f32_16x16x128_f8f6f4 v[50:53], v[2:9], v[168:175], v[50:53]
	v_mfma_f32_16x16x128_f8f6f4 v[42:45], v[10:17], v[168:175], v[196:199]
	v_mfma_f32_16x16x128_f8f6f4 v[34:37], v[2:9], v[176:183], v[200:203]
	v_mfma_f32_16x16x128_f8f6f4 v[26:29], v[10:17], v[176:183], v[204:207]
	v_mfma_f32_16x16x128_f8f6f4 v[18:21], v[2:9], v[184:191], v[220:223]
	v_mfma_f32_16x16x128_f8f6f4 v[10:13], v[10:17], v[184:191], v[224:227]
	v_mfma_f32_16x16x128_f8f6f4 v[54:57], v[144:151], v[160:167], v[54:57]
	v_mfma_f32_16x16x128_f8f6f4 v[46:49], v[152:159], v[160:167], v[228:231]
	v_mfma_f32_16x16x128_f8f6f4 v[38:41], v[144:151], v[168:175], v[232:235]
	v_mfma_f32_16x16x128_f8f6f4 v[30:33], v[152:159], v[168:175], v[236:239]
	v_mfma_f32_16x16x128_f8f6f4 v[22:25], v[144:151], v[176:183], v[240:243]
	v_mfma_f32_16x16x128_f8f6f4 v[14:17], v[152:159], v[176:183], v[244:247]
	v_mfma_f32_16x16x128_f8f6f4 v[6:9], v[144:151], v[184:191], v[248:251]
	v_mfma_f32_16x16x128_f8f6f4 v[2:5], v[152:159], v[184:191], v[130:133]
	s_barrier
	s_add_i32 s21, s21, 2
	s_addk_i32 s20, 0x100
	s_addk_i32 s8, 0x100
	s_cmp_gt_u32 s21, 5
	s_cbranch_scc0 .LBB0_1802
	s_and_b64 vcc, exec, s[14:15]
	s_cbranch_vccz .LBB0_1805
	s_barrier

; #define PG8_STAGE(bufoff, gbase, voff) do { _Pragma("unroll") for (int _i = 0; _i < 2; ++_i) \
;         __builtin_amdgcn_global_load_lds((const unsigned*)(wsb + (size_t)(gbase) + (voff)[_i]), (LAS unsigned*)(lds + (bufoff) + ldsw + _i * 8192), 16, 0, 0); } while (0)
; #define PG8_LDA(dst, b, h) do { _Pragma("unroll") for (int m = 0; m < 4; ++m) { if constexpr (FP8) dst##8[m] = PG8_LD8(pa, PG8_SA(b, h) + m * 2048); \
;         else { _Pragma("unroll") for (int k = 0; k < 2; ++k) dst[m][k] = *(const LAS bf16x8*)(pa + PG8_SA(b, h) + m * 2048 + k * 1024); } } } while (0)
; #define PG8_LDB(dst, b, h) do { _Pragma("unroll") for (int n = 0; n < 2; ++n) { if constexpr (FP8) dst##8[n] = PG8_LD8(pb, PG8_SA(b, h) + n * 2048); \
;         else { _Pragma("unroll") for (int k = 0; k < 2; ++k) dst[n][k] = *(const LAS bf16x8*)(pb + PG8_SA(b, h) + n * 2048 + k * 1024); } } } while (0)
; #define PG8_WAIT_V(n) asm volatile("s_waitcnt vmcnt(" #n ")" ::: "memory")
; #define PG8_WAIT_L(n) asm volatile("s_waitcnt lgkmcnt(" #n ")" ::: "memory")
; #define PG8_BAR __builtin_amdgcn_s_barrier()
; #define PG8_SCHED __builtin_amdgcn_sched_barrier(0)
; template <class Epi, class Sched, bool PERM, bool FP8 = false, bool GATHER = false>
; DI void gemm_phase(LAS unsigned char* lds, const unsigned char* wsb, const unsigned lda, const unsigned ldb, const int nt, const Sched& S, const Epi& E) {
;     ...
;             PG8_LDB(B0, 0, 0); PG8_LDB(B1, 0, 1); PG8_SCHED; PG8_LDA(At, 0, 0); PG8_STAGEA(PG8_SA(1, 1), t + 1, 1, false);
;             if constexpr (GATHER) { if (last) {
;                 int tz = tid; asm volatile("" : "+v"(tz));
; #pragma unroll
;                 for (int i = 0; i < 2; ++i) { int R, C; stage_rc(tz * 16 + i * 8192, R, C);
; #pragma unroll
;                     for (int h = 0; h < 2; ++h) { const unsigned tk = (unsigned)tokt[h * HALF + R]; offC[h][i] = (tk < (unsigned)NTOK ? tk : (unsigned)(NTOK - 1)) * lda + (unsigned)C * 2u; } } } }
;             PG8_WAIT_V(8); PG8_WAIT_L(0); PG8_BAR; PG8_MMA(0, 0, At, B0); PG8_MMA(0, 1, At, B1); PG8_BAR; PG8_SCHED;
;             PG8_LDA(At, 0, 1); PG8_STAGE(PG8_SB(0, 0), b2, voffB); PG8_STAGE(PG8_SB(0, 1), b2 + hstepB, voffB); PG8_STAGEA(PG8_SA(0, 0), k2, 0, last);
;             PG8_WAIT_V(8); PG8_WAIT_L(0); PG8_BAR; PG8_MMA(1, 0, At, B0); PG8_MMA(1, 1, At, B1); PG8_BAR; PG8_SCHED;
.LBB0_2116:
	ds_read_b128 v[130:133], v200
	ds_read_b128 v[134:137], v200 offset:1024
	ds_read_b128 v[138:141], v200 offset:2048
	ds_read_b128 v[142:145], v200 offset:3072
	ds_read_b128 v[146:149], v200 offset:16384
	ds_read_b128 v[150:153], v200 offset:17408
	ds_read_b128 v[154:157], v200 offset:18432
	ds_read_b128 v[158:161], v200 offset:19456
	s_add_i32 s75, s71, 0xfffe0080
	s_cmp_eq_u32 s73, 4
	s_cselect_b32 s74, s68, s72
	s_cselect_b32 s75, s67, s75
	s_add_i32 s76, s74, 0x80
	s_add_u32 s78, s8, s71
	s_addc_u32 s79, s9, 0
	s_mov_b32 m0, s60
	v_lshl_add_u64 v[162:163], s[78:79], 0, v[168:169]
	ds_read_b128 v[170:173], v199
	ds_read_b128 v[174:177], v199 offset:1024
	ds_read_b128 v[178:181], v199 offset:2048
	ds_read_b128 v[182:185], v199 offset:3072
	ds_read_b128 v[186:189], v199 offset:4096
	ds_read_b128 v[190:193], v199 offset:5120
	ds_read_b128 v[202:205], v199 offset:6144
	ds_read_b128 v[206:209], v199 offset:7168
	global_load_lds_dwordx4 v[162:163], off
	v_lshl_add_u64 v[162:163], s[78:79], 0, v[166:167]
	s_mov_b32 m0, s61
	s_nop 0
	global_load_lds_dwordx4 v[162:163], off
	s_waitcnt vmcnt(8)
	s_waitcnt lgkmcnt(0)
	s_barrier
	s_waitcnt lgkmcnt(0)
	v_mfma_f32_16x16x128_f8f6f4 v[126:129], v[130:137], v[170:177], v[126:129]
	v_mfma_f32_16x16x128_f8f6f4 v[122:125], v[138:145], v[170:177], v[122:125]
	v_mfma_f32_16x16x128_f8f6f4 v[114:117], v[130:137], v[178:185], v[114:117]
	v_mfma_f32_16x16x128_f8f6f4 v[106:109], v[138:145], v[178:185], v[106:109]
	v_mfma_f32_16x16x128_f8f6f4 v[98:101], v[130:137], v[186:193], v[98:101]
	v_mfma_f32_16x16x128_f8f6f4 v[162:165], v[138:145], v[186:193], v[90:93]
	v_mfma_f32_16x16x128_f8f6f4 v[194:197], v[130:137], v[202:209], v[82:85]
	v_mfma_f32_16x16x128_f8f6f4 v[210:213], v[138:145], v[202:209], v[74:77]
	v_mfma_f32_16x16x128_f8f6f4 v[118:121], v[146:153], v[170:177], v[118:121]
	v_mfma_f32_16x16x128_f8f6f4 v[110:113], v[154:161], v[170:177], v[110:113]
	v_mfma_f32_16x16x128_f8f6f4 v[102:105], v[146:153], v[178:185], v[102:105]
	v_mfma_f32_16x16x128_f8f6f4 v[170:173], v[154:161], v[178:185], v[94:97]
	v_mfma_f32_16x16x128_f8f6f4 v[174:177], v[146:153], v[186:193], v[86:89]
	v_mfma_f32_16x16x128_f8f6f4 v[178:181], v[154:161], v[186:193], v[78:81]
	v_mfma_f32_16x16x128_f8f6f4 v[182:185], v[146:153], v[202:209], v[70:73]
	v_mfma_f32_16x16x128_f8f6f4 v[186:189], v[154:161], v[202:209], v[66:69]
	s_barrier
	s_add_u32 s78, s8, s74
	s_addc_u32 s79, s9, 0
	s_mov_b32 m0, s28
	v_lshl_add_u64 v[190:191], s[78:79], 0, v[168:169]
	s_add_i32 s77, s74, 0x20000
	ds_read_b128 v[66:69], v199 offset:16384
	ds_read_b128 v[70:73], v199 offset:17408
	ds_read_b128 v[74:77], v199 offset:18432
	ds_read_b128 v[78:81], v199 offset:19456
	ds_read_b128 v[82:85], v199 offset:20480
	ds_read_b128 v[86:89], v199 offset:21504
	ds_read_b128 v[90:93], v199 offset:22528
	ds_read_b128 v[94:97], v199 offset:23552
	global_load_lds_dwordx4 v[190:191], off
	v_lshl_add_u64 v[190:191], s[78:79], 0, v[166:167]
	s_add_u32 s78, s8, s77
	s_mov_b32 m0, s29
	s_addc_u32 s79, s9, 0
	global_load_lds_dwordx4 v[190:191], off
	v_lshl_add_u64 v[190:191], s[78:79], 0, v[168:169]
	s_mov_b32 m0, s46
	s_nop 0
	global_load_lds_dwordx4 v[190:191], off
	v_lshl_add_u64 v[190:191], s[78:79], 0, v[166:167]
	s_add_u32 s78, s8, s75
	s_mov_b32 m0, s47
	s_addc_u32 s79, s9, 0
	global_load_lds_dwordx4 v[190:191], off
	v_lshl_add_u64 v[190:191], s[78:79], 0, v[168:169]
	s_mov_b32 m0, s21
	s_nop 0
	global_load_lds_dwordx4 v[190:191], off
	v_lshl_add_u64 v[190:191], s[78:79], 0, v[166:167]
	s_mov_b32 m0, s48
	s_nop 0
	global_load_lds_dwordx4 v[190:191], off
	s_waitcnt vmcnt(8)
	s_waitcnt lgkmcnt(0)
	s_barrier
	s_waitcnt lgkmcnt(0)
	v_mfma_f32_16x16x128_f8f6f4 v[62:65], v[130:137], v[66:73], v[62:65]
	v_mfma_f32_16x16x128_f8f6f4 v[58:61], v[138:145], v[66:73], v[58:61]
	v_mfma_f32_16x16x128_f8f6f4 v[50:53], v[130:137], v[74:81], v[50:53]
	v_mfma_f32_16x16x128_f8f6f4 v[190:193], v[138:145], v[74:81], v[42:45]
	v_mfma_f32_16x16x128_f8f6f4 v[202:205], v[130:137], v[82:89], v[34:37]
	v_mfma_f32_16x16x128_f8f6f4 v[206:209], v[138:145], v[82:89], v[26:29]
	v_mfma_f32_16x16x128_f8f6f4 v[214:217], v[130:137], v[90:97], v[18:21]
	v_mfma_f32_16x16x128_f8f6f4 v[218:221], v[138:145], v[90:97], v[10:13]
	v_mfma_f32_16x16x128_f8f6f4 v[54:57], v[146:153], v[66:73], v[54:57]
	v_mfma_f32_16x16x128_f8f6f4 v[222:225], v[154:161], v[66:73], v[46:49]
	v_mfma_f32_16x16x128_f8f6f4 v[226:229], v[146:153], v[74:81], v[38:41]
	v_mfma_f32_16x16x128_f8f6f4 v[230:233], v[154:161], v[74:81], v[30:33]
	v_mfma_f32_16x16x128_f8f6f4 v[234:237], v[146:153], v[82:89], v[22:25]
	v_mfma_f32_16x16x128_f8f6f4 v[238:241], v[154:161], v[82:89], v[14:17]
	v_mfma_f32_16x16x128_f8f6f4 v[242:245], v[146:153], v[90:97], v[6:9]
	v_mfma_f32_16x16x128_f8f6f4 v[246:249], v[154:161], v[90:97], v[2:5]
	s_barrier
; #define PG8_STAGE(bufoff, gbase, voff) do { _Pragma("unroll") for (int _i = 0; _i < 2; ++_i) \
;         __builtin_amdgcn_global_load_lds((const unsigned*)(wsb + (size_t)(gbase) + (voff)[_i]), (LAS unsigned*)(lds + (bufoff) + ldsw + _i * 8192), 16, 0, 0); } while (0)
; #define PG8_LDA(dst, b, h) do { _Pragma("unroll") for (int m = 0; m < 4; ++m) { if constexpr (FP8) dst##8[m] = PG8_LD8(pa, PG8_SA(b, h) + m * 2048); \
;         else { _Pragma("unroll") for (int k = 0; k < 2; ++k) dst[m][k] = *(const LAS bf16x8*)(pa + PG8_SA(b, h) + m * 2048 + k * 1024); } } } while (0)
; #define PG8_LDB(dst, b, h) do { _Pragma("unroll") for (int n = 0; n < 2; ++n) { if constexpr (FP8) dst##8[n] = PG8_LD8(pb, PG8_SA(b, h) + n * 2048); \
;         else { _Pragma("unroll") for (int k = 0; k < 2; ++k) dst[n][k] = *(const LAS bf16x8*)(pb + PG8_SA(b, h) + n * 2048 + k * 1024); } } } while (0)
; #define PG8_WAIT_V(n) asm volatile("s_waitcnt vmcnt(" #n ")" ::: "memory")
; #define PG8_WAIT_L(n) asm volatile("s_waitcnt lgkmcnt(" #n ")" ::: "memory")
; #define PG8_BAR __builtin_amdgcn_s_barrier()
; #define PG8_SCHED __builtin_amdgcn_sched_barrier(0)
; template <class Epi, class Sched, bool PERM, bool FP8 = false, bool GATHER = false>
; DI void gemm_phase(LAS unsigned char* lds, const unsigned char* wsb, const unsigned lda, const unsigned ldb, const int nt, const Sched& S, const Epi& E) {
;     ...
;             PG8_LDB(B0, 1, 0); PG8_LDB(B1, 1, 1); PG8_SCHED; PG8_LDA(At, 1, 0); PG8_STAGEA(PG8_SA(0, 1), k2, 1, last);
;             PG8_WAIT_V(8); PG8_WAIT_L(0); PG8_BAR; PG8_MMA(0, 0, At, B0); PG8_MMA(0, 1, At, B1); PG8_BAR; PG8_SCHED;
;             PG8_LDA(At, 1, 1); PG8_STAGE(PG8_SB(1, 0), b3, voffB); PG8_STAGE(PG8_SB(1, 1), b3 + hstepB, voffB); PG8_STAGEA(PG8_SA(1, 0), k3, 0, last);
;             PG8_WAIT_V(8); PG8_WAIT_L(0); PG8_BAR; PG8_MMA(1, 0, At, B0); PG8_MMA(1, 1, At, B1); PG8_BAR; PG8_SCHED;
;         }
;         if (wr == 0) PG8_BAR;
	s_nop 4
	ds_read_b128 v[2:5], v200 offset:32768
	ds_read_b128 v[6:9], v200 offset:33792
	ds_read_b128 v[10:13], v200 offset:34816
	ds_read_b128 v[14:17], v200 offset:35840
	ds_read_b128 v[130:133], v200 offset:49152
	ds_read_b128 v[134:137], v200 offset:50176
	ds_read_b128 v[138:141], v200 offset:51200
	ds_read_b128 v[142:145], v200 offset:52224
	s_add_i32 s77, s75, 0x20000
	s_add_u32 s78, s8, s77
	s_addc_u32 s79, s9, 0
	s_mov_b32 m0, s49
	v_lshl_add_u64 v[66:67], s[78:79], 0, v[168:169]
	ds_read_b128 v[18:21], v199 offset:32768
	ds_read_b128 v[22:25], v199 offset:33792
	ds_read_b128 v[26:29], v199 offset:34816
	ds_read_b128 v[30:33], v199 offset:35840
	ds_read_b128 v[34:37], v199 offset:36864
	ds_read_b128 v[38:41], v199 offset:37888
	ds_read_b128 v[42:45], v199 offset:38912
	ds_read_b128 v[46:49], v199 offset:39936
	global_load_lds_dwordx4 v[66:67], off
	v_lshl_add_u64 v[66:67], s[78:79], 0, v[166:167]
	s_mov_b32 m0, s50
	s_nop 0
	global_load_lds_dwordx4 v[66:67], off
	s_waitcnt vmcnt(8)
	s_waitcnt lgkmcnt(0)
	s_barrier
	s_waitcnt lgkmcnt(0)
	v_mfma_f32_16x16x128_f8f6f4 v[126:129], v[2:9], v[18:25], v[126:129]
	v_mfma_f32_16x16x128_f8f6f4 v[122:125], v[10:17], v[18:25], v[122:125]
	v_mfma_f32_16x16x128_f8f6f4 v[114:117], v[2:9], v[26:33], v[114:117]
	v_mfma_f32_16x16x128_f8f6f4 v[106:109], v[10:17], v[26:33], v[106:109]
	v_mfma_f32_16x16x128_f8f6f4 v[98:101], v[2:9], v[34:41], v[98:101]
	v_mfma_f32_16x16x128_f8f6f4 v[90:93], v[10:17], v[34:41], v[162:165]
	v_mfma_f32_16x16x128_f8f6f4 v[82:85], v[2:9], v[42:49], v[194:197]
	v_mfma_f32_16x16x128_f8f6f4 v[74:77], v[10:17], v[42:49], v[210:213]
	v_mfma_f32_16x16x128_f8f6f4 v[118:121], v[130:137], v[18:25], v[118:121]
	v_mfma_f32_16x16x128_f8f6f4 v[110:113], v[138:145], v[18:25], v[110:113]
	v_mfma_f32_16x16x128_f8f6f4 v[102:105], v[130:137], v[26:33], v[102:105]
	v_mfma_f32_16x16x128_f8f6f4 v[94:97], v[138:145], v[26:33], v[170:173]
	v_mfma_f32_16x16x128_f8f6f4 v[86:89], v[130:137], v[34:41], v[174:177]
	v_mfma_f32_16x16x128_f8f6f4 v[78:81], v[138:145], v[34:41], v[178:181]
	v_mfma_f32_16x16x128_f8f6f4 v[70:73], v[130:137], v[42:49], v[182:185]
	v_mfma_f32_16x16x128_f8f6f4 v[66:69], v[138:145], v[42:49], v[186:189]
	s_barrier
	s_add_u32 s76, s8, s76
	s_addc_u32 s77, s9, 0
	s_mov_b32 m0, s52
	v_lshl_add_u64 v[18:19], s[76:77], 0, v[168:169]
	s_add_i32 s74, s74, 0x20080
	ds_read_b128 v[146:149], v199 offset:49152
	ds_read_b128 v[150:153], v199 offset:50176
	ds_read_b128 v[154:157], v199 offset:51200
	ds_read_b128 v[158:161], v199 offset:52224
	ds_read_b128 v[170:173], v199 offset:53248
	ds_read_b128 v[174:177], v199 offset:54272
	ds_read_b128 v[178:181], v199 offset:55296
	ds_read_b128 v[182:185], v199 offset:56320
	global_load_lds_dwordx4 v[18:19], off
	v_lshl_add_u64 v[18:19], s[76:77], 0, v[166:167]
	s_add_u32 s76, s8, s74
	s_mov_b32 m0, s53
	s_addc_u32 s77, s9, 0
	s_addk_i32 s75, 0x80
	global_load_lds_dwordx4 v[18:19], off
	v_lshl_add_u64 v[18:19], s[76:77], 0, v[168:169]
	s_mov_b32 m0, s56
	s_add_u32 s74, s8, s75
	global_load_lds_dwordx4 v[18:19], off
	v_lshl_add_u64 v[18:19], s[76:77], 0, v[166:167]
	s_mov_b32 m0, s57
	s_addc_u32 s75, s9, 0
	global_load_lds_dwordx4 v[18:19], off
	v_lshl_add_u64 v[18:19], s[74:75], 0, v[168:169]
	s_mov_b32 m0, s54
	s_nop 0
	global_load_lds_dwordx4 v[18:19], off
	v_lshl_add_u64 v[18:19], s[74:75], 0, v[166:167]
	s_mov_b32 m0, s55
	s_nop 0
	global_load_lds_dwordx4 v[18:19], off
	s_waitcnt vmcnt(8)
	s_waitcnt lgkmcnt(0)
	s_barrier
	s_waitcnt lgkmcnt(0)
	v_mfma_f32_16x16x128_f8f6f4 v[62:65], v[2:9], v[146:153], v[62:65]
	v_mfma_f32_16x16x128_f8f6f4 v[58:61], v[10:17], v[146:153], v[58:61]
	v_mfma_f32_16x16x128_f8f6f4 v[50:53], v[2:9], v[154:161], v[50:53]
	v_mfma_f32_16x16x128_f8f6f4 v[42:45], v[10:17], v[154:161], v[190:193]
	v_mfma_f32_16x16x128_f8f6f4 v[34:37], v[2:9], v[170:177], v[202:205]
	v_mfma_f32_16x16x128_f8f6f4 v[26:29], v[10:17], v[170:177], v[206:209]
	v_mfma_f32_16x16x128_f8f6f4 v[18:21], v[2:9], v[178:185], v[214:217]
	v_mfma_f32_16x16x128_f8f6f4 v[10:13], v[10:17], v[178:185], v[218:221]
	v_mfma_f32_16x16x128_f8f6f4 v[54:57], v[130:137], v[146:153], v[54:57]
	v_mfma_f32_16x16x128_f8f6f4 v[46:49], v[138:145], v[146:153], v[222:225]
	v_mfma_f32_16x16x128_f8f6f4 v[38:41], v[130:137], v[154:161], v[226:229]
	v_mfma_f32_16x16x128_f8f6f4 v[30:33], v[138:145], v[154:161], v[230:233]
	v_mfma_f32_16x16x128_f8f6f4 v[22:25], v[130:137], v[170:177], v[234:237]
	v_mfma_f32_16x16x128_f8f6f4 v[14:17], v[138:145], v[170:177], v[238:241]
	v_mfma_f32_16x16x128_f8f6f4 v[6:9], v[130:137], v[178:185], v[242:245]
	v_mfma_f32_16x16x128_f8f6f4 v[2:5], v[138:145], v[178:185], v[246:249]
	s_barrier
	s_add_i32 s73, s73, 2
	s_addk_i32 s71, 0x100
	s_addk_i32 s72, 0x100
	s_cmp_gt_u32 s73, 5
	s_cbranch_scc0 .LBB0_2116
	s_and_b64 vcc, exec, s[12:13]
	s_cbranch_vccz .LBB0_2119
	s_barrier

; #define PG8_STAGE(bufoff, gbase, voff) do { _Pragma("unroll") for (int _i = 0; _i < 2; ++_i) \
;         __builtin_amdgcn_global_load_lds((const unsigned*)(wsb + (size_t)(gbase) + (voff)[_i]), (LAS unsigned*)(lds + (bufoff) + ldsw + _i * 8192), 16, 0, 0); } while (0)
; #define PG8_LDA(dst, b, h) do { _Pragma("unroll") for (int m = 0; m < 4; ++m) { if constexpr (FP8) dst##8[m] = PG8_LD8(pa, PG8_SA(b, h) + m * 2048); \
;         else { _Pragma("unroll") for (int k = 0; k < 2; ++k) dst[m][k] = *(const LAS bf16x8*)(pa + PG8_SA(b, h) + m * 2048 + k * 1024); } } } while (0)
; #define PG8_LDB(dst, b, h) do { _Pragma("unroll") for (int n = 0; n < 2; ++n) { if constexpr (FP8) dst##8[n] = PG8_LD8(pb, PG8_SA(b, h) + n * 2048); \
;         else { _Pragma("unroll") for (int k = 0; k < 2; ++k) dst[n][k] = *(const LAS bf16x8*)(pb + PG8_SA(b, h) + n * 2048 + k * 1024); } } } while (0)
; #define PG8_WAIT_V(n) asm volatile("s_waitcnt vmcnt(" #n ")" ::: "memory")
; #define PG8_WAIT_L(n) asm volatile("s_waitcnt lgkmcnt(" #n ")" ::: "memory")
; #define PG8_BAR __builtin_amdgcn_s_barrier()
; #define PG8_SCHED __builtin_amdgcn_sched_barrier(0)
; template <class Epi, class Sched, bool PERM, bool FP8 = false, bool GATHER = false>
; DI void gemm_phase(LAS unsigned char* lds, const unsigned char* wsb, const unsigned lda, const unsigned ldb, const int nt, const Sched& S, const Epi& E) {
;     ...
;             PG8_LDB(B0, 0, 0); PG8_LDB(B1, 0, 1); PG8_SCHED; PG8_LDA(At, 0, 0); PG8_STAGEA(PG8_SA(1, 1), t + 1, 1, false);
;             if constexpr (GATHER) { if (last) {
;                 int tz = tid; asm volatile("" : "+v"(tz));
; #pragma unroll
;                 for (int i = 0; i < 2; ++i) { int R, C; stage_rc(tz * 16 + i * 8192, R, C);
; #pragma unroll
;                     for (int h = 0; h < 2; ++h) { const unsigned tk = (unsigned)tokt[h * HALF + R]; offC[h][i] = (tk < (unsigned)NTOK ? tk : (unsigned)(NTOK - 1)) * lda + (unsigned)C * 2u; } } } }
;             PG8_WAIT_V(8); PG8_WAIT_L(0); PG8_BAR; PG8_MMA(0, 0, At, B0); PG8_MMA(0, 1, At, B1); PG8_BAR; PG8_SCHED;
;             PG8_LDA(At, 0, 1); PG8_STAGE(PG8_SB(0, 0), b2, voffB); PG8_STAGE(PG8_SB(0, 1), b2 + hstepB, voffB); PG8_STAGEA(PG8_SA(0, 0), k2, 0, last);
;             PG8_WAIT_V(8); PG8_WAIT_L(0); PG8_BAR; PG8_MMA(1, 0, At, B0); PG8_MMA(1, 1, At, B1); PG8_BAR; PG8_SCHED;
.LBB0_2544:
	s_waitcnt vmcnt(8)
	s_add_i32 s84, s80, s44
	s_waitcnt lgkmcnt(0)
	s_and_b64 s[82:83], s[46:47], exec
	s_cselect_b32 s82, s12, s84
	v_mov_b32_e32 v205, v197
	s_add_i32 s83, s82, 0x80
	s_barrier
	s_waitcnt lgkmcnt(0)
	v_mfma_f32_16x16x128_f8f6f4 v[190:193], v[18:25], v[58:65], v[190:193]
	v_mfma_f32_16x16x128_f8f6f4 v[186:189], v[26:33], v[58:65], v[186:189]
	v_mfma_f32_16x16x128_f8f6f4 v[174:177], v[18:25], v[50:57], v[174:177]
	v_mfma_f32_16x16x128_f8f6f4 v[166:169], v[26:33], v[50:57], v[166:169]
	v_mfma_f32_16x16x128_f8f6f4 v[158:161], v[18:25], v[42:49], v[158:161]
	v_mfma_f32_16x16x128_f8f6f4 v[150:153], v[26:33], v[42:49], v[150:153]
	v_mfma_f32_16x16x128_f8f6f4 v[142:145], v[18:25], v[34:41], v[142:145]
	v_mfma_f32_16x16x128_f8f6f4 v[134:137], v[26:33], v[34:41], v[134:137]
	v_mfma_f32_16x16x128_f8f6f4 v[182:185], v[2:9], v[58:65], v[182:185]
	v_mfma_f32_16x16x128_f8f6f4 v[178:181], v[10:17], v[58:65], v[178:181]
	v_mfma_f32_16x16x128_f8f6f4 v[170:173], v[2:9], v[50:57], v[170:173]
	v_mfma_f32_16x16x128_f8f6f4 v[162:165], v[10:17], v[50:57], v[162:165]
	v_mfma_f32_16x16x128_f8f6f4 v[154:157], v[2:9], v[42:49], v[154:157]
	v_mfma_f32_16x16x128_f8f6f4 v[146:149], v[10:17], v[42:49], v[146:149]
	v_mfma_f32_16x16x128_f8f6f4 v[138:141], v[2:9], v[34:41], v[138:141]
	v_mfma_f32_16x16x128_f8f6f4 v[130:133], v[10:17], v[34:41], v[130:133]
	s_barrier
	s_add_u32 s84, s8, s82
	s_addc_u32 s85, s9, 0
	s_mov_b32 m0, s48
	v_lshl_add_u64 v[214:215], s[84:85], 0, v[198:199]
	ds_read_b128 v[34:37], v209 offset:16384
	ds_read_b128 v[38:41], v209 offset:17408
	ds_read_b128 v[42:45], v209 offset:18432
	ds_read_b128 v[46:49], v209 offset:19456
	ds_read_b128 v[50:53], v209 offset:20480
	ds_read_b128 v[54:57], v209 offset:21504
	ds_read_b128 v[58:61], v209 offset:22528
	ds_read_b128 v[62:65], v209 offset:23552
	global_load_lds_dwordx4 v[214:215], off
	v_lshl_add_u64 v[214:215], s[84:85], 0, v[200:201]
	s_add_i32 s84, s82, 0x20000
	s_add_u32 s84, s8, s84
	s_addc_u32 s85, s9, 0
	s_add_u32 s44, s44, 0x100
	s_mov_b32 m0, s49
	s_addc_u32 s45, s45, 0
	global_load_lds_dwordx4 v[214:215], off
	v_lshl_add_u64 v[214:215], s[84:85], 0, v[198:199]
	s_mov_b32 m0, s50
	s_and_b64 s[46:47], s[46:47], exec
	global_load_lds_dwordx4 v[214:215], off
	v_lshl_add_u64 v[214:215], s[84:85], 0, v[200:201]
	s_cselect_b32 s84, 0, s44
	s_mov_b32 m0, s51
	s_add_u32 s46, s10, s84
	global_load_lds_dwordx4 v[214:215], off
	s_addc_u32 s47, s11, 0
	s_mov_b32 m0, s39
	s_nop 0
	global_load_lds_dwordx4 v212, s[46:47]
	s_mov_b32 m0, s52
	s_nop 0
	global_load_lds_dwordx4 v202, s[46:47]
	s_waitcnt vmcnt(8)
	s_waitcnt lgkmcnt(0)
	s_barrier
	s_waitcnt lgkmcnt(0)
	v_mfma_f32_16x16x128_f8f6f4 v[126:129], v[18:25], v[34:41], v[126:129]
	v_mfma_f32_16x16x128_f8f6f4 v[118:121], v[26:33], v[34:41], v[118:121]
	v_mfma_f32_16x16x128_f8f6f4 v[110:113], v[18:25], v[42:49], v[110:113]
	v_mfma_f32_16x16x128_f8f6f4 v[102:105], v[26:33], v[42:49], v[102:105]
	v_mfma_f32_16x16x128_f8f6f4 v[94:97], v[18:25], v[50:57], v[94:97]
	v_mfma_f32_16x16x128_f8f6f4 v[86:89], v[26:33], v[50:57], v[86:89]
	v_mfma_f32_16x16x128_f8f6f4 v[78:81], v[18:25], v[58:65], v[78:81]
	v_mfma_f32_16x16x128_f8f6f4 v[70:73], v[26:33], v[58:65], v[70:73]
	v_mfma_f32_16x16x128_f8f6f4 v[122:125], v[2:9], v[34:41], v[122:125]
	v_mfma_f32_16x16x128_f8f6f4 v[114:117], v[10:17], v[34:41], v[114:117]
	v_mfma_f32_16x16x128_f8f6f4 v[106:109], v[2:9], v[42:49], v[106:109]
	v_mfma_f32_16x16x128_f8f6f4 v[98:101], v[10:17], v[42:49], v[98:101]
	v_mfma_f32_16x16x128_f8f6f4 v[90:93], v[2:9], v[50:57], v[90:93]
	v_mfma_f32_16x16x128_f8f6f4 v[82:85], v[10:17], v[50:57], v[82:85]
	v_mfma_f32_16x16x128_f8f6f4 v[74:77], v[2:9], v[58:65], v[74:77]
	v_mfma_f32_16x16x128_f8f6f4 v[66:69], v[10:17], v[58:65], v[66:69]
	s_barrier
; #define PG8_STAGE(bufoff, gbase, voff) do { _Pragma("unroll") for (int _i = 0; _i < 2; ++_i) \
;         __builtin_amdgcn_global_load_lds((const unsigned*)(wsb + (size_t)(gbase) + (voff)[_i]), (LAS unsigned*)(lds + (bufoff) + ldsw + _i * 8192), 16, 0, 0); } while (0)
; #define PG8_LDA(dst, b, h) do { _Pragma("unroll") for (int m = 0; m < 4; ++m) { if constexpr (FP8) dst##8[m] = PG8_LD8(pa, PG8_SA(b, h) + m * 2048); \
;         else { _Pragma("unroll") for (int k = 0; k < 2; ++k) dst[m][k] = *(const LAS bf16x8*)(pa + PG8_SA(b, h) + m * 2048 + k * 1024); } } } while (0)
; #define PG8_LDB(dst, b, h) do { _Pragma("unroll") for (int n = 0; n < 2; ++n) { if constexpr (FP8) dst##8[n] = PG8_LD8(pb, PG8_SA(b, h) + n * 2048); \
;         else { _Pragma("unroll") for (int k = 0; k < 2; ++k) dst[n][k] = *(const LAS bf16x8*)(pb + PG8_SA(b, h) + n * 2048 + k * 1024); } } } while (0)
; #define PG8_WAIT_V(n) asm volatile("s_waitcnt vmcnt(" #n ")" ::: "memory")
; #define PG8_WAIT_L(n) asm volatile("s_waitcnt lgkmcnt(" #n ")" ::: "memory")
; #define PG8_BAR __builtin_amdgcn_s_barrier()
; #define PG8_SCHED __builtin_amdgcn_sched_barrier(0)
; template <class Epi, class Sched, bool PERM, bool FP8 = false, bool GATHER = false>
; DI void gemm_phase(LAS unsigned char* lds, const unsigned char* wsb, const unsigned lda, const unsigned ldb, const int nt, const Sched& S, const Epi& E) {
;     ...
;             PG8_LDB(B0, 1, 0); PG8_LDB(B1, 1, 1); PG8_SCHED; PG8_LDA(At, 1, 0); PG8_STAGEA(PG8_SA(0, 1), k2, 1, last);
;             PG8_WAIT_V(8); PG8_WAIT_L(0); PG8_BAR; PG8_MMA(0, 0, At, B0); PG8_MMA(0, 1, At, B1); PG8_BAR; PG8_SCHED;
;             PG8_LDA(At, 1, 1); PG8_STAGE(PG8_SB(1, 0), b3, voffB); PG8_STAGE(PG8_SB(1, 1), b3 + hstepB, voffB); PG8_STAGEA(PG8_SA(1, 0), k3, 0, last);
;             PG8_WAIT_V(8); PG8_WAIT_L(0); PG8_BAR; PG8_MMA(1, 0, At, B0); PG8_MMA(1, 1, At, B1); PG8_BAR; PG8_SCHED;
;         }
	ds_read_b128 v[2:5], v210 offset:32768
	ds_read_b128 v[6:9], v210 offset:33792
	ds_read_b128 v[10:13], v210 offset:34816
	ds_read_b128 v[14:17], v210 offset:35840
	ds_read_b128 v[18:21], v210 offset:49152
	ds_read_b128 v[22:25], v210 offset:50176
	ds_read_b128 v[26:29], v210 offset:51200
	ds_read_b128 v[30:33], v210 offset:52224
	s_mov_b32 m0, s53
	v_lshl_add_u64 v[214:215], s[46:47], 0, v[196:197]
	ds_read_b128 v[34:37], v209 offset:32768
	ds_read_b128 v[38:41], v209 offset:33792
	ds_read_b128 v[42:45], v209 offset:34816
	ds_read_b128 v[46:49], v209 offset:35840
	ds_read_b128 v[50:53], v209 offset:36864
	ds_read_b128 v[54:57], v209 offset:37888
	ds_read_b128 v[58:61], v209 offset:38912
	ds_read_b128 v[62:65], v209 offset:39936
	global_load_lds_dwordx4 v[214:215], off
	v_lshl_add_u64 v[214:215], s[46:47], 0, v[204:205]
	s_mov_b32 m0, s54
	s_nop 0
	global_load_lds_dwordx4 v[214:215], off
	s_waitcnt vmcnt(8)
	s_waitcnt lgkmcnt(0)
	s_barrier
	s_waitcnt lgkmcnt(0)
	v_mfma_f32_16x16x128_f8f6f4 v[190:193], v[2:9], v[34:41], v[190:193]
	v_mfma_f32_16x16x128_f8f6f4 v[186:189], v[10:17], v[34:41], v[186:189]
	v_mfma_f32_16x16x128_f8f6f4 v[174:177], v[2:9], v[42:49], v[174:177]
	v_mfma_f32_16x16x128_f8f6f4 v[166:169], v[10:17], v[42:49], v[166:169]
	v_mfma_f32_16x16x128_f8f6f4 v[158:161], v[2:9], v[50:57], v[158:161]
	v_mfma_f32_16x16x128_f8f6f4 v[150:153], v[10:17], v[50:57], v[150:153]
	v_mfma_f32_16x16x128_f8f6f4 v[142:145], v[2:9], v[58:65], v[142:145]
	v_mfma_f32_16x16x128_f8f6f4 v[134:137], v[10:17], v[58:65], v[134:137]
	v_mfma_f32_16x16x128_f8f6f4 v[182:185], v[18:25], v[34:41], v[182:185]
	v_mfma_f32_16x16x128_f8f6f4 v[178:181], v[26:33], v[34:41], v[178:181]
	v_mfma_f32_16x16x128_f8f6f4 v[170:173], v[18:25], v[42:49], v[170:173]
	v_mfma_f32_16x16x128_f8f6f4 v[162:165], v[26:33], v[42:49], v[162:165]
	v_mfma_f32_16x16x128_f8f6f4 v[154:157], v[18:25], v[50:57], v[154:157]
	v_mfma_f32_16x16x128_f8f6f4 v[146:149], v[26:33], v[50:57], v[146:149]
	v_mfma_f32_16x16x128_f8f6f4 v[138:141], v[18:25], v[58:65], v[138:141]
	v_mfma_f32_16x16x128_f8f6f4 v[130:133], v[26:33], v[58:65], v[130:133]
	s_barrier
	s_add_u32 s46, s8, s83
	s_addc_u32 s47, s9, 0
	s_mov_b32 m0, s58
	v_lshl_add_u64 v[214:215], s[46:47], 0, v[198:199]
	s_add_i32 s82, s82, 0x20080
	ds_read_b128 v[34:37], v209 offset:49152
	ds_read_b128 v[38:41], v209 offset:50176
	ds_read_b128 v[42:45], v209 offset:51200
	ds_read_b128 v[46:49], v209 offset:52224
	ds_read_b128 v[50:53], v209 offset:53248
	ds_read_b128 v[54:57], v209 offset:54272
	ds_read_b128 v[58:61], v209 offset:55296
	ds_read_b128 v[62:65], v209 offset:56320
	global_load_lds_dwordx4 v[214:215], off
	v_lshl_add_u64 v[214:215], s[46:47], 0, v[200:201]
	s_add_u32 s46, s8, s82
	s_mov_b32 m0, s59
	s_addc_u32 s47, s9, 0
	global_load_lds_dwordx4 v[214:215], off
	v_lshl_add_u64 v[214:215], s[46:47], 0, v[198:199]
	s_mov_b32 m0, s64
	s_nop 0
	global_load_lds_dwordx4 v[214:215], off
	v_lshl_add_u64 v[214:215], s[46:47], 0, v[200:201]
	s_add_u32 s46, s8, s84
	s_addc_u32 s47, s9, 0
	s_mov_b32 m0, s65
	s_add_u32 s46, s46, 0x5b9d4080
	global_load_lds_dwordx4 v[214:215], off
	s_addc_u32 s47, s47, 0
	s_mov_b32 m0, s60
	s_nop 0
	global_load_lds_dwordx4 v212, s[46:47]
	s_mov_b32 m0, s61
	s_nop 0
	global_load_lds_dwordx4 v202, s[46:47]
	s_waitcnt vmcnt(8)
	s_waitcnt lgkmcnt(0)
	s_barrier
	s_waitcnt lgkmcnt(0)
	v_mfma_f32_16x16x128_f8f6f4 v[126:129], v[2:9], v[34:41], v[126:129]
	v_mfma_f32_16x16x128_f8f6f4 v[118:121], v[10:17], v[34:41], v[118:121]
	v_mfma_f32_16x16x128_f8f6f4 v[110:113], v[2:9], v[42:49], v[110:113]
	v_mfma_f32_16x16x128_f8f6f4 v[102:105], v[10:17], v[42:49], v[102:105]
	v_mfma_f32_16x16x128_f8f6f4 v[94:97], v[2:9], v[50:57], v[94:97]
	v_mfma_f32_16x16x128_f8f6f4 v[86:89], v[10:17], v[50:57], v[86:89]
	v_mfma_f32_16x16x128_f8f6f4 v[78:81], v[2:9], v[58:65], v[78:81]
	v_mfma_f32_16x16x128_f8f6f4 v[70:73], v[10:17], v[58:65], v[70:73]
	v_mfma_f32_16x16x128_f8f6f4 v[122:125], v[18:25], v[34:41], v[122:125]
	v_mfma_f32_16x16x128_f8f6f4 v[114:117], v[26:33], v[34:41], v[114:117]
	v_mfma_f32_16x16x128_f8f6f4 v[106:109], v[18:25], v[42:49], v[106:109]
	v_mfma_f32_16x16x128_f8f6f4 v[98:101], v[26:33], v[42:49], v[98:101]
	v_mfma_f32_16x16x128_f8f6f4 v[90:93], v[18:25], v[50:57], v[90:93]
	v_mfma_f32_16x16x128_f8f6f4 v[82:85], v[26:33], v[50:57], v[82:85]
	v_mfma_f32_16x16x128_f8f6f4 v[74:77], v[18:25], v[58:65], v[74:77]
	v_mfma_f32_16x16x128_f8f6f4 v[66:69], v[26:33], v[58:65], v[66:69]
	s_barrier
	s_add_i32 s81, s81, 2
	s_cmp_gt_u32 s81, 5
	s_cbranch_scc1 .LBB0_2547

; #define PG8_STAGE(bufoff, gbase, voff) do { _Pragma("unroll") for (int _i = 0; _i < 2; ++_i) \
;         __builtin_amdgcn_global_load_lds((const unsigned*)(wsb + (size_t)(gbase) + (voff)[_i]), (LAS unsigned*)(lds + (bufoff) + ldsw + _i * 8192), 16, 0, 0); } while (0)
; #define PG8_LDA(dst, b, h) do { _Pragma("unroll") for (int m = 0; m < 4; ++m) { if constexpr (FP8) dst##8[m] = PG8_LD8(pa, PG8_SA(b, h) + m * 2048); \
;         else { _Pragma("unroll") for (int k = 0; k < 2; ++k) dst[m][k] = *(const LAS bf16x8*)(pa + PG8_SA(b, h) + m * 2048 + k * 1024); } } } while (0)
; #define PG8_LDB(dst, b, h) do { _Pragma("unroll") for (int n = 0; n < 2; ++n) { if constexpr (FP8) dst##8[n] = PG8_LD8(pb, PG8_SA(b, h) + n * 2048); \
;         else { _Pragma("unroll") for (int k = 0; k < 2; ++k) dst[n][k] = *(const LAS bf16x8*)(pb + PG8_SA(b, h) + n * 2048 + k * 1024); } } } while (0)
; #define PG8_WAIT_V(n) asm volatile("s_waitcnt vmcnt(" #n ")" ::: "memory")
; #define PG8_WAIT_L(n) asm volatile("s_waitcnt lgkmcnt(" #n ")" ::: "memory")
; #define PG8_BAR __builtin_amdgcn_s_barrier()
; #define PG8_SCHED __builtin_amdgcn_sched_barrier(0)
; template <class Epi, class Sched, bool PERM, bool FP8 = false, bool GATHER = false>
; DI void gemm_phase(LAS unsigned char* lds, const unsigned char* wsb, const unsigned lda, const unsigned ldb, const int nt, const Sched& S, const Epi& E) {
;     ...
;             PG8_LDB(B0, 0, 0); PG8_LDB(B1, 0, 1); PG8_SCHED; PG8_LDA(At, 0, 0); PG8_STAGEA(PG8_SA(1, 1), t + 1, 1, false);
;             if constexpr (GATHER) { if (last) {
;                 int tz = tid; asm volatile("" : "+v"(tz));
; #pragma unroll
;                 for (int i = 0; i < 2; ++i) { int R, C; stage_rc(tz * 16 + i * 8192, R, C);
; #pragma unroll
;                     for (int h = 0; h < 2; ++h) { const unsigned tk = (unsigned)tokt[h * HALF + R]; offC[h][i] = (tk < (unsigned)NTOK ? tk : (unsigned)(NTOK - 1)) * lda + (unsigned)C * 2u; } } } }
;             PG8_WAIT_V(8); PG8_WAIT_L(0); PG8_BAR; PG8_MMA(0, 0, At, B0); PG8_MMA(0, 1, At, B1); PG8_BAR; PG8_SCHED;
;             PG8_LDA(At, 0, 1); PG8_STAGE(PG8_SB(0, 0), b2, voffB); PG8_STAGE(PG8_SB(0, 1), b2 + hstepB, voffB); PG8_STAGEA(PG8_SA(0, 0), k2, 0, last);
;             PG8_WAIT_V(8); PG8_WAIT_L(0); PG8_BAR; PG8_MMA(1, 0, At, B0); PG8_MMA(1, 1, At, B1); PG8_BAR; PG8_SCHED;
.LBB0_2652:
	ds_read_b128 v[130:133], v154
	ds_read_b128 v[134:137], v154 offset:1024
	ds_read_b128 v[138:141], v154 offset:2048
	ds_read_b128 v[142:145], v154 offset:3072
	ds_read_b128 v[158:161], v154 offset:16384
	ds_read_b128 v[162:165], v154 offset:17408
	ds_read_b128 v[166:169], v154 offset:18432
	ds_read_b128 v[170:173], v154 offset:19456
	s_add_i32 s70, s67, 0xfffe0080
	s_add_i32 s71, s70, s64
	s_cmp_eq_u32 s66, 4
	s_cselect_b64 s[24:25], -1, 0
	s_and_b64 s[68:69], s[24:25], exec
	s_cselect_b32 s68, s65, s71
	s_cselect_b32 s72, 0, s70
	s_add_i32 s69, s68, 0x80
	s_add_i32 s70, s62, s67
	s_add_u32 s70, s8, s70
	s_addc_u32 s71, s9, 0
	v_lshl_add_u64 v[150:151], s[70:71], 0, v[146:147]
	s_add_i32 m0, s26, 0xc000
	ds_read_b128 v[174:177], v153
	ds_read_b128 v[178:181], v153 offset:1024
	ds_read_b128 v[182:185], v153 offset:2048
	ds_read_b128 v[186:189], v153 offset:3072
	ds_read_b128 v[190:193], v153 offset:4096
	ds_read_b128 v[194:197], v153 offset:5120
	ds_read_b128 v[198:201], v153 offset:6144
	ds_read_b128 v[202:205], v153 offset:7168
	global_load_lds_dwordx4 v[150:151], off
	v_lshl_add_u64 v[150:151], s[70:71], 0, v[148:149]
	s_add_i32 m0, s26, 0xe000
	s_nop 0
	global_load_lds_dwordx4 v[150:151], off
	s_waitcnt vmcnt(8)
	s_waitcnt lgkmcnt(0)
	s_barrier
	s_waitcnt lgkmcnt(0)
	v_mfma_f32_16x16x128_f8f6f4 v[126:129], v[130:137], v[174:181], v[126:129]
	v_mfma_f32_16x16x128_f8f6f4 v[122:125], v[138:145], v[174:181], v[122:125]
	v_mfma_f32_16x16x128_f8f6f4 v[118:121], v[130:137], v[182:189], v[118:121]
	v_mfma_f32_16x16x128_f8f6f4 v[114:117], v[138:145], v[182:189], v[114:117]
	v_mfma_f32_16x16x128_f8f6f4 v[206:209], v[130:137], v[190:197], v[94:97]
	v_mfma_f32_16x16x128_f8f6f4 v[210:213], v[138:145], v[190:197], v[90:93]
	v_mfma_f32_16x16x128_f8f6f4 v[214:217], v[130:137], v[198:205], v[82:85]
	v_mfma_f32_16x16x128_f8f6f4 v[218:221], v[138:145], v[198:205], v[74:77]
	v_mfma_f32_16x16x128_f8f6f4 v[110:113], v[158:165], v[174:181], v[110:113]
	v_mfma_f32_16x16x128_f8f6f4 v[106:109], v[166:173], v[174:181], v[106:109]
	v_mfma_f32_16x16x128_f8f6f4 v[102:105], v[158:165], v[182:189], v[102:105]
	v_mfma_f32_16x16x128_f8f6f4 v[98:101], v[166:173], v[182:189], v[98:101]
	v_mfma_f32_16x16x128_f8f6f4 v[174:177], v[158:165], v[190:197], v[86:89]
	v_mfma_f32_16x16x128_f8f6f4 v[178:181], v[166:173], v[190:197], v[78:81]
	v_mfma_f32_16x16x128_f8f6f4 v[182:185], v[158:165], v[198:205], v[70:73]
	v_mfma_f32_16x16x128_f8f6f4 v[186:189], v[166:173], v[198:205], v[66:69]
	s_barrier
	s_add_u32 s70, s8, s68
	s_addc_u32 s71, s9, 0
	s_mov_b32 m0, s27
	v_lshl_add_u64 v[150:151], s[70:71], 0, v[146:147]
	s_nop 0
	ds_read_b128 v[66:69], v153 offset:16384
	ds_read_b128 v[70:73], v153 offset:17408
	ds_read_b128 v[74:77], v153 offset:18432
	ds_read_b128 v[78:81], v153 offset:19456
	ds_read_b128 v[82:85], v153 offset:20480
	ds_read_b128 v[86:89], v153 offset:21504
	ds_read_b128 v[90:93], v153 offset:22528
	ds_read_b128 v[94:97], v153 offset:23552
	global_load_lds_dwordx4 v[150:151], off
	v_lshl_add_u64 v[150:151], s[70:71], 0, v[148:149]
	s_add_i32 s70, s68, 0x20000
	s_add_u32 s70, s8, s70
	s_addc_u32 s71, s9, 0
	s_and_b64 s[24:25], s[20:21], s[24:25]
	s_and_b64 s[24:25], s[24:25], exec
	s_mov_b32 m0, s28
	s_cselect_b32 s24, s58, s62
	global_load_lds_dwordx4 v[150:151], off
	v_lshl_add_u64 v[150:151], s[70:71], 0, v[146:147]
	s_mov_b32 m0, s29
	s_add_i32 s24, s72, s24
	global_load_lds_dwordx4 v[150:151], off
	v_lshl_add_u64 v[150:151], s[70:71], 0, v[148:149]
	s_add_u32 s70, s8, s24
	s_mov_b32 m0, s36
	s_addc_u32 s71, s9, 0
	global_load_lds_dwordx4 v[150:151], off
	v_lshl_add_u64 v[150:151], s[70:71], 0, v[146:147]
	s_mov_b32 m0, s26
	s_nop 0
	global_load_lds_dwordx4 v[150:151], off
	v_lshl_add_u64 v[150:151], s[70:71], 0, v[148:149]
	s_mov_b32 m0, s37
	s_nop 0
	global_load_lds_dwordx4 v[150:151], off
	s_waitcnt vmcnt(8)
	s_waitcnt lgkmcnt(0)
	s_barrier
	s_waitcnt lgkmcnt(0)
	v_mfma_f32_16x16x128_f8f6f4 v[62:65], v[130:137], v[66:73], v[62:65]
	v_mfma_f32_16x16x128_f8f6f4 v[58:61], v[138:145], v[66:73], v[58:61]
	v_mfma_f32_16x16x128_f8f6f4 v[50:53], v[130:137], v[74:81], v[50:53]
	v_mfma_f32_16x16x128_f8f6f4 v[190:193], v[138:145], v[74:81], v[42:45]
	v_mfma_f32_16x16x128_f8f6f4 v[194:197], v[130:137], v[82:89], v[34:37]
	v_mfma_f32_16x16x128_f8f6f4 v[198:201], v[138:145], v[82:89], v[26:29]
	v_mfma_f32_16x16x128_f8f6f4 v[202:205], v[130:137], v[90:97], v[18:21]
	v_mfma_f32_16x16x128_f8f6f4 v[222:225], v[138:145], v[90:97], v[10:13]
	v_mfma_f32_16x16x128_f8f6f4 v[54:57], v[158:165], v[66:73], v[54:57]
	v_mfma_f32_16x16x128_f8f6f4 v[226:229], v[166:173], v[66:73], v[46:49]
	v_mfma_f32_16x16x128_f8f6f4 v[230:233], v[158:165], v[74:81], v[38:41]
	v_mfma_f32_16x16x128_f8f6f4 v[234:237], v[166:173], v[74:81], v[30:33]
	v_mfma_f32_16x16x128_f8f6f4 v[238:241], v[158:165], v[82:89], v[22:25]
	v_mfma_f32_16x16x128_f8f6f4 v[242:245], v[166:173], v[82:89], v[14:17]
	v_mfma_f32_16x16x128_f8f6f4 v[246:249], v[158:165], v[90:97], v[6:9]
	v_mfma_f32_16x16x128_f8f6f4 v[250:253], v[166:173], v[90:97], v[2:5]
	s_barrier
; #define PG8_STAGE(bufoff, gbase, voff) do { _Pragma("unroll") for (int _i = 0; _i < 2; ++_i) \
;         __builtin_amdgcn_global_load_lds((const unsigned*)(wsb + (size_t)(gbase) + (voff)[_i]), (LAS unsigned*)(lds + (bufoff) + ldsw + _i * 8192), 16, 0, 0); } while (0)
; #define PG8_LDA(dst, b, h) do { _Pragma("unroll") for (int m = 0; m < 4; ++m) { if constexpr (FP8) dst##8[m] = PG8_LD8(pa, PG8_SA(b, h) + m * 2048); \
;         else { _Pragma("unroll") for (int k = 0; k < 2; ++k) dst[m][k] = *(const LAS bf16x8*)(pa + PG8_SA(b, h) + m * 2048 + k * 1024); } } } while (0)
; #define PG8_LDB(dst, b, h) do { _Pragma("unroll") for (int n = 0; n < 2; ++n) { if constexpr (FP8) dst##8[n] = PG8_LD8(pb, PG8_SA(b, h) + n * 2048); \
;         else { _Pragma("unroll") for (int k = 0; k < 2; ++k) dst[n][k] = *(const LAS bf16x8*)(pb + PG8_SA(b, h) + n * 2048 + k * 1024); } } } while (0)
; #define PG8_WAIT_V(n) asm volatile("s_waitcnt vmcnt(" #n ")" ::: "memory")
; #define PG8_WAIT_L(n) asm volatile("s_waitcnt lgkmcnt(" #n ")" ::: "memory")
; #define PG8_BAR __builtin_amdgcn_s_barrier()
; #define PG8_SCHED __builtin_amdgcn_sched_barrier(0)
; template <class Epi, class Sched, bool PERM, bool FP8 = false, bool GATHER = false>
; DI void gemm_phase(LAS unsigned char* lds, const unsigned char* wsb, const unsigned lda, const unsigned ldb, const int nt, const Sched& S, const Epi& E) {
;     ...
;             PG8_LDB(B0, 1, 0); PG8_LDB(B1, 1, 1); PG8_SCHED; PG8_LDA(At, 1, 0); PG8_STAGEA(PG8_SA(0, 1), k2, 1, last);
;             PG8_WAIT_V(8); PG8_WAIT_L(0); PG8_BAR; PG8_MMA(0, 0, At, B0); PG8_MMA(0, 1, At, B1); PG8_BAR; PG8_SCHED;
;             PG8_LDA(At, 1, 1); PG8_STAGE(PG8_SB(1, 0), b3, voffB); PG8_STAGE(PG8_SB(1, 1), b3 + hstepB, voffB); PG8_STAGEA(PG8_SA(1, 0), k3, 0, last);
;             PG8_WAIT_V(8); PG8_WAIT_L(0); PG8_BAR; PG8_MMA(1, 0, At, B0); PG8_MMA(1, 1, At, B1); PG8_BAR; PG8_SCHED;
;         }
;         if (wr == 0) PG8_BAR;
	s_nop 4
	ds_read_b128 v[2:5], v154 offset:32768
	ds_read_b128 v[6:9], v154 offset:33792
	ds_read_b128 v[10:13], v154 offset:34816
	ds_read_b128 v[14:17], v154 offset:35840
	ds_read_b128 v[130:133], v154 offset:49152
	ds_read_b128 v[134:137], v154 offset:50176
	ds_read_b128 v[138:141], v154 offset:51200
	ds_read_b128 v[142:145], v154 offset:52224
	s_add_i32 s25, s24, 0x20000
	s_add_u32 s70, s8, s25
	s_addc_u32 s71, s9, 0
	s_mov_b32 m0, s38
	v_lshl_add_u64 v[66:67], s[70:71], 0, v[146:147]
	ds_read_b128 v[18:21], v153 offset:32768
	ds_read_b128 v[22:25], v153 offset:33792
	ds_read_b128 v[26:29], v153 offset:34816
	ds_read_b128 v[30:33], v153 offset:35840
	ds_read_b128 v[34:37], v153 offset:36864
	ds_read_b128 v[38:41], v153 offset:37888
	ds_read_b128 v[42:45], v153 offset:38912
	ds_read_b128 v[46:49], v153 offset:39936
	global_load_lds_dwordx4 v[66:67], off
	v_lshl_add_u64 v[66:67], s[70:71], 0, v[148:149]
	s_mov_b32 m0, s39
	s_nop 0
	global_load_lds_dwordx4 v[66:67], off
	s_waitcnt vmcnt(8)
	s_waitcnt lgkmcnt(0)
	s_barrier
	s_waitcnt lgkmcnt(0)
	v_mfma_f32_16x16x128_f8f6f4 v[126:129], v[2:9], v[18:25], v[126:129]
	v_mfma_f32_16x16x128_f8f6f4 v[122:125], v[10:17], v[18:25], v[122:125]
	v_mfma_f32_16x16x128_f8f6f4 v[118:121], v[2:9], v[26:33], v[118:121]
	v_mfma_f32_16x16x128_f8f6f4 v[114:117], v[10:17], v[26:33], v[114:117]
	v_mfma_f32_16x16x128_f8f6f4 v[94:97], v[2:9], v[34:41], v[206:209]
	v_mfma_f32_16x16x128_f8f6f4 v[90:93], v[10:17], v[34:41], v[210:213]
	v_mfma_f32_16x16x128_f8f6f4 v[82:85], v[2:9], v[42:49], v[214:217]
	v_mfma_f32_16x16x128_f8f6f4 v[74:77], v[10:17], v[42:49], v[218:221]
	v_mfma_f32_16x16x128_f8f6f4 v[110:113], v[130:137], v[18:25], v[110:113]
	v_mfma_f32_16x16x128_f8f6f4 v[106:109], v[138:145], v[18:25], v[106:109]
	v_mfma_f32_16x16x128_f8f6f4 v[102:105], v[130:137], v[26:33], v[102:105]
	v_mfma_f32_16x16x128_f8f6f4 v[98:101], v[138:145], v[26:33], v[98:101]
	v_mfma_f32_16x16x128_f8f6f4 v[86:89], v[130:137], v[34:41], v[174:177]
	v_mfma_f32_16x16x128_f8f6f4 v[78:81], v[138:145], v[34:41], v[178:181]
	v_mfma_f32_16x16x128_f8f6f4 v[70:73], v[130:137], v[42:49], v[182:185]
	v_mfma_f32_16x16x128_f8f6f4 v[66:69], v[138:145], v[42:49], v[186:189]
	s_barrier
	s_add_u32 s70, s8, s69
	s_addc_u32 s71, s9, 0
	s_add_i32 s68, s68, 0x20080
	s_mov_b32 m0, s43
	v_lshl_add_u64 v[18:19], s[70:71], 0, v[146:147]
	s_add_u32 s68, s8, s68
	ds_read_b128 v[158:161], v153 offset:49152
	ds_read_b128 v[162:165], v153 offset:50176
	ds_read_b128 v[166:169], v153 offset:51200
	ds_read_b128 v[170:173], v153 offset:52224
	ds_read_b128 v[174:177], v153 offset:53248
	ds_read_b128 v[178:181], v153 offset:54272
	ds_read_b128 v[182:185], v153 offset:55296
	ds_read_b128 v[186:189], v153 offset:56320
	global_load_lds_dwordx4 v[18:19], off
	v_lshl_add_u64 v[18:19], s[70:71], 0, v[148:149]
	s_mov_b32 m0, s44
	s_addc_u32 s69, s9, 0
	s_addk_i32 s24, 0x80
	global_load_lds_dwordx4 v[18:19], off
	v_lshl_add_u64 v[18:19], s[68:69], 0, v[146:147]
	s_mov_b32 m0, s47
	s_add_u32 s24, s8, s24
	global_load_lds_dwordx4 v[18:19], off
	v_lshl_add_u64 v[18:19], s[68:69], 0, v[148:149]
	s_mov_b32 m0, s48
	s_addc_u32 s25, s9, 0
	global_load_lds_dwordx4 v[18:19], off
	v_lshl_add_u64 v[18:19], s[24:25], 0, v[146:147]
	s_mov_b32 m0, s45
	s_nop 0
	global_load_lds_dwordx4 v[18:19], off
	v_lshl_add_u64 v[18:19], s[24:25], 0, v[148:149]
	s_mov_b32 m0, s46
	s_nop 0
	global_load_lds_dwordx4 v[18:19], off
	s_waitcnt vmcnt(8)
	s_waitcnt lgkmcnt(0)
	s_barrier
	s_waitcnt lgkmcnt(0)
	v_mfma_f32_16x16x128_f8f6f4 v[62:65], v[2:9], v[158:165], v[62:65]
	v_mfma_f32_16x16x128_f8f6f4 v[58:61], v[10:17], v[158:165], v[58:61]
	v_mfma_f32_16x16x128_f8f6f4 v[50:53], v[2:9], v[166:173], v[50:53]
	v_mfma_f32_16x16x128_f8f6f4 v[42:45], v[10:17], v[166:173], v[190:193]
	v_mfma_f32_16x16x128_f8f6f4 v[34:37], v[2:9], v[174:181], v[194:197]
	v_mfma_f32_16x16x128_f8f6f4 v[26:29], v[10:17], v[174:181], v[198:201]
	v_mfma_f32_16x16x128_f8f6f4 v[18:21], v[2:9], v[182:189], v[202:205]
	v_mfma_f32_16x16x128_f8f6f4 v[10:13], v[10:17], v[182:189], v[222:225]
	v_mfma_f32_16x16x128_f8f6f4 v[54:57], v[130:137], v[158:165], v[54:57]
	v_mfma_f32_16x16x128_f8f6f4 v[46:49], v[138:145], v[158:165], v[226:229]
	v_mfma_f32_16x16x128_f8f6f4 v[38:41], v[130:137], v[166:173], v[230:233]
	v_mfma_f32_16x16x128_f8f6f4 v[30:33], v[138:145], v[166:173], v[234:237]
	v_mfma_f32_16x16x128_f8f6f4 v[22:25], v[130:137], v[174:181], v[238:241]
	v_mfma_f32_16x16x128_f8f6f4 v[14:17], v[138:145], v[174:181], v[242:245]
	v_mfma_f32_16x16x128_f8f6f4 v[6:9], v[130:137], v[182:189], v[246:249]
	v_mfma_f32_16x16x128_f8f6f4 v[2:5], v[138:145], v[182:189], v[250:253]
	s_barrier
	s_add_i32 s66, s66, 2
	s_addk_i32 s67, 0x100
	s_cmp_gt_u32 s66, 5
	s_cbranch_scc0 .LBB0_2652
	s_and_b64 vcc, exec, s[12:13]
	s_cbranch_vccz .LBB0_2655
	s_barrier
